# same code as previous, phase starts and MFMA runs placed at 4 mod 8
# baseline (speedup 1.0000x reference)
.LBB0_167:
	s_or_b64 exec, exec, s[0:1]
	v_readlane_b32 s0, v242, 1
	v_mov_b32_e32 v28, v208
	v_readlane_b32 s1, v242, 2
	s_waitcnt lgkmcnt(0)
	s_barrier
	s_nop 0
	s_mov_b32 s4, 0
	s_load_dword s2, s[0:1], 0x110
	s_add_u32 s0, s0, 0x110
	s_addc_u32 s1, s1, 0
	v_writelane_b32 v242, s0, 9
	v_ashrrev_i32_e32 v1, 6, v28
	s_waitcnt lgkmcnt(0)
	s_lshl_b32 s71, s2, 3
	s_abs_i32 s6, s71
	v_cvt_f32_u32_e32 v0, s6
	v_writelane_b32 v242, s1, 10
	s_mov_b32 s0, s2
	v_writelane_b32 v242, s0, 11
	v_rcp_iflag_f32_e32 v0, v0
	s_ashr_i32 s2, s71, 31
	v_writelane_b32 v242, s1, 12
	s_add_i32 s0, s71, 0x87ff
	v_mul_f32_e32 v0, 0x4f7ffffe, v0
	v_cvt_u32_f32_e32 v0, v0
	s_ashr_i32 s1, s0, 31
	v_writelane_b32 v242, s2, 13
	s_xor_b32 s1, s1, s2
	s_sub_i32 s2, 0, s6
	v_readfirstlane_b32 s3, v0
	s_mul_i32 s2, s2, s3
	s_mul_hi_u32 s2, s3, s2
	s_abs_i32 s0, s0
	s_add_i32 s2, s3, s2
	v_writelane_b32 v242, s2, 14
	s_mul_hi_u32 s2, s0, s2
	s_mul_i32 s3, s2, s6
	s_sub_i32 s0, s0, s3
	s_add_i32 s3, s2, 1
	s_sub_i32 s5, s0, s6
	s_cmp_ge_u32 s0, s6
	s_cselect_b32 s2, s3, s2
	s_cselect_b32 s0, s5, s0
	s_add_i32 s3, s2, 1
	s_cmp_ge_u32 s0, s6
	s_cselect_b32 s0, s3, s2
	v_writelane_b32 v242, s6, 15
	s_xor_b32 s0, s0, s1
	s_sub_i32 s1, s0, s1
	v_readlane_b32 s0, v242, 0
	s_lshl_b32 s0, s0, 3
	s_nop 0
	v_add_u32_e32 v0, s0, v1
	v_mul_lo_u32 v88, s1, v0
	v_add_u32_e32 v0, s1, v88
	v_min_i32_e32 v90, 0x8800, v0
	v_writelane_b32 v242, s0, 16
	v_cmp_lt_i32_e32 vcc, v88, v90
	v_writelane_b32 v242, s1, 17
	s_and_saveexec_b64 s[0:1], vcc
	s_cbranch_execz .LBB0_174
	v_readlane_b32 s10, v242, 1
	v_readlane_b32 s11, v242, 2
	s_load_dwordx2 s[2:3], s[10:11], s4 offset:0x0
	s_load_dwordx2 s[8:9], s[10:11], s4 offset:0x10
	s_load_dwordx2 s[6:7], s[10:11], s4 offset:0x30
	s_nop 0
	s_load_dwordx2 s[10:11], s[10:11], s4 offset:0x108
	s_mov_b32 s14, 0x8000
	v_add_u32_e32 v16, 0xffff8000, v88
	v_ashrrev_i32_e32 v89, 31, v88
	v_cmp_gt_i32_e32 vcc, s14, v88
	s_waitcnt lgkmcnt(0)
	v_mov_b32_e32 v18, s9
	v_mov_b32_e32 v19, s3
	v_lshlrev_b32_e32 v0, 2, v28
	v_cndmask_b32_e32 v17, 0, v89, vcc
	v_cndmask_b32_e32 v16, v16, v88, vcc
	v_cndmask_b32_e32 v19, v18, v19, vcc
	v_mov_b32_e32 v18, s8
	v_mov_b32_e32 v20, s2
	v_and_b32_e32 v30, 0xfc, v0
	v_cndmask_b32_e32 v18, v18, v20, vcc
	v_lshlrev_b64 v[16:17], 12, v[16:17]
	v_mov_b32_e32 v81, 0
	v_lshlrev_b32_e32 v80, 2, v30
	v_lshl_add_u64 v[16:17], v[18:19], 0, v[16:17]
	v_lshl_add_u64 v[32:33], v[16:17], 0, v[80:81]
	global_load_dwordx4 v[0:3], v80, s[6:7]
	global_load_dwordx4 v[4:7], v80, s[6:7] offset:1024
	global_load_dwordx4 v[8:11], v80, s[6:7] offset:2048
	global_load_dwordx4 v[12:15], v80, s[6:7] offset:3072
	global_load_dwordx4 v[36:39], v[32:33], off
	global_load_dwordx4 v[24:27], v[32:33], off offset:1024
	global_load_dwordx4 v[20:23], v[32:33], off offset:2048
	global_load_dwordx4 v[16:19], v[32:33], off offset:3072
	v_lshl_add_u64 v[32:33], s[10:11], 0, v[80:81]
	s_mov_b64 s[4:5], 0x4000
	v_lshl_add_u64 v[82:83], v[32:33], 0, s[4:5]
	v_lshlrev_b64 v[32:33], 11, v[88:89]
	v_and_b32_e32 v28, 63, v28
	v_lshl_or_b32 v32, v28, 3, v32
	v_lshl_add_u64 v[28:29], s[10:11], 0, v[32:33]
	s_mov_b64 s[4:5], 0xdbff000
	v_lshl_add_u64 v[84:85], v[28:29], 0, s[4:5]
	v_mov_b32_e32 v93, -1
	s_mov_b64 s[10:11], 0
	s_movk_i32 s15, 0x7fff
	v_lshlrev_b32_e32 v80, 2, v30
	v_mov_b32_e32 v91, 0x358637bd
	s_mov_b32 s16, 0xf800000
	v_mov_b32_e32 v92, 0x260
	s_mov_b64 s[12:13], 0x800
	s_branch .LBB0_170

.LBB0_226:
	s_or_b64 exec, exec, s[0:1]
	v_readlane_b32 s0, v242, 1
	s_waitcnt lgkmcnt(0)
	s_barrier
	s_nop 0
	s_mov_b32 s2, 0
	v_readlane_b32 s1, v242, 2
	s_load_dwordx4 s[8:11], s[0:1], s2 offset:0xe8
	s_load_dwordx2 s[12:13], s[0:1], s2 offset:0xf8
	s_nop 0
	s_load_dwordx2 s[0:1], s[0:1], s2 offset:0x108
	v_readlane_b32 s2, v242, 0
	s_cmpk_lt_i32 s2, 0x6e8
	v_mov_b32_e32 v140, v208
	s_cselect_b64 s[4:5], -1, 0
	v_writelane_b32 v242, s4, 18
	s_cmpk_gt_i32 s2, 0x6e7
	v_readfirstlane_b32 s33, v140
	v_writelane_b32 v242, s5, 19
	s_cbranch_scc1 .LBB0_238
	v_lshlrev_b32_e32 v0, 4, v140
	v_add_u32_e32 v1, 0x2000, v0
	v_ashrrev_i32_e32 v2, 31, v1
	v_lshrrev_b32_e32 v2, 22, v2
	v_add_u32_e32 v2, v1, v2
	v_ashrrev_i32_e32 v2, 10, v2
	v_mul_i32_i24_e32 v3, 0x400, v2
	v_sub_u32_e32 v1, v1, v3
	v_lshrrev_b32_e32 v3, 4, v1
	v_bitop3_b32 v1, v3, v1, 32 bitop3:0x6c
	v_ashrrev_i32_e32 v3, 31, v1
	v_lshrrev_b32_e32 v3, 26, v3
	v_add_u32_e32 v3, v1, v3
	v_lshlrev_b32_e32 v5, 3, v2
	v_ashrrev_i32_e32 v4, 6, v3
	v_and_b32_e32 v5, -16, v5
	v_and_b32_e32 v3, 0xc0, v3
	v_add_u32_e32 v5, v4, v5
	v_sub_u32_e32 v1, v1, v3
	v_mov_b32_e32 v3, 1
	v_and_b32_e32 v4, 3, v4
	s_mov_b32 s2, 0x1fffe0
	v_lshrrev_b32_e32 v6, 2, v5
	v_lshlrev_b32_e32 v7, 1, v5
	v_lshlrev_b32_e32 v2, 5, v2
	v_ashrrev_i16_sdwa v1, v3, sext(v1) dst_sel:DWORD dst_unused:UNUSED_PAD src0_sel:DWORD src1_sel:BYTE_0
	v_and_or_b32 v4, v5, s2, v4
	v_and_b32_e32 v6, 4, v6
	v_and_b32_e32 v7, 24, v7
	v_and_b32_e32 v2, 32, v2
	v_bfe_i32 v1, v1, 0, 16
	v_or3_b32 v4, v4, v6, v7
	v_add_lshl_u32 v1, v2, v1, 1
	v_lshl_add_u32 v128, v4, 11, v1
	v_lshl_add_u32 v130, v5, 11, v1
	v_bfe_i32 v1, v140, 27, 1
	v_lshrrev_b32_e32 v1, 22, v1
	v_add_u32_e32 v1, v0, v1
	v_and_b32_e32 v1, 0xfffffc00, v1
	v_sub_u32_e32 v0, v0, v1
	v_lshrrev_b32_e32 v1, 4, v0
	v_ashrrev_i32_e32 v4, 31, v140
	v_bitop3_b32 v0, v1, v0, 32 bitop3:0x6c
	v_lshrrev_b32_e32 v4, 26, v4
	v_ashrrev_i32_e32 v1, 31, v0
	v_add_u32_e32 v4, v140, v4
	s_waitcnt lgkmcnt(0)
	s_add_u32 s38, s0, 0xfef000
	v_lshrrev_b32_e32 v1, 26, v1
	v_ashrrev_i32_e32 v4, 6, v4
	s_addc_u32 s39, s1, 0
	v_add_u32_e32 v1, v0, v1
	v_lshlrev_b32_e32 v5, 3, v4
	s_add_u32 s40, s0, 0xdbff000
	v_ashrrev_i32_e32 v2, 6, v1
	v_and_b32_e32 v5, -16, v5
	v_readlane_b32 s4, v242, 0
	s_addc_u32 s41, s1, 0
	v_add_u32_e32 v5, v2, v5
	v_and_b32_e32 v2, 3, v2
	s_ashr_i32 s42, s4, 31
	v_and_or_b32 v2, v5, s2, v2
	s_lshr_b32 s2, s42, 29
	s_add_i32 s2, s4, s2
	s_ashr_i32 s5, s33, 6
	s_ashr_i32 s3, s2, 3
	s_and_b32 s2, s2, -8
	s_ashr_i32 s6, s33, 8
	s_lshl_b32 s7, s5, 10
	s_sub_i32 s2, s4, s2
	s_cmp_lt_i32 s2, 0
	s_movk_i32 s43, 0xde
	s_cselect_b32 s4, s43, 0xdd
	s_mul_i32 s2, s4, s2
	s_add_i32 s2, s2, s3
	s_mul_hi_i32 s3, s2, 0x4ec4ec4f
	s_lshr_b32 s4, s3, 31
	s_ashr_i32 s3, s3, 5
	s_add_i32 s3, s3, s4
	s_lshl_b32 s14, s3, 3
	s_mulk_i32 s3, 0x68
	s_sub_i32 s2, s2, s3
	s_bfe_i32 s3, s2, 0x80000
	s_bfe_u32 s3, s3, 0x3000c
	s_add_i32 s3, s2, s3
	s_bfe_i32 s4, s3, 0x80000
	s_and_b32 s3, s3, 0xf8
	s_sub_i32 s2, s2, s3
	s_sext_i32_i16 s4, s4
	s_sext_i32_i8 s2, s2
	s_lshr_b32 s4, s4, 3
	s_add_i32 s14, s14, s2
	v_and_b32_e32 v1, 0xc0, v1
	s_ashr_i32 s15, s14, 31
	s_bfe_i64 s[16:17], s[4:5], 0x100000
	v_sub_u32_e32 v0, v0, v1
	s_lshl_b64 s[2:3], s[14:15], 19
	s_lshl_b64 s[16:17], s[16:17], 19
	v_lshrrev_b32_e32 v6, 2, v5
	v_lshlrev_b32_e32 v7, 1, v5
	v_lshlrev_b32_e32 v4, 5, v4
	v_ashrrev_i16_sdwa v0, v3, sext(v0) dst_sel:DWORD dst_unused:UNUSED_PAD src0_sel:DWORD src1_sel:BYTE_0
	s_add_u32 s16, s38, s16
	v_and_b32_e32 v6, 4, v6
	v_and_b32_e32 v7, 24, v7
	v_and_b32_e32 v4, 32, v4
	v_bfe_i32 v0, v0, 0, 16
	s_addc_u32 s17, s39, s17
	s_add_i32 s15, s7, 0
	v_or3_b32 v2, v2, v6, v7
	v_add_lshl_u32 v0, v4, v0, 1
	s_add_i32 s44, s15, 0x10000
	v_lshl_add_u32 v132, v2, 11, v0
	v_lshl_add_u32 v134, v5, 11, v0
	v_mov_b32_e32 v0, 0x7f
	s_mov_b64 s[18:19], s[16:17]
	s_mov_b32 m0, s44
	s_add_i32 s45, s15, 0x12000
	v_mov_b32_e32 v133, 0
	global_load_lds_dwordx4 v132, s[18:19]
	s_mov_b32 m0, s45
	s_mov_b32 s51, 0
	global_load_lds_dwordx4 v128, s[18:19]
	s_add_u32 s18, s40, s2
	s_addc_u32 s19, s41, s3
	s_mov_b64 s[2:3], s[18:19]
	s_mov_b32 m0, s15
	s_add_i32 s46, s15, 0x2000
	v_mov_b32_e32 v129, v133
	global_load_lds_dwordx4 v134, s[2:3]
	s_mov_b32 m0, s46
	v_mov_b32_e32 v135, v133
	global_load_lds_dwordx4 v130, s[2:3]
	s_add_u32 s2, s16, 0x40000
	s_addc_u32 s3, s17, 0
	s_add_i32 s47, s15, 0x14000
	s_mov_b32 m0, s47
	s_add_i32 s48, s15, 0x16000
	v_mov_b32_e32 v131, v133
	global_load_lds_dwordx4 v132, s[2:3]
	s_mov_b32 m0, s48
	s_nop 0
	global_load_lds_dwordx4 v128, s[2:3]
	s_add_u32 s2, s18, 0x40000
	s_addc_u32 s3, s19, 0
	s_add_i32 s49, s15, 0x4000
	s_mov_b32 m0, s49
	s_add_i32 s50, s15, 0x6000
	s_cmp_lg_u32 s6, 1
	global_load_lds_dwordx4 v134, s[2:3]
	s_mov_b32 m0, s50
	s_nop 0
	global_load_lds_dwordx4 v130, s[2:3]
	s_cbranch_scc1 .LBB0_229
	s_barrier

.LBB0_315:
	s_or_b64 exec, exec, s[0:1]
	v_readlane_b32 s0, v242, 0
	s_and_b32 s31, s0, 3
	v_mov_b32_e32 v24, v208
	s_lshl_b32 s1, s31, 6
	s_waitcnt lgkmcnt(0)
	s_barrier
	s_nop 0
	s_mov_b32 s2, 0
	s_cmpk_lt_i32 s0, 0x880
	v_lshrrev_b32_e32 v0, 4, v24
	v_ashrrev_i32_e32 v22, 8, v24
	v_bfe_u32 v1, v0, 1, 1
	s_cselect_b64 s[10:11], -1, 0
	s_cmpk_gt_i32 s0, 0x87f
	v_cmp_eq_u32_e32 vcc, v1, v22
	s_cselect_b64 s[72:73], -1, 0
	s_mov_b32 s3, 0
	v_cndmask_b32_e64 v7, 0, -1, vcc
	s_and_b64 vcc, exec, s[72:73]
	v_writelane_b32 v242, s1, 20
	s_cbranch_vccnz .LBB0_336
	v_readlane_b32 s0, v242, 1
	v_readlane_b32 s1, v242, 2
	s_load_dwordx4 s[4:7], s[0:1], s2 offset:0x60
	s_nop 0
	s_load_dwordx2 s[0:1], s[0:1], s2 offset:0x108
	v_lshrrev_b32_e32 v28, 2, v24
	v_and_b32_e32 v86, 15, v24
	v_and_b32_e32 v20, 48, v28
	v_readlane_b32 s8, v242, 20
	v_ashrrev_i32_e32 v23, 31, v22
	v_lshlrev_b64 v[2:3], 14, v[22:23]
	v_or3_b32 v1, v86, s8, v20
	v_lshlrev_b32_e32 v0, 13, v0
	s_waitcnt lgkmcnt(0)
	v_lshl_add_u64 v[2:3], s[4:5], 0, v[2:3]
	v_lshlrev_b32_e32 v12, 2, v1
	v_mov_b32_e32 v13, 0
	v_and_b32_e32 v0, 0x2000, v0
	v_lshl_add_u64 v[2:3], v[2:3], 0, v[12:13]
	v_mov_b32_e32 v1, v13
	v_lshl_add_u64 v[0:1], v[2:3], 0, v[0:1]
	s_movk_i32 s2, 0x1000
	v_add_co_u32_e32 v2, vcc, s2, v0
	s_lshl_b32 s2, s8, 2
	s_nop 0
	v_addc_co_u32_e32 v3, vcc, 0, v1, vcc
	global_load_dword v4, v[0:1], off
	global_load_dword v6, v[0:1], off offset:1024
	global_load_dword v5, v[0:1], off offset:2048
	global_load_dword v8, v[0:1], off offset:3072
	global_load_dword v9, v[2:3], off
	global_load_dword v10, v[2:3], off offset:1024
	global_load_dword v26, v[2:3], off offset:2048
	global_load_dword v27, v[2:3], off offset:3072
	v_lshlrev_b64 v[0:1], 10, v[22:23]
	v_lshl_add_u64 v[0:1], s[6:7], 0, v[0:1]
	v_bfe_u32 v25, v24, 4, 2
	v_lshl_add_u64 v[0:1], v[0:1], 0, s[2:3]
	v_lshlrev_b32_e32 v12, 2, v20
	v_lshl_add_u64 v[0:1], v[0:1], 0, v[12:13]
	v_lshlrev_b32_e32 v12, 4, v25
	v_lshl_add_u64 v[0:1], v[0:1], 0, v[12:13]
	global_load_dwordx4 v[0:3], v[0:1], off
	v_readlane_b32 s2, v242, 0
	s_ashr_i32 s2, s2, 2
	s_mul_hi_i32 s3, s2, 0x78787879
	s_lshr_b32 s4, s3, 31
	s_ashr_i32 s5, s3, 5
	s_add_i32 s5, s5, s4
	s_mul_i32 s3, s5, 0x44
	s_sub_i32 s2, s2, s3
	s_lshl_b32 s6, s2, 6
	s_cmp_gt_i32 s2, 3
	v_lshlrev_b32_e32 v30, 2, v25
	s_cbranch_scc0 .LBB0_318
	s_lshl_b32 s2, s5, 12
	s_add_i32 s2, s6, s2
	s_add_i32 s4, s2, 0xffffff00
	s_cbranch_execz .LBB0_319
	s_branch .LBB0_320

.LBB0_449:
	v_writelane_b32 v242, s31, 21
	s_or_b64 exec, exec, s[0:1]
	v_readlane_b32 s6, v242, 1
	s_waitcnt lgkmcnt(0)
	s_barrier
	s_nop 0
	s_mov_b32 s4, 0
	v_readlane_b32 s7, v242, 2
	s_load_dwordx2 s[0:1], s[6:7], s4 offset:0x108
	s_load_dwordx2 s[2:3], s[6:7], s4 offset:0x70
	s_load_dwordx8 s[52:59], s[6:7], s4 offset:0x50
	v_mov_b32_e32 v40, v208
	v_readlane_b32 s5, v242, 20
	v_ashrrev_i32_e32 v34, 8, v40
	v_lshrrev_b32_e32 v39, 2, v40
	v_lshrrev_b32_e32 v0, 4, v40
	v_and_b32_e32 v112, 15, v40
	v_and_b32_e32 v38, 48, v39
	v_ashrrev_i32_e32 v35, 31, v34
	s_waitcnt lgkmcnt(0)
	s_add_u32 s50, s0, 0x11fff000
	v_bfe_u32 v0, v0, 1, 1
	v_or3_b32 v1, v112, s5, v38
	v_lshlrev_b64 v[2:3], 14, v[34:35]
	s_addc_u32 s51, s1, 0
	v_cmp_eq_u32_e32 vcc, v0, v34
	v_lshlrev_b32_e32 v0, 9, v40
	v_lshl_add_u64 v[2:3], s[56:57], 0, v[2:3]
	v_lshlrev_b32_e32 v32, 2, v1
	v_mov_b32_e32 v33, 0
	s_add_u32 s61, s0, 0x284ff000
	v_and_b32_e32 v0, 0x2000, v0
	v_lshl_add_u64 v[2:3], v[2:3], 0, v[32:33]
	v_mov_b32_e32 v1, v33
	s_addc_u32 s64, s1, 0
	v_lshl_add_u64 v[0:1], v[2:3], 0, v[0:1]
	s_movk_i32 s4, 0x1000
	s_lshl_b32 s6, s5, 2
	s_waitcnt vmcnt(5)
	v_cndmask_b32_e64 v11, 0, -1, vcc
	v_add_co_u32_e32 v2, vcc, s4, v0
	s_mov_b32 s4, s6
	v_writelane_b32 v242, s4, 22
	v_addc_co_u32_e32 v3, vcc, 0, v1, vcc
	s_nop 0
	v_writelane_b32 v242, s5, 23
	global_load_dword v9, v[0:1], off
	global_load_dword v44, v[0:1], off offset:1024
	global_load_dword v10, v[0:1], off offset:2048
	global_load_dword v45, v[0:1], off offset:3072
	global_load_dword v46, v[2:3], off
	global_load_dword v48, v[2:3], off offset:1024
	global_load_dword v47, v[2:3], off offset:2048
	global_load_dword v49, v[2:3], off offset:3072
	v_readlane_b32 s4, v242, 21
	v_lshlrev_b64 v[0:1], 10, v[34:35]
	s_lshl_b32 s5, s4, 7
	s_lshl_b32 s4, s4, 9
	s_mov_b32 s7, 0
	v_lshl_add_u64 v[0:1], s[58:59], 0, v[0:1]
	s_add_u32 s2, s2, s4
	v_bfe_u32 v8, v40, 4, 2
	v_lshl_add_u64 v[0:1], v[0:1], 0, s[6:7]
	v_lshlrev_b32_e32 v32, 2, v38
	v_lshlrev_b32_e32 v36, 6, v34
	s_addc_u32 s3, s3, 0
	v_lshlrev_b32_e32 v4, 2, v112
	v_mov_b32_e32 v5, v33
	v_lshl_add_u64 v[0:1], v[0:1], 0, v[32:33]
	v_lshlrev_b32_e32 v32, 4, v8
	v_lshl_add_u64 v[4:5], s[2:3], 0, v[4:5]
	v_ashrrev_i32_e32 v37, 31, v36
	v_lshl_add_u64 v[0:1], v[0:1], 0, v[32:33]
	v_lshl_add_u64 v[4:5], v[36:37], 2, v[4:5]
	global_load_dwordx4 v[0:3], v[0:1], off
	s_nop 0
	global_load_dword v113, v[4:5], off
	global_load_dword v114, v[4:5], off offset:64
	global_load_dword v115, v[4:5], off offset:128
	global_load_dword v116, v[4:5], off offset:192
	v_cndmask_b32_e64 v4, 0, 1, s[10:11]
	v_writelane_b32 v242, s5, 24
	v_cmp_ne_u32_e64 s[2:3], 1, v4
	s_andn2_b64 vcc, exec, s[10:11]
	s_nop 0
	v_writelane_b32 v242, s2, 25
	s_nop 1
	v_writelane_b32 v242, s3, 26
	s_cbranch_vccnz .LBB0_452
	v_readlane_b32 s2, v242, 0
	s_ashr_i32 s2, s2, 2
	s_mul_hi_i32 s3, s2, 0x78787879
	s_lshr_b32 s4, s3, 31
	s_ashr_i32 s5, s3, 5
	s_add_i32 s5, s5, s4
	s_mul_i32 s3, s5, 0x44
	s_sub_i32 s4, s2, s3
	s_lshl_b32 s7, s4, 6
	s_cmp_gt_i32 s4, 3
	s_cbranch_scc0 .LBB0_453
	s_lshl_b32 s2, s5, 12
	s_add_i32 s2, s7, s2
	s_add_i32 s6, s2, 0xffffff00
	s_cbranch_execz .LBB0_454
	s_branch .LBB0_455

.LBB0_1120:
	s_or_b64 exec, exec, s[0:1]
	s_waitcnt lgkmcnt(0)
	v_mov_b32_e32 v0, v208
	s_barrier
	s_nop 0
	s_mov_b32 s2, 0
	v_readlane_b32 s0, v242, 16
	v_ashrrev_i32_e32 v1, 6, v0
	s_nop 0
	v_add_u32_e32 v1, s0, v1
	v_readlane_b32 s0, v242, 17
	s_nop 1
	v_mul_lo_u32 v84, v1, s0
	v_add_u32_e32 v1, s0, v84
	v_min_i32_e32 v114, 0x8800, v1
	v_cmp_lt_i32_e32 vcc, v84, v114
	s_and_saveexec_b64 s[0:1], vcc
	s_cbranch_execz .LBB0_1145
	v_readlane_b32 s4, v242, 1
	v_readlane_b32 s5, v242, 2
	s_load_dwordx2 s[6:7], s[4:5], s2 offset:0x108
	s_nop 0
	s_load_dwordx2 s[2:3], s[4:5], s2 offset:0x30
	v_lshlrev_b32_e32 v1, 2, v0
	v_mov_b32_e32 v83, 0
	v_and_b32_e32 v82, 0xfc, v1
	v_lshlrev_b32_e32 v2, 2, v82
	v_mov_b32_e32 v3, v83
	s_waitcnt lgkmcnt(0)
	v_lshl_add_u64 v[2:3], s[2:3], 0, v[2:3]
	s_mov_b64 s[2:3], 0x1000
	s_add_u32 s10, s6, 0xdcf000
	v_lshl_add_u64 v[4:5], v[2:3], 0, s[2:3]
	s_movk_i32 s2, 0x1000
	s_addc_u32 s11, s7, 0
	v_add_co_u32_e32 v2, vcc, s2, v2
	s_add_u32 s14, s6, 0x37ff000
	s_nop 0
	v_addc_co_u32_e32 v3, vcc, 0, v3, vcc
	v_ashrrev_i32_e32 v85, 31, v84
	s_addc_u32 s15, s7, 0
	global_load_dwordx4 v[18:21], v[4:5], off offset:1024
	global_load_dwordx4 v[22:25], v[4:5], off offset:2048
	global_load_dwordx4 v[26:29], v[2:3], off
	global_load_dwordx4 v[30:33], v[4:5], off offset:3072
	v_lshlrev_b64 v[2:3], 11, v[84:85]
	v_lshl_add_u64 v[2:3], s[14:15], 0, v[2:3]
	v_lshlrev_b32_e32 v4, 1, v82
	v_mov_b32_e32 v5, v83
	v_lshl_add_u64 v[2:3], v[2:3], 0, v[4:5]
	global_load_dwordx2 v[112:113], v[2:3], off
	global_load_dwordx2 v[110:111], v[2:3], off offset:512
	global_load_dwordx2 v[108:109], v[2:3], off offset:1024
	global_load_dwordx2 v[104:105], v[2:3], off offset:1536
	v_and_b32_e32 v2, 15, v0
	v_lshlrev_b64 v[0:1], 6, v[84:85]
	v_lshl_add_u64 v[0:1], s[10:11], 0, v[0:1]
	v_lshlrev_b32_e32 v2, 2, v2
	v_mov_b32_e32 v3, v83
	v_lshl_add_u64 v[0:1], v[0:1], 0, v[2:3]
	global_load_dword v126, v[0:1], off
	v_add_u32_e32 v0, 1, v84
	v_cmp_lt_i32_e32 vcc, v0, v114
	v_mov_b32_e32 v116, -1
	v_mov_b32_e32 v115, -1
	s_and_saveexec_b64 s[2:3], vcc
	s_cbranch_execz .LBB0_1123
	v_ashrrev_i32_e32 v1, 31, v0
	v_lshlrev_b64 v[0:1], 6, v[0:1]
	v_lshl_add_u64 v[0:1], s[10:11], 0, v[0:1]
	v_lshl_add_u64 v[0:1], v[0:1], 0, v[2:3]
	global_load_dword v115, v[0:1], off

.LBB0_1204:
	s_add_u32 s30, s28, 0x100
	ds_read_b128 v[158:161], v141
	ds_read_b128 v[162:165], v142
	ds_read_b128 v[166:169], v149
	ds_read_b128 v[170:173], v150
	s_addc_u32 s31, s29, 0
	s_and_b32 s61, s30, 0x700
	s_add_u32 s62, s16, s61
	s_addc_u32 s63, s17, 0
	s_cmp_eq_u32 s60, 12
	s_cselect_b64 s[36:37], -1, 0
	s_and_b64 s[34:35], s[36:37], exec
	s_cselect_b32 s35, s19, s63
	s_cselect_b32 s34, s21, s62
	s_cselect_b32 s62, 0, 0
	s_cselect_b32 s61, 0, s61
	s_add_u32 s28, s22, s28
	s_addc_u32 s29, s23, s29
	s_add_u32 s28, s28, 0x40080
	s_addc_u32 s29, s29, 0
	ds_read_b128 v[174:177], v157
	ds_read_b128 v[178:181], v157 offset:1024
	ds_read_b128 v[182:185], v157 offset:2048
	ds_read_b128 v[186:189], v157 offset:3072
	ds_read_b128 v[190:193], v157 offset:4096
	ds_read_b128 v[194:197], v157 offset:5120
	ds_read_b128 v[198:201], v157 offset:6144
	ds_read_b128 v[202:205], v157 offset:7168
	s_add_i32 m0, s3, 0xc000
	s_nop 0
	global_load_lds_dwordx4 v134, s[28:29]
	s_add_i32 m0, s3, 0xe000
	s_nop 0
	global_load_lds_dwordx4 v130, s[28:29]
	s_waitcnt lgkmcnt(8)
	s_nop 0
	s_barrier
	s_waitcnt lgkmcnt(0)
	s_setprio 1
	s_waitcnt lgkmcnt(0)
	v_mfma_f32_16x16x32_bf16 v[124:127], v[158:161], v[174:177], v[124:127]
	v_mfma_f32_16x16x32_bf16 v[120:123], v[166:169], v[174:177], v[120:123]
	v_mfma_f32_16x16x32_bf16 v[116:119], v[158:161], v[182:185], v[116:119]
	v_mfma_f32_16x16x32_bf16 v[108:111], v[166:169], v[182:185], v[108:111]
	v_mfma_f32_16x16x32_bf16 v[100:103], v[158:161], v[190:193], v[100:103]
	v_mfma_f32_16x16x32_bf16 v[92:95], v[166:169], v[190:193], v[92:95]
	v_mfma_f32_16x16x32_bf16 v[84:87], v[158:161], v[198:201], v[84:87]
	v_mfma_f32_16x16x32_bf16 v[76:79], v[166:169], v[198:201], v[76:79]
	v_mfma_f32_16x16x32_bf16 v[124:127], v[162:165], v[178:181], v[124:127]
	v_mfma_f32_16x16x32_bf16 v[120:123], v[170:173], v[178:181], v[120:123]
	v_mfma_f32_16x16x32_bf16 v[116:119], v[162:165], v[186:189], v[116:119]
	v_mfma_f32_16x16x32_bf16 v[108:111], v[170:173], v[186:189], v[108:111]
	v_mfma_f32_16x16x32_bf16 v[100:103], v[162:165], v[194:197], v[100:103]
	v_mfma_f32_16x16x32_bf16 v[92:95], v[170:173], v[194:197], v[92:95]
	v_mfma_f32_16x16x32_bf16 v[84:87], v[162:165], v[202:205], v[84:87]
	v_mfma_f32_16x16x32_bf16 v[76:79], v[170:173], v[202:205], v[76:79]
	s_setprio 0
	s_barrier
	s_mov_b64 s[28:29], s[34:35]
	s_mov_b32 m0, s44
	ds_read_b128 v[210:213], v143
	ds_read_b128 v[214:217], v144
	ds_read_b128 v[218:221], v151
	ds_read_b128 v[222:225], v152
	s_nop 0
	global_load_lds_dwordx4 v132, s[28:29]
	s_mov_b32 m0, s45
	s_nop 0
	global_load_lds_dwordx4 v128, s[28:29]
	s_nop 0
	s_barrier
	s_waitcnt lgkmcnt(0)
	s_setprio 1
	s_waitcnt lgkmcnt(0)
	v_mfma_f32_16x16x32_bf16 v[112:115], v[210:213], v[174:177], v[112:115]
	v_mfma_f32_16x16x32_bf16 v[104:107], v[218:221], v[174:177], v[104:107]
	v_mfma_f32_16x16x32_bf16 v[96:99], v[210:213], v[182:185], v[96:99]
	v_mfma_f32_16x16x32_bf16 v[88:91], v[218:221], v[182:185], v[88:91]
	v_mfma_f32_16x16x32_bf16 v[80:83], v[210:213], v[190:193], v[80:83]
	v_mfma_f32_16x16x32_bf16 v[72:75], v[218:221], v[190:193], v[72:75]
	v_mfma_f32_16x16x32_bf16 v[68:71], v[210:213], v[198:201], v[68:71]
	v_mfma_f32_16x16x32_bf16 v[64:67], v[218:221], v[198:201], v[64:67]
	v_mfma_f32_16x16x32_bf16 v[112:115], v[214:217], v[178:181], v[112:115]
	v_mfma_f32_16x16x32_bf16 v[104:107], v[222:225], v[178:181], v[104:107]
	v_mfma_f32_16x16x32_bf16 v[96:99], v[214:217], v[186:189], v[96:99]
	v_mfma_f32_16x16x32_bf16 v[88:91], v[222:225], v[186:189], v[88:91]
	v_mfma_f32_16x16x32_bf16 v[80:83], v[214:217], v[194:197], v[80:83]
	v_mfma_f32_16x16x32_bf16 v[72:75], v[222:225], v[194:197], v[72:75]
	v_mfma_f32_16x16x32_bf16 v[68:71], v[214:217], v[202:205], v[68:71]
	v_mfma_f32_16x16x32_bf16 v[64:67], v[222:225], v[202:205], v[64:67]
	s_setprio 0
	s_and_b64 s[28:29], s[12:13], s[36:37]
	s_and_b64 s[28:29], s[28:29], exec
	s_cselect_b32 s28, s24, s22
	s_cselect_b32 s29, s25, s23
	s_add_u32 s28, s28, s61
	s_addc_u32 s29, s29, s62
	s_mov_b64 s[36:37], s[28:29]
	s_mov_b32 m0, s3
	s_barrier
	ds_read_b128 v[174:177], v157 offset:16384
	ds_read_b128 v[178:181], v157 offset:17408
	ds_read_b128 v[182:185], v157 offset:18432
	ds_read_b128 v[186:189], v157 offset:19456
	ds_read_b128 v[190:193], v157 offset:20480
	ds_read_b128 v[194:197], v157 offset:21504
	ds_read_b128 v[198:201], v157 offset:22528
	ds_read_b128 v[202:205], v157 offset:23552
	s_nop 0
	global_load_lds_dwordx4 v134, s[36:37]
	s_mov_b32 m0, s46
	s_nop 0
	global_load_lds_dwordx4 v130, s[36:37]
	s_nop 0
	s_barrier
	s_waitcnt lgkmcnt(0)
	s_setprio 1
	s_waitcnt lgkmcnt(0)
	v_mfma_f32_16x16x32_bf16 v[60:63], v[158:161], v[174:177], v[60:63]
	v_mfma_f32_16x16x32_bf16 v[56:59], v[166:169], v[174:177], v[56:59]
	v_mfma_f32_16x16x32_bf16 v[52:55], v[158:161], v[182:185], v[52:55]
	v_mfma_f32_16x16x32_bf16 v[48:51], v[166:169], v[182:185], v[48:51]
	v_mfma_f32_16x16x32_bf16 v[36:39], v[158:161], v[190:193], v[36:39]
	v_mfma_f32_16x16x32_bf16 v[32:35], v[166:169], v[190:193], v[32:35]
	v_mfma_f32_16x16x32_bf16 v[20:23], v[158:161], v[198:201], v[20:23]
	v_mfma_f32_16x16x32_bf16 v[16:19], v[166:169], v[198:201], v[16:19]
	v_mfma_f32_16x16x32_bf16 v[60:63], v[162:165], v[178:181], v[60:63]
	v_mfma_f32_16x16x32_bf16 v[56:59], v[170:173], v[178:181], v[56:59]
	v_mfma_f32_16x16x32_bf16 v[52:55], v[162:165], v[186:189], v[52:55]
	v_mfma_f32_16x16x32_bf16 v[48:51], v[170:173], v[186:189], v[48:51]
	v_mfma_f32_16x16x32_bf16 v[36:39], v[162:165], v[194:197], v[36:39]
	v_mfma_f32_16x16x32_bf16 v[32:35], v[170:173], v[194:197], v[32:35]
	v_mfma_f32_16x16x32_bf16 v[20:23], v[162:165], v[202:205], v[20:23]
	v_mfma_f32_16x16x32_bf16 v[16:19], v[170:173], v[202:205], v[16:19]
	s_setprio 0
	s_barrier
	s_add_u32 s36, s34, 0x40000
	s_addc_u32 s37, s35, 0
	s_mov_b32 m0, s47
	s_nop 0
	global_load_lds_dwordx4 v132, s[36:37]
	s_mov_b32 m0, s48
	s_nop 0
	global_load_lds_dwordx4 v128, s[36:37]
	s_waitcnt vmcnt(6)
	s_barrier
	s_setprio 1
	v_mfma_f32_16x16x32_bf16 v[44:47], v[210:213], v[174:177], v[44:47]
	v_mfma_f32_16x16x32_bf16 v[40:43], v[218:221], v[174:177], v[40:43]
	v_mfma_f32_16x16x32_bf16 v[28:31], v[210:213], v[182:185], v[28:31]
	v_mfma_f32_16x16x32_bf16 v[24:27], v[218:221], v[182:185], v[24:27]
	v_mfma_f32_16x16x32_bf16 v[12:15], v[210:213], v[190:193], v[12:15]
	v_mfma_f32_16x16x32_bf16 v[8:11], v[218:221], v[190:193], v[8:11]
	v_mfma_f32_16x16x32_bf16 v[4:7], v[210:213], v[198:201], v[4:7]
	v_mfma_f32_16x16x32_bf16 v[0:3], v[218:221], v[198:201], v[0:3]
	v_mfma_f32_16x16x32_bf16 v[44:47], v[214:217], v[178:181], v[44:47]
	v_mfma_f32_16x16x32_bf16 v[40:43], v[222:225], v[178:181], v[40:43]
	v_mfma_f32_16x16x32_bf16 v[28:31], v[214:217], v[186:189], v[28:31]
	v_mfma_f32_16x16x32_bf16 v[24:27], v[222:225], v[186:189], v[24:27]
	v_mfma_f32_16x16x32_bf16 v[12:15], v[214:217], v[194:197], v[12:15]
	v_mfma_f32_16x16x32_bf16 v[8:11], v[222:225], v[194:197], v[8:11]
	v_mfma_f32_16x16x32_bf16 v[4:7], v[214:217], v[202:205], v[4:7]
	v_mfma_f32_16x16x32_bf16 v[0:3], v[222:225], v[202:205], v[0:3]
	s_setprio 0
	s_barrier
	ds_read_b128 v[158:161], v145
	ds_read_b128 v[162:165], v146
	ds_read_b128 v[166:169], v153
	ds_read_b128 v[170:173], v154
	s_add_u32 s36, s28, 0x40000
	s_addc_u32 s37, s29, 0
	s_mov_b32 m0, s49
	ds_read_b128 v[174:177], v157 offset:32768
	ds_read_b128 v[178:181], v157 offset:33792
	ds_read_b128 v[182:185], v157 offset:34816
	ds_read_b128 v[186:189], v157 offset:35840
	ds_read_b128 v[190:193], v157 offset:36864
	ds_read_b128 v[194:197], v157 offset:37888
	ds_read_b128 v[198:201], v157 offset:38912
	ds_read_b128 v[202:205], v157 offset:39936
	s_nop 0
	global_load_lds_dwordx4 v134, s[36:37]
	s_mov_b32 m0, s50
	s_nop 0
	global_load_lds_dwordx4 v130, s[36:37]
	s_waitcnt lgkmcnt(8)
	s_barrier
	s_waitcnt lgkmcnt(0)
	s_setprio 1
	s_waitcnt lgkmcnt(0)
	v_mfma_f32_16x16x32_bf16 v[124:127], v[158:161], v[174:177], v[124:127]
	v_mfma_f32_16x16x32_bf16 v[120:123], v[166:169], v[174:177], v[120:123]
	v_mfma_f32_16x16x32_bf16 v[116:119], v[158:161], v[182:185], v[116:119]
	v_mfma_f32_16x16x32_bf16 v[108:111], v[166:169], v[182:185], v[108:111]
	v_mfma_f32_16x16x32_bf16 v[100:103], v[158:161], v[190:193], v[100:103]
	v_mfma_f32_16x16x32_bf16 v[92:95], v[166:169], v[190:193], v[92:95]
	v_mfma_f32_16x16x32_bf16 v[84:87], v[158:161], v[198:201], v[84:87]
	v_mfma_f32_16x16x32_bf16 v[76:79], v[166:169], v[198:201], v[76:79]
	v_mfma_f32_16x16x32_bf16 v[124:127], v[162:165], v[178:181], v[124:127]
	v_mfma_f32_16x16x32_bf16 v[120:123], v[170:173], v[178:181], v[120:123]
	v_mfma_f32_16x16x32_bf16 v[116:119], v[162:165], v[186:189], v[116:119]
	v_mfma_f32_16x16x32_bf16 v[108:111], v[170:173], v[186:189], v[108:111]
	v_mfma_f32_16x16x32_bf16 v[100:103], v[162:165], v[194:197], v[100:103]
	v_mfma_f32_16x16x32_bf16 v[92:95], v[170:173], v[194:197], v[92:95]
	v_mfma_f32_16x16x32_bf16 v[84:87], v[162:165], v[202:205], v[84:87]
	v_mfma_f32_16x16x32_bf16 v[76:79], v[170:173], v[202:205], v[76:79]
	s_setprio 0
	s_barrier
	s_add_u32 s36, s34, 0x80
	s_addc_u32 s37, s35, 0
	s_mov_b32 m0, s52
	ds_read_b128 v[210:213], v147
	ds_read_b128 v[214:217], v148
	ds_read_b128 v[218:221], v155
	ds_read_b128 v[222:225], v156
	s_nop 0
	global_load_lds_dwordx4 v132, s[36:37]
	s_mov_b32 m0, s53
	s_nop 0
	global_load_lds_dwordx4 v128, s[36:37]
	s_nop 0
	s_barrier
	s_waitcnt lgkmcnt(0)
	s_setprio 1
	s_waitcnt lgkmcnt(0)
	v_mfma_f32_16x16x32_bf16 v[112:115], v[210:213], v[174:177], v[112:115]
	v_mfma_f32_16x16x32_bf16 v[104:107], v[218:221], v[174:177], v[104:107]
	v_mfma_f32_16x16x32_bf16 v[96:99], v[210:213], v[182:185], v[96:99]
	v_mfma_f32_16x16x32_bf16 v[88:91], v[218:221], v[182:185], v[88:91]
	v_mfma_f32_16x16x32_bf16 v[80:83], v[210:213], v[190:193], v[80:83]
	v_mfma_f32_16x16x32_bf16 v[72:75], v[218:221], v[190:193], v[72:75]
	v_mfma_f32_16x16x32_bf16 v[68:71], v[210:213], v[198:201], v[68:71]
	v_mfma_f32_16x16x32_bf16 v[64:67], v[218:221], v[198:201], v[64:67]
	v_mfma_f32_16x16x32_bf16 v[112:115], v[214:217], v[178:181], v[112:115]
	v_mfma_f32_16x16x32_bf16 v[104:107], v[222:225], v[178:181], v[104:107]
	v_mfma_f32_16x16x32_bf16 v[96:99], v[214:217], v[186:189], v[96:99]
	v_mfma_f32_16x16x32_bf16 v[88:91], v[222:225], v[186:189], v[88:91]
	v_mfma_f32_16x16x32_bf16 v[80:83], v[214:217], v[194:197], v[80:83]
	v_mfma_f32_16x16x32_bf16 v[72:75], v[222:225], v[194:197], v[72:75]
	v_mfma_f32_16x16x32_bf16 v[68:71], v[214:217], v[202:205], v[68:71]
	v_mfma_f32_16x16x32_bf16 v[64:67], v[222:225], v[202:205], v[64:67]
	s_setprio 0
	s_add_u32 s28, s28, 0x80
	s_addc_u32 s29, s29, 0
	s_mov_b32 m0, s54
	s_barrier
	ds_read_b128 v[174:177], v157 offset:49152
	ds_read_b128 v[178:181], v157 offset:50176
	ds_read_b128 v[182:185], v157 offset:51200
	ds_read_b128 v[186:189], v157 offset:52224
	ds_read_b128 v[190:193], v157 offset:53248
	ds_read_b128 v[194:197], v157 offset:54272
	ds_read_b128 v[198:201], v157 offset:55296
	ds_read_b128 v[202:205], v157 offset:56320
	s_nop 0
	global_load_lds_dwordx4 v134, s[28:29]
	s_mov_b32 m0, s55
	s_nop 0
	global_load_lds_dwordx4 v130, s[28:29]
	s_nop 0
	s_barrier
	s_waitcnt lgkmcnt(0)
	s_setprio 1
	s_waitcnt lgkmcnt(0)
	v_mfma_f32_16x16x32_bf16 v[60:63], v[158:161], v[174:177], v[60:63]
	v_mfma_f32_16x16x32_bf16 v[56:59], v[166:169], v[174:177], v[56:59]
	v_mfma_f32_16x16x32_bf16 v[52:55], v[158:161], v[182:185], v[52:55]
	v_mfma_f32_16x16x32_bf16 v[48:51], v[166:169], v[182:185], v[48:51]
	v_mfma_f32_16x16x32_bf16 v[36:39], v[158:161], v[190:193], v[36:39]
	v_mfma_f32_16x16x32_bf16 v[32:35], v[166:169], v[190:193], v[32:35]
	v_mfma_f32_16x16x32_bf16 v[20:23], v[158:161], v[198:201], v[20:23]
	v_mfma_f32_16x16x32_bf16 v[16:19], v[166:169], v[198:201], v[16:19]
	v_mfma_f32_16x16x32_bf16 v[60:63], v[162:165], v[178:181], v[60:63]
	v_mfma_f32_16x16x32_bf16 v[56:59], v[170:173], v[178:181], v[56:59]
	v_mfma_f32_16x16x32_bf16 v[52:55], v[162:165], v[186:189], v[52:55]
	v_mfma_f32_16x16x32_bf16 v[48:51], v[170:173], v[186:189], v[48:51]
	v_mfma_f32_16x16x32_bf16 v[36:39], v[162:165], v[194:197], v[36:39]
	v_mfma_f32_16x16x32_bf16 v[32:35], v[170:173], v[194:197], v[32:35]
	v_mfma_f32_16x16x32_bf16 v[20:23], v[162:165], v[202:205], v[20:23]
	v_mfma_f32_16x16x32_bf16 v[16:19], v[170:173], v[202:205], v[16:19]
	s_setprio 0
	s_barrier
	s_add_u32 s28, s34, 0x40080
	s_addc_u32 s29, s35, 0
	s_mov_b32 m0, s56
	s_nop 0
	global_load_lds_dwordx4 v132, s[28:29]
	s_mov_b32 m0, s57
	s_nop 0
	global_load_lds_dwordx4 v128, s[28:29]
	s_waitcnt vmcnt(6)
	s_barrier
	s_setprio 1
	v_mfma_f32_16x16x32_bf16 v[44:47], v[210:213], v[174:177], v[44:47]
	v_mfma_f32_16x16x32_bf16 v[40:43], v[218:221], v[174:177], v[40:43]
	v_mfma_f32_16x16x32_bf16 v[28:31], v[210:213], v[182:185], v[28:31]
	v_mfma_f32_16x16x32_bf16 v[24:27], v[218:221], v[182:185], v[24:27]
	v_mfma_f32_16x16x32_bf16 v[12:15], v[210:213], v[190:193], v[12:15]
	v_mfma_f32_16x16x32_bf16 v[8:11], v[218:221], v[190:193], v[8:11]
	v_mfma_f32_16x16x32_bf16 v[4:7], v[210:213], v[198:201], v[4:7]
	v_mfma_f32_16x16x32_bf16 v[0:3], v[218:221], v[198:201], v[0:3]
	v_mfma_f32_16x16x32_bf16 v[44:47], v[214:217], v[178:181], v[44:47]
	v_mfma_f32_16x16x32_bf16 v[40:43], v[222:225], v[178:181], v[40:43]
	v_mfma_f32_16x16x32_bf16 v[28:31], v[214:217], v[186:189], v[28:31]
	v_mfma_f32_16x16x32_bf16 v[24:27], v[222:225], v[186:189], v[24:27]
	v_mfma_f32_16x16x32_bf16 v[12:15], v[214:217], v[194:197], v[12:15]
	v_mfma_f32_16x16x32_bf16 v[8:11], v[222:225], v[194:197], v[8:11]
	v_mfma_f32_16x16x32_bf16 v[4:7], v[214:217], v[202:205], v[4:7]
	v_mfma_f32_16x16x32_bf16 v[0:3], v[222:225], v[202:205], v[0:3]
	s_setprio 0
	s_add_i32 s60, s60, 2
	s_cmp_gt_u32 s60, 13
	s_mov_b64 s[28:29], s[30:31]
	s_barrier
	s_cbranch_scc0 .LBB0_1204
	v_mov_b32_e32 v159, v140
	s_mov_b64 s[12:13], 0x80000
	v_ashrrev_i32_e32 v158, 2, v159
	v_and_b32_e32 v158, 0xffffffc0, v158
	v_lshl_add_u32 v158, s2, 8, v158
	v_and_or_b32 v158, v159, 15, v158
	v_lshrrev_b32_e32 v159, 1, v159
	v_and_b32_e32 v159, 0x78, v159
	v_lshl_or_b32 v160, s59, 8, v159
	v_ashrrev_i32_e32 v159, 31, v158
	v_ashrrev_i32_e32 v161, 31, v160
	v_lshlrev_b64 v[162:163], 12, v[158:159]
	v_lshl_add_u64 v[162:163], s[0:1], 0, v[162:163]
	v_lshlrev_b64 v[160:161], 1, v[160:161]
	v_lshl_add_u64 v[162:163], v[162:163], 0, v[160:161]
	s_mov_b32 s2, 0x80000
	v_cvt_pk_bf16_f32 v60, v60, v61
	v_cvt_pk_bf16_f32 v61, v62, v63
	v_cvt_pk_bf16_f32 v62, v56, v57
	v_add_co_u32_e32 v56, vcc, s2, v162
	v_cvt_pk_bf16_f32 v68, v68, v69
	v_cvt_pk_bf16_f32 v69, v70, v71
	v_cvt_pk_bf16_f32 v70, v64, v65
	v_lshl_add_u64 v[64:65], v[162:163], 0, s[12:13]
	v_addc_co_u32_e32 v57, vcc, 0, v163, vcc
	v_cvt_pk_bf16_f32 v44, v44, v45
	v_cvt_pk_bf16_f32 v45, v46, v47
	v_cvt_pk_bf16_f32 v46, v40, v41
	v_cvt_pk_bf16_f32 v47, v42, v43
	s_mov_b32 s2, 0x90000
	v_cvt_pk_bf16_f32 v112, v112, v113
	v_cvt_pk_bf16_f32 v113, v114, v115
	v_cvt_pk_bf16_f32 v114, v104, v105
	v_or_b32_e32 v104, 16, v158
	global_store_dwordx4 v[64:65], v[44:47], off offset:256
	s_mov_b64 s[12:13], 0x90000
	v_ashrrev_i32_e32 v105, 31, v104
	v_add_co_u32_e32 v46, vcc, s2, v162
	v_cvt_pk_bf16_f32 v96, v96, v97
	v_cvt_pk_bf16_f32 v97, v98, v99
	v_cvt_pk_bf16_f32 v98, v88, v89
	v_or_b32_e32 v88, 32, v158
	v_lshl_add_u64 v[44:45], v[162:163], 0, s[12:13]
	v_addc_co_u32_e32 v47, vcc, 0, v163, vcc
	v_cvt_pk_bf16_f32 v28, v28, v29
	v_cvt_pk_bf16_f32 v29, v30, v31
	v_cvt_pk_bf16_f32 v30, v24, v25
	v_cvt_pk_bf16_f32 v31, v26, v27
	s_mov_b32 s2, 0xa0000
	v_lshlrev_b64 v[104:105], 12, v[104:105]
	v_ashrrev_i32_e32 v89, 31, v88
	v_cvt_pk_bf16_f32 v80, v80, v81
	v_cvt_pk_bf16_f32 v81, v82, v83
	v_cvt_pk_bf16_f32 v82, v72, v73
	v_or_b32_e32 v72, 48, v158
	global_store_dwordx4 v[44:45], v[28:31], off offset:256
	s_mov_b64 s[12:13], 0xa0000
	v_cvt_pk_bf16_f32 v115, v106, v107
	v_add_co_u32_e32 v30, vcc, s2, v162
	v_lshl_add_u64 v[104:105], s[0:1], 0, v[104:105]
	v_lshlrev_b64 v[88:89], 12, v[88:89]
	v_ashrrev_i32_e32 v73, 31, v72
	v_lshl_add_u64 v[28:29], v[162:163], 0, s[12:13]
	v_addc_co_u32_e32 v31, vcc, 0, v163, vcc
	v_cvt_pk_bf16_f32 v12, v12, v13
	v_cvt_pk_bf16_f32 v13, v14, v15
	v_cvt_pk_bf16_f32 v14, v8, v9
	v_cvt_pk_bf16_f32 v15, v10, v11
	s_mov_b32 s2, 0xb0000
	global_store_dwordx4 v[162:163], v[112:115], off offset:256
	v_cvt_pk_bf16_f32 v99, v90, v91
	v_lshl_add_u64 v[88:89], s[0:1], 0, v[88:89]
	v_lshl_add_u64 v[112:113], v[104:105], 0, v[160:161]
	v_lshlrev_b64 v[72:73], 12, v[72:73]
	global_store_dwordx4 v[28:29], v[12:15], off offset:256
	global_store_dwordx4 v[112:113], v[96:99], off offset:256
	v_cvt_pk_bf16_f32 v83, v74, v75
	v_add_co_u32_e32 v14, vcc, s2, v162
	v_lshl_add_u64 v[96:97], v[88:89], 0, v[160:161]
	v_lshl_add_u64 v[72:73], s[0:1], 0, v[72:73]
	s_mov_b64 s[12:13], 0xb0000
	v_addc_co_u32_e32 v15, vcc, 0, v163, vcc
	v_cvt_pk_bf16_f32 v124, v124, v125
	v_cvt_pk_bf16_f32 v125, v126, v127
	v_cvt_pk_bf16_f32 v126, v120, v121
	v_cvt_pk_bf16_f32 v127, v122, v123
	v_cvt_pk_bf16_f32 v104, v116, v117
	v_cvt_pk_bf16_f32 v105, v118, v119
	v_cvt_pk_bf16_f32 v106, v108, v109
	v_cvt_pk_bf16_f32 v107, v110, v111
	v_cvt_pk_bf16_f32 v88, v100, v101
	v_cvt_pk_bf16_f32 v89, v102, v103
	v_cvt_pk_bf16_f32 v90, v92, v93
	v_cvt_pk_bf16_f32 v91, v94, v95
	global_store_dwordx4 v[96:97], v[80:83], off offset:256
	v_cvt_pk_bf16_f32 v74, v76, v77
	v_cvt_pk_bf16_f32 v75, v78, v79
	v_lshl_add_u64 v[80:81], v[72:73], 0, v[160:161]
	v_cvt_pk_bf16_f32 v72, v84, v85
	v_cvt_pk_bf16_f32 v73, v86, v87
	v_cvt_pk_bf16_f32 v71, v66, v67
	v_cvt_pk_bf16_f32 v63, v58, v59
	v_cvt_pk_bf16_f32 v40, v52, v53
	v_cvt_pk_bf16_f32 v41, v54, v55
	v_cvt_pk_bf16_f32 v42, v48, v49
	v_cvt_pk_bf16_f32 v43, v50, v51
	v_cvt_pk_bf16_f32 v24, v36, v37
	v_cvt_pk_bf16_f32 v25, v38, v39
	v_cvt_pk_bf16_f32 v26, v32, v33
	v_cvt_pk_bf16_f32 v27, v34, v35
	v_lshl_add_u64 v[12:13], v[162:163], 0, s[12:13]
	v_cvt_pk_bf16_f32 v8, v20, v21
	v_cvt_pk_bf16_f32 v9, v22, v23
	v_cvt_pk_bf16_f32 v10, v16, v17
	v_cvt_pk_bf16_f32 v11, v18, v19
	v_cvt_pk_bf16_f32 v4, v4, v5
	v_cvt_pk_bf16_f32 v5, v6, v7
	v_cvt_pk_bf16_f32 v6, v0, v1
	v_cvt_pk_bf16_f32 v7, v2, v3
	s_and_b64 vcc, exec, s[6:7]
	s_mov_b32 s59, s18
	s_mov_b32 s2, s20
	s_mov_b64 s[16:17], s[26:27]
	s_mov_b64 s[22:23], s[24:25]
	global_store_dwordx4 v[162:163], v[124:127], off
	global_store_dwordx4 v[112:113], v[104:107], off
	global_store_dwordx4 v[96:97], v[88:91], off
	global_store_dwordx4 v[80:81], v[72:75], off
	global_store_dwordx4 v[80:81], v[68:71], off offset:256
	global_store_dwordx4 v[56:57], v[60:63], off
	global_store_dwordx4 v[46:47], v[40:43], off
	global_store_dwordx4 v[30:31], v[24:27], off
	global_store_dwordx4 v[14:15], v[8:11], off
	global_store_dwordx4 v[12:13], v[4:7], off offset:256
	s_cbranch_vccz .LBB0_1201
	s_waitcnt vmcnt(0)
	v_readlane_b32 s54, v242, 34
	s_cmpk_gt_u32 s33, 0xff
	v_readlane_b32 s55, v242, 35
	s_cbranch_scc1 .LBB0_1208
	s_barrier

.LBB0_1286:
	s_or_b64 exec, exec, s[0:1]
	v_readlane_b32 s1, v242, 29
	s_and_b32 s38, s1, 0x180
	s_or_b32 s1, s38, 0x200
	v_writelane_b32 v242, s1, 55
	v_mov_b32_e32 v71, v208
	v_readlane_b32 s2, v242, 25
	v_readlane_b32 s3, v242, 26
	s_or_b32 s23, s38, 0x400
	s_and_b64 vcc, exec, s[2:3]
	s_or_b32 s22, s38, 0x600
	s_waitcnt lgkmcnt(0)
	s_barrier
	s_nop 0
	s_mov_b32 s0, 0
	s_cbranch_vccnz .LBB0_1307
	v_readlane_b32 s4, v242, 1
	v_readlane_b32 s5, v242, 2
	s_load_dwordx4 s[8:11], s[4:5], s0 offset:0x88
	s_load_dwordx2 s[2:3], s[4:5], s0 offset:0xa0
	s_load_dwordx4 s[12:15], s[4:5], s0 offset:0xb0
	s_nop 0
	s_load_dwordx2 s[0:1], s[4:5], s0 offset:0x108
	v_and_b32_e32 v64, 48, v71
	v_mov_b32_e32 v65, 0
	v_ashrrev_i32_e32 v68, 6, v71
	v_and_b32_e32 v67, 15, v71
	s_waitcnt lgkmcnt(0)
	v_lshl_add_u64 v[0:1], s[0:1], 0, v[64:65]
	s_mov_b64 s[4:5], 0x2d2f000
	v_lshl_or_b32 v66, v68, 4, v67
	v_lshl_add_u64 v[48:49], v[0:1], 0, s[4:5]
	v_readlane_b32 s4, v242, 55
	v_add_u32_e32 v136, s38, v66
	v_add_u32_e32 v32, s23, v66
	v_add_u32_e32 v16, s4, v66
	v_add_u32_e32 v50, s22, v66
	v_ashrrev_i32_e32 v137, 31, v136
	v_ashrrev_i32_e32 v17, 31, v16
	v_ashrrev_i32_e32 v33, 31, v32
	v_ashrrev_i32_e32 v51, 31, v50
	v_and_b32_e32 v69, 63, v71
	v_lshlrev_b64 v[0:1], 8, v[136:137]
	v_lshlrev_b64 v[16:17], 8, v[16:17]
	v_lshlrev_b64 v[32:33], 8, v[32:33]
	v_lshlrev_b64 v[50:51], 8, v[50:51]
	v_lshlrev_b64 v[72:73], 2, v[136:137]
	v_lshl_add_u64 v[12:13], v[48:49], 0, v[0:1]
	v_lshl_add_u64 v[28:29], v[48:49], 0, v[16:17]
	v_lshl_add_u64 v[44:45], v[48:49], 0, v[32:33]
	v_lshl_add_u64 v[60:61], v[48:49], 0, v[50:51]
	v_lshl_add_u64 v[74:75], s[2:3], 0, v[72:73]
	v_lshl_add_u64 v[78:79], s[12:13], 0, v[72:73]
	v_lshlrev_b32_e32 v70, 1, v69
	global_load_dwordx4 v[0:3], v[12:13], off
	global_load_dwordx4 v[4:7], v[12:13], off offset:64
	global_load_dwordx4 v[8:11], v[12:13], off offset:128
	s_nop 0
	global_load_dwordx4 v[12:15], v[12:13], off offset:192
	s_nop 0
	global_load_dwordx4 v[16:19], v[28:29], off
	global_load_dwordx4 v[20:23], v[28:29], off offset:64
	global_load_dwordx4 v[24:27], v[28:29], off offset:128
	s_nop 0
	global_load_dwordx4 v[28:31], v[28:29], off offset:192
	s_nop 0
	global_load_dwordx4 v[32:35], v[44:45], off
	global_load_dwordx4 v[36:39], v[44:45], off offset:64
	global_load_dwordx4 v[40:43], v[44:45], off offset:128
	s_nop 0
	global_load_dwordx4 v[44:47], v[44:45], off offset:192
	s_nop 0
	global_load_dwordx4 v[48:51], v[60:61], off
	global_load_dwordx4 v[52:55], v[60:61], off offset:64
	global_load_dwordx4 v[56:59], v[60:61], off offset:128
	s_nop 0
	global_load_dwordx4 v[60:63], v[60:61], off offset:192
	v_lshl_add_u64 v[80:81], s[14:15], 0, v[72:73]
	global_load_dword v77, v[74:75], off
	s_nop 0
	global_load_dword v74, v[74:75], off offset:2048
	s_nop 0
	global_load_dword v76, v[78:79], off
	global_load_dword v73, v[78:79], off offset:2048
	global_load_dword v75, v[80:81], off
	global_load_dword v72, v[80:81], off offset:2048
	v_or_b32_e32 v78, s38, v70
	v_lshlrev_b32_e32 v78, 2, v78
	v_mov_b32_e32 v79, v65
	v_lshl_add_u64 v[80:81], s[8:9], 0, v[78:79]
	s_movk_i32 s5, 0x1000
	global_load_dwordx2 v[138:139], v78, s[10:11]
	global_load_dwordx2 v[140:141], v78, s[8:9]
	global_load_dwordx2 v[142:143], v78, s[8:9] offset:2048
	v_add_co_u32_e32 v78, vcc, s5, v80
	v_readlane_b32 s2, v242, 0
	s_nop 0
	v_addc_co_u32_e32 v79, vcc, 0, v81, vcc
	global_load_dwordx2 v[144:145], v[78:79], off
	global_load_dwordx2 v[146:147], v[78:79], off offset:2048
	s_ashr_i32 s2, s2, 2
	s_mul_hi_i32 s3, s2, 0x78787879
	s_lshr_b32 s4, s3, 31
	s_ashr_i32 s7, s3, 5
	s_add_i32 s7, s7, s4
	s_mul_i32 s3, s7, 0x44
	s_sub_i32 s2, s2, s3
	s_lshl_b32 s8, s2, 6
	s_cmp_gt_i32 s2, 3
	s_cbranch_scc0 .LBB0_1289
	s_lshl_b32 s4, s7, 12
	s_add_i32 s2, s8, s4
	s_add_i32 s6, s2, 0xffffff00
	v_bfe_u32 v65, v71, 4, 2
	s_cbranch_execz .LBB0_1290
	s_branch .LBB0_1291

.LBB0_1558:
	s_add_u32 s36, s34, 0x100
	ds_read_b128 v[32:35], v167
	ds_read_b128 v[36:39], v168
	ds_read_b128 v[48:51], v175
	ds_read_b128 v[52:55], v176
	s_addc_u32 s37, s35, 0
	s_and_b32 s25, s36, 0x700
	s_add_u32 s33, s4, s25
	s_addc_u32 s65, s5, 0
	s_cmp_eq_u32 s23, 12
	s_cselect_b64 s[40:41], -1, 0
	s_and_b64 s[38:39], s[40:41], exec
	s_cselect_b32 s39, s1, s65
	s_cselect_b32 s38, s10, s33
	s_cselect_b32 s33, 0, 0
	s_cselect_b32 s25, 0, s25
	s_add_u32 s34, s30, s34
	s_addc_u32 s35, s31, s35
	s_add_u32 s34, s34, 0x40080
	s_addc_u32 s35, s35, 0
	ds_read_b128 v[158:161], v183
	ds_read_b128 v[162:165], v183 offset:1024
	ds_read_b128 v[184:187], v183 offset:2048
	ds_read_b128 v[188:191], v183 offset:3072
	ds_read_b128 v[192:195], v183 offset:4096
	ds_read_b128 v[196:199], v183 offset:5120
	ds_read_b128 v[200:203], v183 offset:6144
	ds_read_b128 v[204:207], v183 offset:7168
	s_add_i32 m0, s3, 0xc000
	s_nop 0
	global_load_lds_dwordx4 v144, s[34:35]
	s_add_i32 m0, s3, 0xe000
	s_nop 0
	global_load_lds_dwordx4 v148, s[34:35]
	s_waitcnt lgkmcnt(8)
	s_barrier
	s_waitcnt lgkmcnt(0)
	s_setprio 1
	s_waitcnt lgkmcnt(0)
	v_mfma_f32_16x16x32_bf16 v[140:143], v[32:35], v[158:161], v[140:143]
	v_mfma_f32_16x16x32_bf16 v[136:139], v[48:51], v[158:161], v[136:139]
	v_mfma_f32_16x16x32_bf16 v[124:127], v[32:35], v[184:187], v[124:127]
	v_mfma_f32_16x16x32_bf16 v[120:123], v[48:51], v[184:187], v[120:123]
	v_mfma_f32_16x16x32_bf16 v[108:111], v[32:35], v[192:195], v[108:111]
	v_mfma_f32_16x16x32_bf16 v[104:107], v[48:51], v[192:195], v[104:107]
	v_mfma_f32_16x16x32_bf16 v[92:95], v[32:35], v[200:203], v[92:95]
	v_mfma_f32_16x16x32_bf16 v[88:91], v[48:51], v[200:203], v[88:91]
	v_mfma_f32_16x16x32_bf16 v[140:143], v[36:39], v[162:165], v[140:143]
	v_mfma_f32_16x16x32_bf16 v[136:139], v[52:55], v[162:165], v[136:139]
	v_mfma_f32_16x16x32_bf16 v[124:127], v[36:39], v[188:191], v[124:127]
	v_mfma_f32_16x16x32_bf16 v[120:123], v[52:55], v[188:191], v[120:123]
	v_mfma_f32_16x16x32_bf16 v[108:111], v[36:39], v[196:199], v[108:111]
	v_mfma_f32_16x16x32_bf16 v[104:107], v[52:55], v[196:199], v[104:107]
	v_mfma_f32_16x16x32_bf16 v[92:95], v[36:39], v[204:207], v[92:95]
	v_mfma_f32_16x16x32_bf16 v[88:91], v[52:55], v[204:207], v[88:91]
	s_setprio 0
	s_barrier
	s_mov_b64 s[34:35], s[38:39]
	s_mov_b32 m0, s47
	ds_read_b128 v[210:213], v169
	ds_read_b128 v[214:217], v170
	ds_read_b128 v[218:221], v177
	ds_read_b128 v[222:225], v178
	s_nop 0
	global_load_lds_dwordx4 v146, s[34:35]
	s_mov_b32 m0, s48
	s_nop 0
	global_load_lds_dwordx4 v150, s[34:35]
	s_nop 0
	s_barrier
	s_waitcnt lgkmcnt(0)
	s_setprio 1
	s_waitcnt lgkmcnt(0)
	v_mfma_f32_16x16x32_bf16 v[132:135], v[210:213], v[158:161], v[132:135]
	v_mfma_f32_16x16x32_bf16 v[128:131], v[218:221], v[158:161], v[128:131]
	v_mfma_f32_16x16x32_bf16 v[116:119], v[210:213], v[184:187], v[116:119]
	v_mfma_f32_16x16x32_bf16 v[112:115], v[218:221], v[184:187], v[112:115]
	v_mfma_f32_16x16x32_bf16 v[100:103], v[210:213], v[192:195], v[100:103]
	v_mfma_f32_16x16x32_bf16 v[96:99], v[218:221], v[192:195], v[96:99]
	v_mfma_f32_16x16x32_bf16 v[84:87], v[210:213], v[200:203], v[84:87]
	v_mfma_f32_16x16x32_bf16 v[80:83], v[218:221], v[200:203], v[80:83]
	v_mfma_f32_16x16x32_bf16 v[132:135], v[214:217], v[162:165], v[132:135]
	v_mfma_f32_16x16x32_bf16 v[128:131], v[222:225], v[162:165], v[128:131]
	v_mfma_f32_16x16x32_bf16 v[116:119], v[214:217], v[188:191], v[116:119]
	v_mfma_f32_16x16x32_bf16 v[112:115], v[222:225], v[188:191], v[112:115]
	v_mfma_f32_16x16x32_bf16 v[100:103], v[214:217], v[196:199], v[100:103]
	v_mfma_f32_16x16x32_bf16 v[96:99], v[222:225], v[196:199], v[96:99]
	v_mfma_f32_16x16x32_bf16 v[84:87], v[214:217], v[204:207], v[84:87]
	v_mfma_f32_16x16x32_bf16 v[80:83], v[222:225], v[204:207], v[80:83]
	s_setprio 0
	s_and_b64 s[34:35], s[14:15], s[40:41]
	s_and_b64 s[34:35], s[34:35], exec
	s_cselect_b32 s34, s26, s30
	s_cselect_b32 s35, s27, s31
	s_add_u32 s34, s34, s25
	s_addc_u32 s35, s35, s33
	s_mov_b64 s[40:41], s[34:35]
	s_mov_b32 m0, s3
	s_barrier
	ds_read_b128 v[158:161], v183 offset:16384
	ds_read_b128 v[162:165], v183 offset:17408
	ds_read_b128 v[184:187], v183 offset:18432
	ds_read_b128 v[188:191], v183 offset:19456
	ds_read_b128 v[192:195], v183 offset:20480
	ds_read_b128 v[196:199], v183 offset:21504
	ds_read_b128 v[200:203], v183 offset:22528
	ds_read_b128 v[204:207], v183 offset:23552
	s_nop 0
	global_load_lds_dwordx4 v144, s[40:41]
	s_mov_b32 m0, s49
	s_nop 0
	global_load_lds_dwordx4 v148, s[40:41]
	s_nop 0
	s_barrier
	s_waitcnt lgkmcnt(0)
	s_setprio 1
	s_waitcnt lgkmcnt(0)
	v_mfma_f32_16x16x32_bf16 v[76:79], v[32:35], v[158:161], v[76:79]
	v_mfma_f32_16x16x32_bf16 v[72:75], v[48:51], v[158:161], v[72:75]
	v_mfma_f32_16x16x32_bf16 v[60:63], v[32:35], v[184:187], v[60:63]
	v_mfma_f32_16x16x32_bf16 v[56:59], v[48:51], v[184:187], v[56:59]
	v_mfma_f32_16x16x32_bf16 v[28:31], v[32:35], v[192:195], v[28:31]
	v_mfma_f32_16x16x32_bf16 v[24:27], v[48:51], v[192:195], v[24:27]
	v_mfma_f32_16x16x32_bf16 v[12:15], v[32:35], v[200:203], v[12:15]
	v_mfma_f32_16x16x32_bf16 v[8:11], v[48:51], v[200:203], v[8:11]
	v_mfma_f32_16x16x32_bf16 v[76:79], v[36:39], v[162:165], v[76:79]
	v_mfma_f32_16x16x32_bf16 v[72:75], v[52:55], v[162:165], v[72:75]
	v_mfma_f32_16x16x32_bf16 v[60:63], v[36:39], v[188:191], v[60:63]
	v_mfma_f32_16x16x32_bf16 v[56:59], v[52:55], v[188:191], v[56:59]
	v_mfma_f32_16x16x32_bf16 v[28:31], v[36:39], v[196:199], v[28:31]
	v_mfma_f32_16x16x32_bf16 v[24:27], v[52:55], v[196:199], v[24:27]
	v_mfma_f32_16x16x32_bf16 v[12:15], v[36:39], v[204:207], v[12:15]
	v_mfma_f32_16x16x32_bf16 v[8:11], v[52:55], v[204:207], v[8:11]
	s_setprio 0
	s_barrier
	s_add_u32 s40, s38, 0x40000
	s_addc_u32 s41, s39, 0
	s_mov_b32 m0, s50
	s_nop 0
	global_load_lds_dwordx4 v146, s[40:41]
	s_mov_b32 m0, s51
	s_nop 0
	global_load_lds_dwordx4 v150, s[40:41]
	s_waitcnt vmcnt(6)
	s_barrier
	s_setprio 1
	v_mfma_f32_16x16x32_bf16 v[44:47], v[210:213], v[184:187], v[44:47]
	v_mfma_f32_16x16x32_bf16 v[40:43], v[218:221], v[184:187], v[40:43]
	v_mfma_f32_16x16x32_bf16 v[20:23], v[210:213], v[192:195], v[20:23]
	v_mfma_f32_16x16x32_bf16 v[16:19], v[218:221], v[192:195], v[16:19]
	v_mfma_f32_16x16x32_bf16 v[4:7], v[210:213], v[200:203], v[4:7]
	v_mfma_f32_16x16x32_bf16 v[0:3], v[218:221], v[200:203], v[0:3]
	v_mfma_f32_16x16x32_bf16 v[32:35], v[210:213], v[158:161], v[68:71]
	v_mfma_f32_16x16x32_bf16 v[36:39], v[218:221], v[158:161], v[64:67]
	v_mfma_f32_16x16x32_bf16 v[44:47], v[214:217], v[188:191], v[44:47]
	v_mfma_f32_16x16x32_bf16 v[40:43], v[222:225], v[188:191], v[40:43]
	v_mfma_f32_16x16x32_bf16 v[20:23], v[214:217], v[196:199], v[20:23]
	v_mfma_f32_16x16x32_bf16 v[16:19], v[222:225], v[196:199], v[16:19]
	v_mfma_f32_16x16x32_bf16 v[4:7], v[214:217], v[204:207], v[4:7]
	v_mfma_f32_16x16x32_bf16 v[0:3], v[222:225], v[204:207], v[0:3]
	v_mfma_f32_16x16x32_bf16 v[32:35], v[214:217], v[162:165], v[32:35]
	v_mfma_f32_16x16x32_bf16 v[36:39], v[222:225], v[162:165], v[36:39]
	s_setprio 0
	s_barrier
	ds_read_b128 v[48:51], v171
	ds_read_b128 v[52:55], v172
	ds_read_b128 v[64:67], v179
	ds_read_b128 v[68:71], v180
	s_add_u32 s40, s34, 0x40000
	s_addc_u32 s41, s35, 0
	s_mov_b32 m0, s52
	ds_read_b128 v[158:161], v183 offset:32768
	ds_read_b128 v[162:165], v183 offset:33792
	ds_read_b128 v[184:187], v183 offset:34816
	ds_read_b128 v[188:191], v183 offset:35840
	ds_read_b128 v[192:195], v183 offset:36864
	ds_read_b128 v[196:199], v183 offset:37888
	ds_read_b128 v[200:203], v183 offset:38912
	ds_read_b128 v[204:207], v183 offset:39936
	s_nop 0
	global_load_lds_dwordx4 v144, s[40:41]
	s_mov_b32 m0, s53
	s_nop 0
	global_load_lds_dwordx4 v148, s[40:41]
	s_waitcnt lgkmcnt(8)
	s_barrier
	s_waitcnt lgkmcnt(0)
	s_setprio 1
	s_waitcnt lgkmcnt(0)
	v_mfma_f32_16x16x32_bf16 v[140:143], v[48:51], v[158:161], v[140:143]
	v_mfma_f32_16x16x32_bf16 v[136:139], v[64:67], v[158:161], v[136:139]
	v_mfma_f32_16x16x32_bf16 v[124:127], v[48:51], v[184:187], v[124:127]
	v_mfma_f32_16x16x32_bf16 v[120:123], v[64:67], v[184:187], v[120:123]
	v_mfma_f32_16x16x32_bf16 v[108:111], v[48:51], v[192:195], v[108:111]
	v_mfma_f32_16x16x32_bf16 v[104:107], v[64:67], v[192:195], v[104:107]
	v_mfma_f32_16x16x32_bf16 v[92:95], v[48:51], v[200:203], v[92:95]
	v_mfma_f32_16x16x32_bf16 v[88:91], v[64:67], v[200:203], v[88:91]
	v_mfma_f32_16x16x32_bf16 v[140:143], v[52:55], v[162:165], v[140:143]
	v_mfma_f32_16x16x32_bf16 v[136:139], v[68:71], v[162:165], v[136:139]
	v_mfma_f32_16x16x32_bf16 v[124:127], v[52:55], v[188:191], v[124:127]
	v_mfma_f32_16x16x32_bf16 v[120:123], v[68:71], v[188:191], v[120:123]
	v_mfma_f32_16x16x32_bf16 v[108:111], v[52:55], v[196:199], v[108:111]
	v_mfma_f32_16x16x32_bf16 v[104:107], v[68:71], v[196:199], v[104:107]
	v_mfma_f32_16x16x32_bf16 v[92:95], v[52:55], v[204:207], v[92:95]
	v_mfma_f32_16x16x32_bf16 v[88:91], v[68:71], v[204:207], v[88:91]
	s_setprio 0
	s_barrier
	s_add_u32 s40, s38, 0x80
	s_addc_u32 s41, s39, 0
	s_mov_b32 m0, s56
	ds_read_b128 v[210:213], v173
	ds_read_b128 v[214:217], v174
	ds_read_b128 v[218:221], v181
	ds_read_b128 v[222:225], v182
	s_nop 0
	global_load_lds_dwordx4 v146, s[40:41]
	s_mov_b32 m0, s57
	s_nop 0
	global_load_lds_dwordx4 v150, s[40:41]
	s_nop 0
	s_barrier
	s_waitcnt lgkmcnt(0)
	s_setprio 1
	s_waitcnt lgkmcnt(0)
	v_mfma_f32_16x16x32_bf16 v[132:135], v[210:213], v[158:161], v[132:135]
	v_mfma_f32_16x16x32_bf16 v[128:131], v[218:221], v[158:161], v[128:131]
	v_mfma_f32_16x16x32_bf16 v[116:119], v[210:213], v[184:187], v[116:119]
	v_mfma_f32_16x16x32_bf16 v[112:115], v[218:221], v[184:187], v[112:115]
	v_mfma_f32_16x16x32_bf16 v[100:103], v[210:213], v[192:195], v[100:103]
	v_mfma_f32_16x16x32_bf16 v[96:99], v[218:221], v[192:195], v[96:99]
	v_mfma_f32_16x16x32_bf16 v[84:87], v[210:213], v[200:203], v[84:87]
	v_mfma_f32_16x16x32_bf16 v[80:83], v[218:221], v[200:203], v[80:83]
	v_mfma_f32_16x16x32_bf16 v[132:135], v[214:217], v[162:165], v[132:135]
	v_mfma_f32_16x16x32_bf16 v[128:131], v[222:225], v[162:165], v[128:131]
	v_mfma_f32_16x16x32_bf16 v[116:119], v[214:217], v[188:191], v[116:119]
	v_mfma_f32_16x16x32_bf16 v[112:115], v[222:225], v[188:191], v[112:115]
	v_mfma_f32_16x16x32_bf16 v[100:103], v[214:217], v[196:199], v[100:103]
	v_mfma_f32_16x16x32_bf16 v[96:99], v[222:225], v[196:199], v[96:99]
	v_mfma_f32_16x16x32_bf16 v[84:87], v[214:217], v[204:207], v[84:87]
	v_mfma_f32_16x16x32_bf16 v[80:83], v[222:225], v[204:207], v[80:83]
	s_setprio 0
	s_add_u32 s34, s34, 0x80
	s_addc_u32 s35, s35, 0
	s_mov_b32 m0, s58
	s_barrier
	ds_read_b128 v[158:161], v183 offset:49152
	ds_read_b128 v[162:165], v183 offset:50176
	ds_read_b128 v[184:187], v183 offset:51200
	ds_read_b128 v[188:191], v183 offset:52224
	ds_read_b128 v[192:195], v183 offset:53248
	ds_read_b128 v[196:199], v183 offset:54272
	ds_read_b128 v[200:203], v183 offset:55296
	ds_read_b128 v[204:207], v183 offset:56320
	s_nop 0
	global_load_lds_dwordx4 v144, s[34:35]
	s_mov_b32 m0, s59
	s_nop 0
	global_load_lds_dwordx4 v148, s[34:35]
	s_nop 0
	s_barrier
	s_waitcnt lgkmcnt(0)
	s_setprio 1
	s_waitcnt lgkmcnt(0)
	v_mfma_f32_16x16x32_bf16 v[76:79], v[48:51], v[158:161], v[76:79]
	v_mfma_f32_16x16x32_bf16 v[72:75], v[64:67], v[158:161], v[72:75]
	v_mfma_f32_16x16x32_bf16 v[60:63], v[48:51], v[184:187], v[60:63]
	v_mfma_f32_16x16x32_bf16 v[56:59], v[64:67], v[184:187], v[56:59]
	v_mfma_f32_16x16x32_bf16 v[28:31], v[48:51], v[192:195], v[28:31]
	v_mfma_f32_16x16x32_bf16 v[24:27], v[64:67], v[192:195], v[24:27]
	v_mfma_f32_16x16x32_bf16 v[12:15], v[48:51], v[200:203], v[12:15]
	v_mfma_f32_16x16x32_bf16 v[8:11], v[64:67], v[200:203], v[8:11]
	v_mfma_f32_16x16x32_bf16 v[76:79], v[52:55], v[162:165], v[76:79]
	v_mfma_f32_16x16x32_bf16 v[72:75], v[68:71], v[162:165], v[72:75]
	v_mfma_f32_16x16x32_bf16 v[60:63], v[52:55], v[188:191], v[60:63]
	v_mfma_f32_16x16x32_bf16 v[56:59], v[68:71], v[188:191], v[56:59]
	v_mfma_f32_16x16x32_bf16 v[28:31], v[52:55], v[196:199], v[28:31]
	v_mfma_f32_16x16x32_bf16 v[24:27], v[68:71], v[196:199], v[24:27]
	v_mfma_f32_16x16x32_bf16 v[12:15], v[52:55], v[204:207], v[12:15]
	v_mfma_f32_16x16x32_bf16 v[8:11], v[68:71], v[204:207], v[8:11]
	s_setprio 0
	s_barrier
	s_add_u32 s34, s38, 0x40080
	s_addc_u32 s35, s39, 0
	s_mov_b32 m0, s60
	s_nop 0
	global_load_lds_dwordx4 v146, s[34:35]
	s_mov_b32 m0, s61
	s_nop 0
	global_load_lds_dwordx4 v150, s[34:35]
	s_waitcnt vmcnt(6)
	s_barrier
	s_setprio 1
	v_mfma_f32_16x16x32_bf16 v[32:35], v[210:213], v[158:161], v[32:35]
	v_mfma_f32_16x16x32_bf16 v[68:71], v[214:217], v[162:165], v[32:35]
	v_mfma_f32_16x16x32_bf16 v[32:35], v[218:221], v[158:161], v[36:39]
	v_mfma_f32_16x16x32_bf16 v[64:67], v[222:225], v[162:165], v[32:35]
	v_mfma_f32_16x16x32_bf16 v[32:35], v[210:213], v[184:187], v[44:47]
	v_mfma_f32_16x16x32_bf16 v[44:47], v[214:217], v[188:191], v[32:35]
	v_mfma_f32_16x16x32_bf16 v[32:35], v[218:221], v[184:187], v[40:43]
	v_mfma_f32_16x16x32_bf16 v[20:23], v[210:213], v[192:195], v[20:23]
	v_mfma_f32_16x16x32_bf16 v[16:19], v[218:221], v[192:195], v[16:19]
	v_mfma_f32_16x16x32_bf16 v[4:7], v[210:213], v[200:203], v[4:7]
	v_mfma_f32_16x16x32_bf16 v[0:3], v[218:221], v[200:203], v[0:3]
	v_mfma_f32_16x16x32_bf16 v[40:43], v[222:225], v[188:191], v[32:35]
	v_mfma_f32_16x16x32_bf16 v[20:23], v[214:217], v[196:199], v[20:23]
	v_mfma_f32_16x16x32_bf16 v[16:19], v[222:225], v[196:199], v[16:19]
	v_mfma_f32_16x16x32_bf16 v[4:7], v[214:217], v[204:207], v[4:7]
	v_mfma_f32_16x16x32_bf16 v[0:3], v[222:225], v[204:207], v[0:3]
	s_setprio 0
	s_add_i32 s23, s23, 2
	s_cmp_gt_u32 s23, 13
	s_mov_b64 s[34:35], s[36:37]
	s_barrier
	s_cbranch_scc0 .LBB0_1558
	v_mov_b32_e32 v32, v166
	s_cmpk_gt_i32 s2, 0x7f
	s_mov_b64 s[4:5], 0xc000
	s_cbranch_scc1 .LBB0_1561
	s_ashr_i32 s1, s2, 31
	s_lshr_b32 s1, s1, 28
	s_add_i32 s1, s2, s1
	s_ashr_i32 s1, s1, 4
	s_mul_hi_i32 s5, s1, 0x1800
	s_mul_i32 s4, s1, 0x1800

.LBB0_1979:
	s_or_b64 exec, exec, s[0:1]
	v_readlane_b32 s2, v242, 1
	v_readlane_b32 s3, v242, 2
	s_waitcnt lgkmcnt(0)
	s_barrier
	s_nop 0
	s_mov_b32 s0, 0
	s_load_dwordx2 s[8:9], s[2:3], s0 offset:0x108
	v_mov_b32_e32 v209, v208
	s_nop 0
	v_ashrrev_i32_e32 v0, 8, v209
	v_cmp_gt_i32_e32 vcc, 10, v0
	s_and_saveexec_b64 s[0:1], vcc
	s_cbranch_execz .LBB0_1986
	v_readlane_b32 s4, v242, 11
	v_readlane_b32 s5, v242, 12
	v_and_b32_e32 v2, 0xff, v209
	s_waitcnt lgkmcnt(0)
	s_add_u32 s2, s8, 0xd8b000
	v_readlane_b32 s5, v242, 0
	v_lshlrev_b32_e32 v1, 2, v2
	s_addc_u32 s3, s9, 0
	s_mov_b32 s6, s4
	s_ashr_i32 s7, s4, 31
	s_ashr_i32 s4, s5, 31
	v_lshl_or_b32 v1, v0, 10, v1
	v_mov_b32_e32 v6, s5
	v_mov_b32_e32 v7, s4
	v_add_u32_e32 v1, 0, v1
	v_add_u32_e32 v3, 0x20010, v1
	v_add_u32_e32 v4, -2, v0
	v_mad_i64_i32 v[0:1], s[4:5], s6, v0, v[6:7]
	s_mov_b32 s4, s6
	s_nop 0
	v_writelane_b32 v242, s4, 11
	s_mov_b64 s[10:11], 0
	s_mov_b64 s[12:13], 0x880
	v_writelane_b32 v242, s5, 12
	s_lshl_b64 s[4:5], s[6:7], 1
	s_mov_b32 s16, 0x78787879
	s_movk_i32 s17, 0x88
	v_mov_b32_e32 v5, 3
	v_mov_b32_e32 v6, 30
	s_branch .LBB0_1982

.LBB0_1994:
	s_add_i32 s22, s4, 0xf2401100
	s_and_b32 s52, s22, 0x300
	s_add_u32 s24, s2, s52
	s_addc_u32 s25, s3, 0
	s_and_b64 s[22:23], s[26:27], exec
	s_cselect_b32 s23, s21, s25
	s_cselect_b32 s22, s50, s24
	s_mov_b64 s[24:25], s[22:23]
	s_mov_b32 m0, s34
	ds_read_b128 v[16:19], v217
	ds_read_b128 v[20:23], v218
	ds_read_b128 v[24:27], v225
	ds_read_b128 v[28:31], v226
	v_mov_b32_e32 v203, v197
	global_load_lds_dwordx4 v194, s[24:25]
	v_lshl_add_u64 v[236:237], s[24:25], 0, v[192:193]
	s_mov_b32 m0, s35
	s_add_u32 s24, s22, 0x80
	global_load_lds_dwordx4 v[236:237], off
	s_barrier
	s_waitcnt lgkmcnt(0)
	s_addc_u32 s25, s23, 0
	s_and_b64 s[26:27], s[26:27], exec
	s_cselect_b32 s27, 0, 0
	s_cselect_b32 s26, 0, s52
	s_setprio 1
	s_waitcnt lgkmcnt(0)
	v_mfma_scale_f32_16x16x128_f8f6f4 v[184:187], v[16:23], v[56:63], v[184:187], v212, v212 op_sel_hi:[0,0,0]
	v_mfma_scale_f32_16x16x128_f8f6f4 v[176:179], v[24:31], v[56:63], v[176:179], v212, v212 op_sel_hi:[0,0,0]
	v_mfma_scale_f32_16x16x128_f8f6f4 v[168:171], v[16:23], v[48:55], v[168:171], v212, v212 op_sel_hi:[0,0,0]
	v_mfma_scale_f32_16x16x128_f8f6f4 v[160:163], v[24:31], v[48:55], v[160:163], v212, v212 op_sel_hi:[0,0,0]
	v_mfma_scale_f32_16x16x128_f8f6f4 v[152:155], v[16:23], v[40:47], v[152:155], v212, v212 op_sel_hi:[0,0,0]
	v_mfma_scale_f32_16x16x128_f8f6f4 v[144:147], v[24:31], v[40:47], v[144:147], v212, v212 op_sel_hi:[0,0,0]
	v_mfma_scale_f32_16x16x128_f8f6f4 v[136:139], v[16:23], v[32:39], v[136:139], v212, v212 op_sel_hi:[0,0,0]
	v_mfma_scale_f32_16x16x128_f8f6f4 v[128:131], v[24:31], v[32:39], v[128:131], v212, v212 op_sel_hi:[0,0,0]
	s_setprio 0
	s_add_u32 s26, s6, s26
	s_addc_u32 s27, s7, s27
	s_mov_b64 s[52:53], s[26:27]
	s_mov_b32 m0, s1
	s_barrier
	ds_read_b128 v[32:35], v231 offset:16384
	ds_read_b128 v[40:43], v231 offset:18432
	ds_read_b128 v[36:39], v232 offset:16384
	ds_read_b128 v[44:47], v232 offset:18432
	ds_read_b128 v[48:51], v231 offset:20480
	ds_read_b128 v[56:59], v231 offset:22528
	ds_read_b128 v[52:55], v232 offset:20480
	ds_read_b128 v[60:63], v232 offset:22528
	s_nop 0
	global_load_lds_dwordx4 v198, s[52:53]
	s_mov_b32 m0, s36
	s_nop 0
	global_load_lds_dwordx4 v200, s[52:53]
	s_nop 0
	s_barrier
	s_waitcnt lgkmcnt(0)
	s_setprio 1
	s_waitcnt lgkmcnt(0)
	v_mfma_scale_f32_16x16x128_f8f6f4 v[124:127], v[0:7], v[32:39], v[124:127], v212, v212 op_sel_hi:[0,0,0]
	v_mfma_scale_f32_16x16x128_f8f6f4 v[116:119], v[8:15], v[32:39], v[116:119], v212, v212 op_sel_hi:[0,0,0]
	v_mfma_scale_f32_16x16x128_f8f6f4 v[108:111], v[0:7], v[40:47], v[108:111], v212, v212 op_sel_hi:[0,0,0]
	v_mfma_scale_f32_16x16x128_f8f6f4 v[100:103], v[8:15], v[40:47], v[100:103], v212, v212 op_sel_hi:[0,0,0]
	v_mfma_scale_f32_16x16x128_f8f6f4 v[92:95], v[0:7], v[48:55], v[92:95], v212, v212 op_sel_hi:[0,0,0]
	v_mfma_scale_f32_16x16x128_f8f6f4 v[84:87], v[8:15], v[48:55], v[84:87], v212, v212 op_sel_hi:[0,0,0]
	v_mfma_scale_f32_16x16x128_f8f6f4 v[76:79], v[0:7], v[56:63], v[76:79], v212, v212 op_sel_hi:[0,0,0]
	v_mfma_scale_f32_16x16x128_f8f6f4 v[68:71], v[8:15], v[56:63], v[68:71], v212, v212 op_sel_hi:[0,0,0]
	s_setprio 0
	s_barrier
	s_add_u32 s52, s22, 0x20000
	s_addc_u32 s53, s23, 0
	s_mov_b32 m0, s37
	s_nop 0
	global_load_lds_dwordx4 v194, s[52:53]
	s_mov_b32 m0, s38
	s_nop 0
	global_load_lds_dwordx4 v192, s[52:53]
	s_waitcnt vmcnt(6)
	s_barrier
	s_setprio 1
	v_mfma_scale_f32_16x16x128_f8f6f4 v[120:123], v[16:23], v[32:39], v[120:123], v212, v212 op_sel_hi:[0,0,0]
	v_mfma_scale_f32_16x16x128_f8f6f4 v[112:115], v[24:31], v[32:39], v[112:115], v212, v212 op_sel_hi:[0,0,0]
	v_mfma_scale_f32_16x16x128_f8f6f4 v[104:107], v[16:23], v[40:47], v[104:107], v212, v212 op_sel_hi:[0,0,0]
	v_mfma_scale_f32_16x16x128_f8f6f4 v[96:99], v[24:31], v[40:47], v[96:99], v212, v212 op_sel_hi:[0,0,0]
	v_mfma_scale_f32_16x16x128_f8f6f4 v[88:91], v[16:23], v[48:55], v[88:91], v212, v212 op_sel_hi:[0,0,0]
	v_mfma_scale_f32_16x16x128_f8f6f4 v[80:83], v[24:31], v[48:55], v[80:83], v212, v212 op_sel_hi:[0,0,0]
	v_mfma_scale_f32_16x16x128_f8f6f4 v[72:75], v[16:23], v[56:63], v[72:75], v212, v212 op_sel_hi:[0,0,0]
	v_mfma_scale_f32_16x16x128_f8f6f4 v[64:67], v[24:31], v[56:63], v[64:67], v212, v212 op_sel_hi:[0,0,0]
	s_setprio 0
	s_barrier
	ds_read_b128 v[0:3], v219
	ds_read_b128 v[4:7], v220
	ds_read_b128 v[8:11], v227
	ds_read_b128 v[12:15], v228
	s_mov_b64 s[52:53], s[26:27]
	s_mov_b32 m0, s39
	ds_read_b128 v[16:19], v231 offset:32768
	ds_read_b128 v[24:27], v231 offset:34816
	ds_read_b128 v[20:23], v232 offset:32768
	ds_read_b128 v[28:31], v232 offset:34816
	ds_read_b128 v[32:35], v231 offset:36864
	ds_read_b128 v[40:43], v231 offset:38912
	ds_read_b128 v[36:39], v232 offset:36864
	ds_read_b128 v[44:47], v232 offset:38912
	s_nop 0
	global_load_lds_dwordx4 v196, s[52:53]
	s_mov_b32 m0, s40
	s_nop 0
	global_load_lds_dwordx4 v202, s[52:53]
	s_waitcnt lgkmcnt(8)
	s_barrier
	s_waitcnt lgkmcnt(0)
	s_setprio 1
	s_waitcnt lgkmcnt(0)
	v_mfma_scale_f32_16x16x128_f8f6f4 v[188:191], v[0:7], v[16:23], v[188:191], v212, v212 op_sel_hi:[0,0,0]
	v_mfma_scale_f32_16x16x128_f8f6f4 v[180:183], v[8:15], v[16:23], v[180:183], v212, v212 op_sel_hi:[0,0,0]
	v_mfma_scale_f32_16x16x128_f8f6f4 v[172:175], v[0:7], v[24:31], v[172:175], v212, v212 op_sel_hi:[0,0,0]
	v_mfma_scale_f32_16x16x128_f8f6f4 v[164:167], v[8:15], v[24:31], v[164:167], v212, v212 op_sel_hi:[0,0,0]
	v_mfma_scale_f32_16x16x128_f8f6f4 v[156:159], v[0:7], v[32:39], v[156:159], v212, v212 op_sel_hi:[0,0,0]
	v_mfma_scale_f32_16x16x128_f8f6f4 v[148:151], v[8:15], v[32:39], v[148:151], v212, v212 op_sel_hi:[0,0,0]
	v_mfma_scale_f32_16x16x128_f8f6f4 v[140:143], v[0:7], v[40:47], v[140:143], v212, v212 op_sel_hi:[0,0,0]
	v_mfma_scale_f32_16x16x128_f8f6f4 v[132:135], v[8:15], v[40:47], v[132:135], v212, v212 op_sel_hi:[0,0,0]
	s_setprio 0
	s_barrier
	s_mov_b32 m0, s42
	ds_read_b128 v[48:51], v221
	ds_read_b128 v[52:55], v222
	ds_read_b128 v[56:59], v229
	ds_read_b128 v[60:63], v230
	s_nop 0
	global_load_lds_dwordx4 v194, s[24:25]
	s_mov_b32 m0, s43
	s_nop 0
	global_load_lds_dwordx4 v192, s[24:25]
	s_barrier
	s_waitcnt lgkmcnt(0)
	s_setprio 1
	s_waitcnt lgkmcnt(0)
	v_mfma_scale_f32_16x16x128_f8f6f4 v[184:187], v[48:55], v[16:23], v[184:187], v212, v212 op_sel_hi:[0,0,0]
	v_mfma_scale_f32_16x16x128_f8f6f4 v[176:179], v[56:63], v[16:23], v[176:179], v212, v212 op_sel_hi:[0,0,0]
	v_mfma_scale_f32_16x16x128_f8f6f4 v[168:171], v[48:55], v[24:31], v[168:171], v212, v212 op_sel_hi:[0,0,0]
	v_mfma_scale_f32_16x16x128_f8f6f4 v[160:163], v[56:63], v[24:31], v[160:163], v212, v212 op_sel_hi:[0,0,0]
	v_mfma_scale_f32_16x16x128_f8f6f4 v[152:155], v[48:55], v[32:39], v[152:155], v212, v212 op_sel_hi:[0,0,0]
	v_mfma_scale_f32_16x16x128_f8f6f4 v[144:147], v[56:63], v[32:39], v[144:147], v212, v212 op_sel_hi:[0,0,0]
	v_mfma_scale_f32_16x16x128_f8f6f4 v[136:139], v[48:55], v[40:47], v[136:139], v212, v212 op_sel_hi:[0,0,0]
	v_mfma_scale_f32_16x16x128_f8f6f4 v[128:131], v[56:63], v[40:47], v[128:131], v212, v212 op_sel_hi:[0,0,0]
	s_setprio 0
	s_add_u32 s24, s26, 0x80
	s_addc_u32 s25, s27, 0
	s_mov_b32 m0, s44
	s_barrier
	ds_read_b128 v[16:19], v231 offset:49152
	ds_read_b128 v[24:27], v231 offset:51200
	ds_read_b128 v[20:23], v232 offset:49152
	ds_read_b128 v[28:31], v232 offset:51200
	ds_read_b128 v[32:35], v231 offset:53248
	ds_read_b128 v[40:43], v231 offset:55296
	ds_read_b128 v[36:39], v232 offset:53248
	ds_read_b128 v[44:47], v232 offset:55296
	s_nop 0
	global_load_lds_dwordx4 v198, s[24:25]
	s_mov_b32 m0, s45
	s_nop 0
	global_load_lds_dwordx4 v200, s[24:25]
	s_nop 0
	s_barrier
	s_waitcnt lgkmcnt(0)
	s_setprio 1
	s_waitcnt lgkmcnt(0)
	v_mfma_scale_f32_16x16x128_f8f6f4 v[124:127], v[0:7], v[16:23], v[124:127], v212, v212 op_sel_hi:[0,0,0]
	v_mfma_scale_f32_16x16x128_f8f6f4 v[116:119], v[8:15], v[16:23], v[116:119], v212, v212 op_sel_hi:[0,0,0]
	v_mfma_scale_f32_16x16x128_f8f6f4 v[108:111], v[0:7], v[24:31], v[108:111], v212, v212 op_sel_hi:[0,0,0]
	v_mfma_scale_f32_16x16x128_f8f6f4 v[100:103], v[8:15], v[24:31], v[100:103], v212, v212 op_sel_hi:[0,0,0]
	v_mfma_scale_f32_16x16x128_f8f6f4 v[92:95], v[0:7], v[32:39], v[92:95], v212, v212 op_sel_hi:[0,0,0]
	v_mfma_scale_f32_16x16x128_f8f6f4 v[84:87], v[8:15], v[32:39], v[84:87], v212, v212 op_sel_hi:[0,0,0]
	v_mfma_scale_f32_16x16x128_f8f6f4 v[76:79], v[0:7], v[40:47], v[76:79], v212, v212 op_sel_hi:[0,0,0]
	v_mfma_scale_f32_16x16x128_f8f6f4 v[68:71], v[8:15], v[40:47], v[68:71], v212, v212 op_sel_hi:[0,0,0]
	s_setprio 0
	s_barrier
	s_add_u32 s22, s22, 0x20080
	s_addc_u32 s23, s23, 0
	s_mov_b32 m0, s46
	s_nop 0
	global_load_lds_dwordx4 v194, s[22:23]
	s_mov_b32 m0, s47
	s_nop 0
	global_load_lds_dwordx4 v192, s[22:23]
	s_waitcnt vmcnt(6)
	s_barrier
	s_setprio 1
	v_mfma_scale_f32_16x16x128_f8f6f4 v[120:123], v[48:55], v[16:23], v[120:123], v212, v212 op_sel_hi:[0,0,0]
	v_mfma_scale_f32_16x16x128_f8f6f4 v[112:115], v[56:63], v[16:23], v[112:115], v212, v212 op_sel_hi:[0,0,0]
	v_mfma_scale_f32_16x16x128_f8f6f4 v[104:107], v[48:55], v[24:31], v[104:107], v212, v212 op_sel_hi:[0,0,0]
	v_mfma_scale_f32_16x16x128_f8f6f4 v[96:99], v[56:63], v[24:31], v[96:99], v212, v212 op_sel_hi:[0,0,0]
	v_mfma_scale_f32_16x16x128_f8f6f4 v[88:91], v[48:55], v[32:39], v[88:91], v212, v212 op_sel_hi:[0,0,0]
	v_mfma_scale_f32_16x16x128_f8f6f4 v[80:83], v[56:63], v[32:39], v[80:83], v212, v212 op_sel_hi:[0,0,0]
	v_mfma_scale_f32_16x16x128_f8f6f4 v[72:75], v[48:55], v[40:47], v[72:75], v212, v212 op_sel_hi:[0,0,0]
	v_mfma_scale_f32_16x16x128_f8f6f4 v[64:67], v[56:63], v[40:47], v[64:67], v212, v212 op_sel_hi:[0,0,0]
	s_setprio 0
	s_add_i32 s51, s51, 2
	s_add_u32 s4, s4, 0x100
	s_addc_u32 s5, s5, 0
	s_cmp_gt_u32 s51, 5
	s_barrier
	s_cbranch_scc1 .LBB0_1990

.LBB0_2052:
	s_or_b64 exec, exec, s[0:1]
	v_readlane_b32 s2, v242, 37
	v_mov_b32_e32 v172, v208
	v_readlane_b32 s3, v242, 38
	s_waitcnt lgkmcnt(0)
	s_barrier
	s_nop 0
	s_mov_b32 s0, 0
	s_and_b64 vcc, exec, s[2:3]
	v_readfirstlane_b32 s34, v172
	s_cbranch_vccnz .LBB0_2064
	v_lshlrev_b32_e32 v0, 4, v172
	v_add_u32_e32 v1, 0x2000, v0
	v_ashrrev_i32_e32 v2, 31, v1
	v_lshrrev_b32_e32 v2, 22, v2
	v_add_u32_e32 v2, v1, v2
	v_ashrrev_i32_e32 v2, 10, v2
	v_mul_i32_i24_e32 v3, 0x400, v2
	v_sub_u32_e32 v1, v1, v3
	v_lshrrev_b32_e32 v3, 4, v1
	v_bitop3_b32 v1, v3, v1, 32 bitop3:0x6c
	v_ashrrev_i32_e32 v3, 31, v1
	v_lshrrev_b32_e32 v3, 26, v3
	v_add_u32_e32 v3, v1, v3
	v_lshlrev_b32_e32 v5, 3, v2
	v_readlane_b32 s2, v242, 1
	v_ashrrev_i32_e32 v4, 6, v3
	v_and_b32_e32 v5, -16, v5
	v_and_b32_e32 v3, 0xc0, v3
	v_readlane_b32 s3, v242, 2
	v_add_u32_e32 v5, v4, v5
	v_sub_u32_e32 v1, v1, v3
	v_mov_b32_e32 v3, 1
	s_load_dwordx2 s[6:7], s[2:3], s0 offset:0x108
	v_and_b32_e32 v4, 3, v4
	s_mov_b32 s0, 0x3fffe0
	v_lshrrev_b32_e32 v6, 2, v5
	v_lshlrev_b32_e32 v7, 1, v5
	v_lshlrev_b32_e32 v2, 5, v2
	v_ashrrev_i16_sdwa v1, v3, sext(v1) dst_sel:DWORD dst_unused:UNUSED_PAD src0_sel:DWORD src1_sel:BYTE_0
	v_and_or_b32 v4, v5, s0, v4
	v_and_b32_e32 v6, 4, v6
	v_and_b32_e32 v7, 24, v7
	v_and_b32_e32 v2, 32, v2
	v_bfe_i32 v1, v1, 0, 16
	v_or3_b32 v4, v4, v6, v7
	v_add_lshl_u32 v1, v2, v1, 1
	v_lshl_add_u32 v160, v4, 10, v1
	v_lshl_add_u32 v162, v5, 10, v1
	v_bfe_i32 v1, v172, 27, 1
	v_lshrrev_b32_e32 v1, 22, v1
	v_add_u32_e32 v1, v0, v1
	v_and_b32_e32 v1, 0xfffffc00, v1
	v_sub_u32_e32 v0, v0, v1
	v_lshrrev_b32_e32 v1, 4, v0
	v_ashrrev_i32_e32 v4, 31, v172
	v_bitop3_b32 v0, v1, v0, 32 bitop3:0x6c
	v_lshrrev_b32_e32 v4, 26, v4
	v_ashrrev_i32_e32 v1, 31, v0
	v_add_u32_e32 v4, v172, v4
	s_waitcnt lgkmcnt(0)
	s_add_u32 s35, s6, 0xbbff000
	v_lshrrev_b32_e32 v1, 26, v1
	v_ashrrev_i32_e32 v4, 6, v4
	s_addc_u32 s36, s7, 0
	v_add_u32_e32 v1, v0, v1
	v_lshlrev_b32_e32 v5, 3, v4
	s_add_u32 s37, s6, 0x1a7ff000
	v_ashrrev_i32_e32 v2, 6, v1
	v_and_b32_e32 v5, -16, v5
	v_readlane_b32 s2, v242, 0
	s_addc_u32 s38, s7, 0
	v_add_u32_e32 v5, v2, v5
	v_and_b32_e32 v2, 3, v2
	s_ashr_i32 s39, s2, 31
	v_and_or_b32 v2, v5, s0, v2
	s_lshr_b32 s0, s39, 29
	s_add_i32 s0, s2, s0
	s_ashr_i32 s12, s34, 6
	s_ashr_i32 s1, s0, 3
	s_and_b32 s0, s0, -8
	s_ashr_i32 s13, s34, 8
	s_lshl_b32 s10, s12, 10
	s_sub_i32 s0, s2, s0
	s_cmp_lt_i32 s0, 0
	s_movk_i32 s40, 0x89
	s_cselect_b32 s2, s40, 0x88
	s_mul_i32 s0, s2, s0
	s_add_i32 s0, s0, s1
	s_mul_hi_i32 s1, s0, 0x78787879
	s_lshr_b32 s2, s1, 31
	s_ashr_i32 s1, s1, 5
	s_add_i32 s2, s1, s2
	s_mul_i32 s1, s2, 0x44
	s_sub_i32 s0, s0, s1
	s_bfe_i32 s1, s0, 0x80000
	s_bfe_u32 s1, s1, 0x5000a
	s_add_i32 s1, s0, s1
	s_bfe_i32 s3, s1, 0x80000
	v_and_b32_e32 v1, 0xc0, v1
	s_sext_i32_i16 s3, s3
	v_sub_u32_e32 v0, v0, v1
	s_ashr_i32 s3, s3, 5
	v_lshrrev_b32_e32 v6, 2, v5
	v_lshlrev_b32_e32 v7, 1, v5
	v_lshlrev_b32_e32 v4, 5, v4
	v_ashrrev_i16_sdwa v0, v3, sext(v0) dst_sel:DWORD dst_unused:UNUSED_PAD src0_sel:DWORD src1_sel:BYTE_0
	s_lshl_b32 s3, s3, 3
	v_and_b32_e32 v6, 4, v6
	v_and_b32_e32 v7, 24, v7
	v_and_b32_e32 v4, 32, v4
	v_bfe_i32 v0, v0, 0, 16
	s_sub_i32 s4, 17, s3
	s_and_b32 s1, s1, 0xffe0
	v_or3_b32 v2, v2, v6, v7
	v_add_lshl_u32 v0, v4, v0, 1
	s_min_u32 s4, s4, 8
	s_sub_i32 s5, s0, s1
	v_lshl_add_u32 v164, v2, 10, v0
	s_sext_i32_i8 s0, s5
	v_cvt_f32_ubyte0_e32 v2, s4
	v_cvt_f32_i32_e32 v1, s0
	v_rcp_iflag_f32_e32 v3, v2
	v_lshl_add_u32 v166, v5, 10, v0
	s_ashr_i32 s0, s0, 30
	s_or_b32 s8, s0, 1
	v_mul_f32_e32 v0, v1, v3
	v_trunc_f32_e32 v0, v0
	v_fma_f32 v1, -v0, v2, v1
	v_cvt_i32_f32_e32 v0, v0
	v_cmp_ge_f32_e64 s[0:1], |v1|, v2
	s_and_b64 s[0:1], s[0:1], exec
	s_cselect_b32 s0, s8, 0
	v_readfirstlane_b32 s1, v0
	s_add_i32 s0, s1, s0
	s_sext_i32_i8 s1, s0
	s_mul_i32 s0, s0, s4
	s_sub_i32 s0, s5, s0
	s_mul_i32 s4, s2, 17
	s_sext_i32_i8 s0, s0
	s_add_i32 s3, s3, s4
	s_add_i32 s22, s3, s0
	s_lshl_b32 s0, s2, 2
	s_add_i32 s0, s0, s1
	s_ashr_i32 s23, s22, 31
	s_ashr_i32 s1, s0, 31
	s_lshl_b64 s[4:5], s[22:23], 18
	s_lshl_b64 s[2:3], s[0:1], 18
	s_add_u32 s2, s35, s2
	s_addc_u32 s3, s36, s3
	s_add_i32 s1, s10, 0
	s_add_i32 s23, s1, 0x10000
	s_add_i32 s41, s1, 0x12000
	v_mov_b32_e32 v173, 0x7f
	s_mov_b64 s[8:9], s[2:3]
	s_mov_b32 m0, s23
	s_add_u32 s4, s37, s4
	s_addc_u32 s5, s38, s5
	global_load_lds_dwordx4 v164, s[8:9]
	s_mov_b32 m0, s41
	s_add_i32 s42, s1, 0x2000
	global_load_lds_dwordx4 v160, s[8:9]
	s_mov_b64 s[8:9], s[4:5]
	s_mov_b32 m0, s1
	v_mov_b32_e32 v165, 0
	global_load_lds_dwordx4 v166, s[8:9]
	s_mov_b32 m0, s42
	s_mov_b32 s47, 0
	global_load_lds_dwordx4 v162, s[8:9]
	s_add_u32 s8, s2, 0x20000
	s_addc_u32 s9, s3, 0
	s_add_i32 s43, s1, 0x14000
	s_mov_b32 m0, s43
	s_add_i32 s44, s1, 0x16000
	v_mov_b32_e32 v161, v165
	global_load_lds_dwordx4 v164, s[8:9]
	s_mov_b32 m0, s44
	v_mov_b32_e32 v167, v165
	global_load_lds_dwordx4 v160, s[8:9]
	s_add_u32 s8, s4, 0x20000
	s_addc_u32 s9, s5, 0
	s_add_i32 s45, s1, 0x4000
	s_mov_b32 m0, s45
	s_add_i32 s46, s1, 0x6000
	s_cmp_lg_u32 s13, 1
	global_load_lds_dwordx4 v166, s[8:9]
	s_mov_b32 m0, s46
	v_mov_b32_e32 v163, v165
	global_load_lds_dwordx4 v162, s[8:9]
	s_cbranch_scc1 .LBB0_2055
	s_barrier

.LBB0_2059:
	s_add_u32 s24, s28, 0x100
	ds_read_b128 v[0:3], v174
	ds_read_b128 v[4:7], v175
	ds_read_b128 v[8:11], v182
	ds_read_b128 v[12:15], v183
	s_addc_u32 s25, s29, 0
	s_and_b32 s57, s24, 0x300
	s_add_u32 s56, s2, s57
	s_addc_u32 s58, s3, 0
	s_cmp_eq_u32 s33, 4
	s_cselect_b64 s[30:31], -1, 0
	s_and_b64 s[26:27], s[30:31], exec
	s_cselect_b32 s27, s13, s58
	s_cselect_b32 s26, s19, s56
	s_cselect_b32 s56, 0, 0
	s_cselect_b32 s57, 0, s57
	s_add_u32 s28, s4, s28
	s_addc_u32 s29, s5, s29
	s_add_u32 s28, s28, 0x20080
	s_addc_u32 s29, s29, 0
	ds_read_b128 v[194:197], v190
	ds_read_b128 v[210:213], v190 offset:2048
	ds_read_b128 v[198:201], v191
	ds_read_b128 v[214:217], v191 offset:2048
	ds_read_b128 v[218:221], v190 offset:4096
	ds_read_b128 v[226:229], v190 offset:6144
	ds_read_b128 v[222:225], v191 offset:4096
	ds_read_b128 v[230:233], v191 offset:6144
	s_add_i32 m0, s1, 0xc000
	s_nop 0
	global_load_lds_dwordx4 v166, s[28:29]
	s_add_i32 m0, s1, 0xe000
	s_nop 0
	global_load_lds_dwordx4 v162, s[28:29]
	s_waitcnt lgkmcnt(8)
	s_nop 0
	s_barrier
	s_waitcnt lgkmcnt(0)
	s_setprio 1
	s_waitcnt lgkmcnt(0)
	v_mfma_scale_f32_16x16x128_f8f6f4 v[156:159], v[0:7], v[194:201], v[156:159], v173, v173 op_sel_hi:[0,0,0]
	v_mfma_scale_f32_16x16x128_f8f6f4 v[152:155], v[8:15], v[194:201], v[152:155], v173, v173 op_sel_hi:[0,0,0]
	v_mfma_scale_f32_16x16x128_f8f6f4 v[140:143], v[0:7], v[210:217], v[140:143], v173, v173 op_sel_hi:[0,0,0]
	v_mfma_scale_f32_16x16x128_f8f6f4 v[136:139], v[8:15], v[210:217], v[136:139], v173, v173 op_sel_hi:[0,0,0]
	v_mfma_scale_f32_16x16x128_f8f6f4 v[124:127], v[0:7], v[218:225], v[124:127], v173, v173 op_sel_hi:[0,0,0]
	v_mfma_scale_f32_16x16x128_f8f6f4 v[120:123], v[8:15], v[218:225], v[120:123], v173, v173 op_sel_hi:[0,0,0]
	v_mfma_scale_f32_16x16x128_f8f6f4 v[108:111], v[0:7], v[226:233], v[108:111], v173, v173 op_sel_hi:[0,0,0]
	v_mfma_scale_f32_16x16x128_f8f6f4 v[104:107], v[8:15], v[226:233], v[104:107], v173, v173 op_sel_hi:[0,0,0]
	s_setprio 0
	s_barrier
	s_mov_b64 s[28:29], s[26:27]
	s_mov_b32 m0, s23
	ds_read_b128 v[16:19], v176
	ds_read_b128 v[20:23], v177
	ds_read_b128 v[24:27], v184
	ds_read_b128 v[28:31], v185
	s_nop 0
	global_load_lds_dwordx4 v164, s[28:29]
	s_mov_b32 m0, s41
	s_nop 0
	global_load_lds_dwordx4 v160, s[28:29]
	s_nop 0
	s_barrier
	s_waitcnt lgkmcnt(0)
	s_setprio 1
	s_waitcnt lgkmcnt(0)
	v_mfma_scale_f32_16x16x128_f8f6f4 v[148:151], v[16:23], v[194:201], v[148:151], v173, v173 op_sel_hi:[0,0,0]
	v_mfma_scale_f32_16x16x128_f8f6f4 v[144:147], v[24:31], v[194:201], v[144:147], v173, v173 op_sel_hi:[0,0,0]
	v_mfma_scale_f32_16x16x128_f8f6f4 v[132:135], v[16:23], v[210:217], v[132:135], v173, v173 op_sel_hi:[0,0,0]
	v_mfma_scale_f32_16x16x128_f8f6f4 v[128:131], v[24:31], v[210:217], v[128:131], v173, v173 op_sel_hi:[0,0,0]
	v_mfma_scale_f32_16x16x128_f8f6f4 v[116:119], v[16:23], v[218:225], v[116:119], v173, v173 op_sel_hi:[0,0,0]
	v_mfma_scale_f32_16x16x128_f8f6f4 v[112:115], v[24:31], v[218:225], v[112:115], v173, v173 op_sel_hi:[0,0,0]
	v_mfma_scale_f32_16x16x128_f8f6f4 v[100:103], v[16:23], v[226:233], v[100:103], v173, v173 op_sel_hi:[0,0,0]
	v_mfma_scale_f32_16x16x128_f8f6f4 v[96:99], v[24:31], v[226:233], v[96:99], v173, v173 op_sel_hi:[0,0,0]
	s_setprio 0
	s_and_b64 s[28:29], s[16:17], s[30:31]
	s_and_b64 s[28:29], s[28:29], exec
	s_cselect_b32 s28, s6, s4
	s_cselect_b32 s29, s7, s5
	s_add_u32 s28, s28, s57
	s_addc_u32 s29, s29, s56
	s_mov_b64 s[30:31], s[28:29]
	s_mov_b32 m0, s1
	s_barrier
	ds_read_b128 v[194:197], v190 offset:16384
	ds_read_b128 v[210:213], v190 offset:18432
	ds_read_b128 v[198:201], v191 offset:16384
	ds_read_b128 v[214:217], v191 offset:18432
	ds_read_b128 v[218:221], v190 offset:20480
	ds_read_b128 v[226:229], v190 offset:22528
	ds_read_b128 v[222:225], v191 offset:20480
	ds_read_b128 v[230:233], v191 offset:22528
	s_nop 0
	global_load_lds_dwordx4 v166, s[30:31]
	s_mov_b32 m0, s42
	s_nop 0
	global_load_lds_dwordx4 v162, s[30:31]
	s_nop 0
	s_barrier
	s_waitcnt lgkmcnt(0)
	s_setprio 1
	s_waitcnt lgkmcnt(0)
	v_mfma_scale_f32_16x16x128_f8f6f4 v[92:95], v[0:7], v[194:201], v[92:95], v173, v173 op_sel_hi:[0,0,0]
	v_mfma_scale_f32_16x16x128_f8f6f4 v[88:91], v[8:15], v[194:201], v[88:91], v173, v173 op_sel_hi:[0,0,0]
	v_mfma_scale_f32_16x16x128_f8f6f4 v[76:79], v[0:7], v[210:217], v[76:79], v173, v173 op_sel_hi:[0,0,0]
	v_mfma_scale_f32_16x16x128_f8f6f4 v[72:75], v[8:15], v[210:217], v[72:75], v173, v173 op_sel_hi:[0,0,0]
	v_mfma_scale_f32_16x16x128_f8f6f4 v[60:63], v[0:7], v[218:225], v[60:63], v173, v173 op_sel_hi:[0,0,0]
	v_mfma_scale_f32_16x16x128_f8f6f4 v[56:59], v[8:15], v[218:225], v[56:59], v173, v173 op_sel_hi:[0,0,0]
	v_mfma_scale_f32_16x16x128_f8f6f4 v[44:47], v[0:7], v[226:233], v[44:47], v173, v173 op_sel_hi:[0,0,0]
	v_mfma_scale_f32_16x16x128_f8f6f4 v[40:43], v[8:15], v[226:233], v[40:43], v173, v173 op_sel_hi:[0,0,0]
	s_setprio 0
	s_barrier
	s_add_u32 s30, s26, 0x20000
	s_addc_u32 s31, s27, 0
	s_mov_b32 m0, s43
	s_nop 0
	global_load_lds_dwordx4 v164, s[30:31]
	s_mov_b32 m0, s44
	s_nop 0
	global_load_lds_dwordx4 v160, s[30:31]
	s_waitcnt vmcnt(6)
	s_barrier
	s_setprio 1
	v_mfma_scale_f32_16x16x128_f8f6f4 v[84:87], v[16:23], v[194:201], v[84:87], v173, v173 op_sel_hi:[0,0,0]
	v_mfma_scale_f32_16x16x128_f8f6f4 v[80:83], v[24:31], v[194:201], v[80:83], v173, v173 op_sel_hi:[0,0,0]
	v_mfma_scale_f32_16x16x128_f8f6f4 v[68:71], v[16:23], v[210:217], v[68:71], v173, v173 op_sel_hi:[0,0,0]
	v_mfma_scale_f32_16x16x128_f8f6f4 v[64:67], v[24:31], v[210:217], v[64:67], v173, v173 op_sel_hi:[0,0,0]
	v_mfma_scale_f32_16x16x128_f8f6f4 v[52:55], v[16:23], v[218:225], v[52:55], v173, v173 op_sel_hi:[0,0,0]
	v_mfma_scale_f32_16x16x128_f8f6f4 v[48:51], v[24:31], v[218:225], v[48:51], v173, v173 op_sel_hi:[0,0,0]
	v_mfma_scale_f32_16x16x128_f8f6f4 v[36:39], v[16:23], v[226:233], v[36:39], v173, v173 op_sel_hi:[0,0,0]
	v_mfma_scale_f32_16x16x128_f8f6f4 v[32:35], v[24:31], v[226:233], v[32:35], v173, v173 op_sel_hi:[0,0,0]
	s_setprio 0
	s_barrier
	ds_read_b128 v[0:3], v178
	ds_read_b128 v[4:7], v179
	ds_read_b128 v[8:11], v186
	ds_read_b128 v[12:15], v187
	s_add_u32 s30, s28, 0x20000
	s_addc_u32 s31, s29, 0
	s_mov_b32 m0, s45
	ds_read_b128 v[16:19], v190 offset:32768
	ds_read_b128 v[24:27], v190 offset:34816
	ds_read_b128 v[20:23], v191 offset:32768
	ds_read_b128 v[28:31], v191 offset:34816
	ds_read_b128 v[194:197], v190 offset:36864
	ds_read_b128 v[210:213], v190 offset:38912
	ds_read_b128 v[198:201], v191 offset:36864
	ds_read_b128 v[214:217], v191 offset:38912
	s_nop 0
	global_load_lds_dwordx4 v166, s[30:31]
	s_mov_b32 m0, s46
	s_nop 0
	global_load_lds_dwordx4 v162, s[30:31]
	s_waitcnt lgkmcnt(8)
	s_barrier
	s_waitcnt lgkmcnt(0)
	s_setprio 1
	s_waitcnt lgkmcnt(0)
	v_mfma_scale_f32_16x16x128_f8f6f4 v[156:159], v[0:7], v[16:23], v[156:159], v173, v173 op_sel_hi:[0,0,0]
	v_mfma_scale_f32_16x16x128_f8f6f4 v[152:155], v[8:15], v[16:23], v[152:155], v173, v173 op_sel_hi:[0,0,0]
	v_mfma_scale_f32_16x16x128_f8f6f4 v[140:143], v[0:7], v[24:31], v[140:143], v173, v173 op_sel_hi:[0,0,0]
	v_mfma_scale_f32_16x16x128_f8f6f4 v[136:139], v[8:15], v[24:31], v[136:139], v173, v173 op_sel_hi:[0,0,0]
	v_mfma_scale_f32_16x16x128_f8f6f4 v[124:127], v[0:7], v[194:201], v[124:127], v173, v173 op_sel_hi:[0,0,0]
	v_mfma_scale_f32_16x16x128_f8f6f4 v[120:123], v[8:15], v[194:201], v[120:123], v173, v173 op_sel_hi:[0,0,0]
	v_mfma_scale_f32_16x16x128_f8f6f4 v[108:111], v[0:7], v[210:217], v[108:111], v173, v173 op_sel_hi:[0,0,0]
	v_mfma_scale_f32_16x16x128_f8f6f4 v[104:107], v[8:15], v[210:217], v[104:107], v173, v173 op_sel_hi:[0,0,0]
	s_setprio 0
	s_barrier
	s_add_u32 s30, s26, 0x80
	s_addc_u32 s31, s27, 0
	s_mov_b32 m0, s48
	ds_read_b128 v[218:221], v180
	ds_read_b128 v[222:225], v181
	ds_read_b128 v[226:229], v188
	ds_read_b128 v[230:233], v189
	s_nop 0
	global_load_lds_dwordx4 v164, s[30:31]
	s_mov_b32 m0, s49
	s_nop 0
	global_load_lds_dwordx4 v160, s[30:31]
	s_nop 0
	s_barrier
	s_waitcnt lgkmcnt(0)
	s_setprio 1
	s_waitcnt lgkmcnt(0)
	v_mfma_scale_f32_16x16x128_f8f6f4 v[148:151], v[218:225], v[16:23], v[148:151], v173, v173 op_sel_hi:[0,0,0]
	v_mfma_scale_f32_16x16x128_f8f6f4 v[144:147], v[226:233], v[16:23], v[144:147], v173, v173 op_sel_hi:[0,0,0]
	v_mfma_scale_f32_16x16x128_f8f6f4 v[132:135], v[218:225], v[24:31], v[132:135], v173, v173 op_sel_hi:[0,0,0]
	v_mfma_scale_f32_16x16x128_f8f6f4 v[128:131], v[226:233], v[24:31], v[128:131], v173, v173 op_sel_hi:[0,0,0]
	v_mfma_scale_f32_16x16x128_f8f6f4 v[116:119], v[218:225], v[194:201], v[116:119], v173, v173 op_sel_hi:[0,0,0]
	v_mfma_scale_f32_16x16x128_f8f6f4 v[112:115], v[226:233], v[194:201], v[112:115], v173, v173 op_sel_hi:[0,0,0]
	v_mfma_scale_f32_16x16x128_f8f6f4 v[100:103], v[218:225], v[210:217], v[100:103], v173, v173 op_sel_hi:[0,0,0]
	v_mfma_scale_f32_16x16x128_f8f6f4 v[96:99], v[226:233], v[210:217], v[96:99], v173, v173 op_sel_hi:[0,0,0]
	s_setprio 0
	s_add_u32 s28, s28, 0x80
	s_addc_u32 s29, s29, 0
	s_mov_b32 m0, s50
	s_barrier
	ds_read_b128 v[16:19], v190 offset:49152
	ds_read_b128 v[24:27], v190 offset:51200
	ds_read_b128 v[20:23], v191 offset:49152
	ds_read_b128 v[28:31], v191 offset:51200
	ds_read_b128 v[194:197], v190 offset:53248
	ds_read_b128 v[210:213], v190 offset:55296
	ds_read_b128 v[198:201], v191 offset:53248
	ds_read_b128 v[214:217], v191 offset:55296
	s_nop 0
	global_load_lds_dwordx4 v166, s[28:29]
	s_mov_b32 m0, s51
	s_nop 0
	global_load_lds_dwordx4 v162, s[28:29]
	s_nop 0
	s_barrier
	s_waitcnt lgkmcnt(0)
	s_setprio 1
	s_waitcnt lgkmcnt(0)
	v_mfma_scale_f32_16x16x128_f8f6f4 v[92:95], v[0:7], v[16:23], v[92:95], v173, v173 op_sel_hi:[0,0,0]
	v_mfma_scale_f32_16x16x128_f8f6f4 v[88:91], v[8:15], v[16:23], v[88:91], v173, v173 op_sel_hi:[0,0,0]
	v_mfma_scale_f32_16x16x128_f8f6f4 v[76:79], v[0:7], v[24:31], v[76:79], v173, v173 op_sel_hi:[0,0,0]
	v_mfma_scale_f32_16x16x128_f8f6f4 v[72:75], v[8:15], v[24:31], v[72:75], v173, v173 op_sel_hi:[0,0,0]
	v_mfma_scale_f32_16x16x128_f8f6f4 v[60:63], v[0:7], v[194:201], v[60:63], v173, v173 op_sel_hi:[0,0,0]
	v_mfma_scale_f32_16x16x128_f8f6f4 v[56:59], v[8:15], v[194:201], v[56:59], v173, v173 op_sel_hi:[0,0,0]
	v_mfma_scale_f32_16x16x128_f8f6f4 v[44:47], v[0:7], v[210:217], v[44:47], v173, v173 op_sel_hi:[0,0,0]
	v_mfma_scale_f32_16x16x128_f8f6f4 v[40:43], v[8:15], v[210:217], v[40:43], v173, v173 op_sel_hi:[0,0,0]
	s_setprio 0
	s_barrier
	s_add_u32 s26, s26, 0x20080
	s_addc_u32 s27, s27, 0
	s_mov_b32 m0, s52
	s_nop 0
	global_load_lds_dwordx4 v164, s[26:27]
	s_mov_b32 m0, s53
	s_nop 0
	global_load_lds_dwordx4 v160, s[26:27]
	s_waitcnt vmcnt(6)
	s_barrier
	s_setprio 1
	v_mfma_scale_f32_16x16x128_f8f6f4 v[84:87], v[218:225], v[16:23], v[84:87], v173, v173 op_sel_hi:[0,0,0]
	v_mfma_scale_f32_16x16x128_f8f6f4 v[80:83], v[226:233], v[16:23], v[80:83], v173, v173 op_sel_hi:[0,0,0]
	v_mfma_scale_f32_16x16x128_f8f6f4 v[68:71], v[218:225], v[24:31], v[68:71], v173, v173 op_sel_hi:[0,0,0]
	v_mfma_scale_f32_16x16x128_f8f6f4 v[64:67], v[226:233], v[24:31], v[64:67], v173, v173 op_sel_hi:[0,0,0]
	v_mfma_scale_f32_16x16x128_f8f6f4 v[52:55], v[218:225], v[194:201], v[52:55], v173, v173 op_sel_hi:[0,0,0]
	v_mfma_scale_f32_16x16x128_f8f6f4 v[48:51], v[226:233], v[194:201], v[48:51], v173, v173 op_sel_hi:[0,0,0]
	v_mfma_scale_f32_16x16x128_f8f6f4 v[36:39], v[218:225], v[210:217], v[36:39], v173, v173 op_sel_hi:[0,0,0]
	v_mfma_scale_f32_16x16x128_f8f6f4 v[32:35], v[226:233], v[210:217], v[32:35], v173, v173 op_sel_hi:[0,0,0]
	s_setprio 0
	s_add_i32 s33, s33, 2
	s_cmp_gt_u32 s33, 5
	s_mov_b64 s[28:29], s[24:25]
	s_barrier
	s_cbranch_scc0 .LBB0_2059
	v_mov_b32_e32 v0, v172
	s_ashr_i32 s2, s0, 31
	v_ashrrev_i32_e32 v1, 2, v0
	v_and_b32_e32 v1, 0xffffffc0, v1
	v_lshl_add_u32 v1, s22, 8, v1
	v_and_or_b32 v6, v0, 15, v1
	v_ashrrev_i32_e32 v7, 31, v6
	v_lshl_add_u64 v[2:3], v[6:7], 2, s[8:9]
	global_load_dword v14, v[2:3], off
	global_load_dword v194, v[2:3], off offset:64
	global_load_dword v195, v[2:3], off offset:128
	global_load_dword v196, v[2:3], off offset:192
	global_load_dword v197, v[2:3], off offset:512
	global_load_dword v198, v[2:3], off offset:576
	global_load_dword v199, v[2:3], off offset:640
	global_load_dword v200, v[2:3], off offset:704
	s_lshr_b32 s2, s2, 30
	s_add_i32 s2, s0, s2
	v_lshrrev_b32_e32 v0, 1, v0
	s_and_b32 s2, s2, 0xfffffc
	v_and_b32_e32 v0, 0x78, v0
	s_sub_i32 s0, s0, s2
	v_lshl_or_b32 v4, s0, 8, v0
	v_lshlrev_b64 v[0:1], 10, v[6:7]
	v_mov_b32_e32 v8, 0
	v_mov_b32_e32 v9, 0
	v_mov_b32_e32 v10, 0
	v_mov_b32_e32 v11, 0
	v_ashrrev_i32_e32 v5, 31, v4
	v_or_b32_e32 v12, 16, v6
	v_lshl_add_u64 v[0:1], s[10:11], 0, v[0:1]
	v_ashrrev_i32_e32 v13, 31, v12
	v_lshl_add_u64 v[0:1], v[0:1], 0, v[4:5]
	s_mov_b32 s0, 0x20000
	s_mov_b64 s[2:3], 0x20000
	s_mov_b64 s[4:5], s[6:7]
	s_mov_b64 s[6:7], 0x2c000
	s_mov_b32 s13, 0x2c000
	s_mov_b32 s22, s12
	s_waitcnt vmcnt(0)
	v_mul_f32_e32 v7, 0x3d000000, v14
	v_mul_f32_e32 v14, 0x42000000, v7
	v_pk_mul_f32 v[18:19], v[156:157], v[14:15] op_sel_hi:[1,0]
	v_pk_mul_f32 v[22:23], v[152:153], v[14:15] op_sel_hi:[1,0]
	v_pk_mul_f32 v[16:17], v[158:159], v[14:15] op_sel_hi:[1,0]
	v_pk_mul_f32 v[20:21], v[154:155], v[14:15] op_sel_hi:[1,0]
	v_pk_mul_f32 v[24:25], v[150:151], v[14:15] op_sel_hi:[1,0]
	v_pk_mul_f32 v[26:27], v[148:149], v[14:15] op_sel_hi:[1,0]
	v_pk_mul_f32 v[28:29], v[146:147], v[14:15] op_sel_hi:[1,0]
	v_pk_mul_f32 v[14:15], v[144:145], v[14:15] op_sel_hi:[1,0]
	v_med3_f32 v7, v18, s55, v192
	v_med3_f32 v18, v22, s55, v192
	v_med3_f32 v19, v19, s55, v192
	v_med3_f32 v22, v23, s55, v192
	v_med3_f32 v23, v26, s55, v192
	v_med3_f32 v14, v14, s55, v192
	v_med3_f32 v26, v27, s55, v192
	v_med3_f32 v15, v15, s55, v192
	v_cvt_pk_fp8_f32 v8, v7, v19
	v_cvt_pk_fp8_f32 v9, v18, v22
	v_cvt_pk_fp8_f32 v10, v23, v26
	v_cvt_pk_fp8_f32 v11, v14, v15
	v_med3_f32 v16, v16, s55, v192
	v_med3_f32 v20, v20, s55, v192
	v_med3_f32 v17, v17, s55, v192
	v_med3_f32 v21, v21, s55, v192
	v_med3_f32 v24, v24, s55, v192
	v_med3_f32 v27, v28, s55, v192
	v_med3_f32 v25, v25, s55, v192
	v_med3_f32 v28, v29, s55, v192
	v_cvt_pk_fp8_f32 v8, v16, v17 op_sel:[0,0,1]
	v_cvt_pk_fp8_f32 v9, v20, v21 op_sel:[0,0,1]
	v_cvt_pk_fp8_f32 v10, v24, v25 op_sel:[0,0,1]
	v_cvt_pk_fp8_f32 v11, v27, v28 op_sel:[0,0,1]
	v_lshl_add_u64 v[14:15], v[12:13], 2, s[8:9]
	global_store_dwordx2 v[0:1], v[8:9], off
	global_store_dwordx2 v[0:1], v[10:11], off offset:128
	v_mov_b32_e32 v8, 0
	v_mov_b32_e32 v9, 0
	v_mov_b32_e32 v10, 0
	v_mov_b32_e32 v11, 0
	v_lshlrev_b64 v[12:13], 10, v[12:13]
	v_or_b32_e32 v14, 32, v6
	v_lshl_add_u64 v[12:13], s[10:11], 0, v[12:13]
	v_ashrrev_i32_e32 v15, 31, v14
	v_lshl_add_u64 v[12:13], v[12:13], 0, v[4:5]
	v_lshl_add_u64 v[16:17], v[14:15], 2, s[8:9]
	v_or_b32_e32 v6, 48, v6
	v_mul_f32_e32 v7, 0x3d000000, v194
	v_mul_f32_e32 v18, 0x42000000, v7
	v_pk_mul_f32 v[22:23], v[140:141], v[18:19] op_sel_hi:[1,0]
	v_pk_mul_f32 v[26:27], v[136:137], v[18:19] op_sel_hi:[1,0]
	v_pk_mul_f32 v[20:21], v[142:143], v[18:19] op_sel_hi:[1,0]
	v_pk_mul_f32 v[24:25], v[138:139], v[18:19] op_sel_hi:[1,0]
	v_pk_mul_f32 v[28:29], v[134:135], v[18:19] op_sel_hi:[1,0]
	v_pk_mul_f32 v[30:31], v[132:133], v[18:19] op_sel_hi:[1,0]
	v_pk_mul_f32 v[130:131], v[130:131], v[18:19] op_sel_hi:[1,0]
	v_pk_mul_f32 v[18:19], v[128:129], v[18:19] op_sel_hi:[1,0]
	v_med3_f32 v7, v22, s55, v192
	v_med3_f32 v22, v26, s55, v192
	v_med3_f32 v23, v23, s55, v192
	v_med3_f32 v26, v27, s55, v192
	v_med3_f32 v27, v30, s55, v192
	v_med3_f32 v18, v18, s55, v192
	v_med3_f32 v30, v31, s55, v192
	v_med3_f32 v19, v19, s55, v192
	v_cvt_pk_fp8_f32 v8, v7, v23
	v_cvt_pk_fp8_f32 v9, v22, v26
	v_cvt_pk_fp8_f32 v10, v27, v30
	v_cvt_pk_fp8_f32 v11, v18, v19
	v_med3_f32 v20, v20, s55, v192
	v_med3_f32 v24, v24, s55, v192
	v_med3_f32 v21, v21, s55, v192
	v_med3_f32 v25, v25, s55, v192
	v_med3_f32 v28, v28, s55, v192
	v_med3_f32 v31, v130, s55, v192
	v_med3_f32 v29, v29, s55, v192
	v_med3_f32 v128, v131, s55, v192
	v_cvt_pk_fp8_f32 v8, v20, v21 op_sel:[0,0,1]
	v_cvt_pk_fp8_f32 v9, v24, v25 op_sel:[0,0,1]
	v_cvt_pk_fp8_f32 v10, v28, v29 op_sel:[0,0,1]
	v_cvt_pk_fp8_f32 v11, v31, v128 op_sel:[0,0,1]
	global_store_dwordx2 v[12:13], v[8:9], off
	global_store_dwordx2 v[12:13], v[10:11], off offset:128
	v_mov_b32_e32 v8, 0
	v_mov_b32_e32 v9, 0
	v_mov_b32_e32 v10, 0
	v_mov_b32_e32 v11, 0
	v_lshlrev_b64 v[12:13], 10, v[14:15]
	v_lshl_add_u64 v[12:13], s[10:11], 0, v[12:13]
	v_ashrrev_i32_e32 v7, 31, v6
	v_lshl_add_u64 v[12:13], v[12:13], 0, v[4:5]
	v_lshl_add_u64 v[14:15], v[6:7], 2, s[8:9]
	v_lshlrev_b64 v[6:7], 10, v[6:7]
	v_lshl_add_u64 v[6:7], s[10:11], 0, v[6:7]
	v_lshl_add_u64 v[4:5], v[6:7], 0, v[4:5]
	v_mov_b32_e32 v6, 0
	v_mov_b32_e32 v7, 0
	v_mul_f32_e32 v16, 0x3d000000, v195
	v_mul_f32_e32 v16, 0x42000000, v16
	v_pk_mul_f32 v[20:21], v[124:125], v[16:17] op_sel_hi:[1,0]
	v_pk_mul_f32 v[24:25], v[120:121], v[16:17] op_sel_hi:[1,0]
	v_pk_mul_f32 v[18:19], v[126:127], v[16:17] op_sel_hi:[1,0]
	v_pk_mul_f32 v[22:23], v[122:123], v[16:17] op_sel_hi:[1,0]
	v_pk_mul_f32 v[26:27], v[118:119], v[16:17] op_sel_hi:[1,0]
	v_pk_mul_f32 v[28:29], v[116:117], v[16:17] op_sel_hi:[1,0]
	v_pk_mul_f32 v[30:31], v[114:115], v[16:17] op_sel_hi:[1,0]
	v_pk_mul_f32 v[16:17], v[112:113], v[16:17] op_sel_hi:[1,0]
	v_med3_f32 v20, v20, s55, v192
	v_med3_f32 v24, v24, s55, v192
	v_med3_f32 v21, v21, s55, v192
	v_med3_f32 v25, v25, s55, v192
	v_med3_f32 v28, v28, s55, v192
	v_med3_f32 v16, v16, s55, v192
	v_med3_f32 v29, v29, s55, v192
	v_med3_f32 v17, v17, s55, v192
	v_cvt_pk_fp8_f32 v8, v20, v21
	v_cvt_pk_fp8_f32 v9, v24, v25
	v_cvt_pk_fp8_f32 v10, v28, v29
	v_cvt_pk_fp8_f32 v11, v16, v17
	v_med3_f32 v18, v18, s55, v192
	v_med3_f32 v22, v22, s55, v192
	v_med3_f32 v19, v19, s55, v192
	v_med3_f32 v23, v23, s55, v192
	v_med3_f32 v26, v26, s55, v192
	v_med3_f32 v30, v30, s55, v192
	v_med3_f32 v27, v27, s55, v192
	v_med3_f32 v31, v31, s55, v192
	v_cvt_pk_fp8_f32 v8, v18, v19 op_sel:[0,0,1]
	v_cvt_pk_fp8_f32 v9, v22, v23 op_sel:[0,0,1]
	v_cvt_pk_fp8_f32 v10, v26, v27 op_sel:[0,0,1]
	v_cvt_pk_fp8_f32 v11, v30, v31 op_sel:[0,0,1]
	global_store_dwordx2 v[12:13], v[8:9], off
	global_store_dwordx2 v[12:13], v[10:11], off offset:128
	v_mov_b32_e32 v8, 0
	v_mov_b32_e32 v9, 0
	v_mov_b32_e32 v10, 0
	v_mov_b32_e32 v11, 0
	v_mul_f32_e32 v12, 0x3d000000, v196
	v_mul_f32_e32 v12, 0x42000000, v12
	v_pk_mul_f32 v[16:17], v[108:109], v[12:13] op_sel_hi:[1,0]
	v_pk_mul_f32 v[20:21], v[104:105], v[12:13] op_sel_hi:[1,0]
	v_pk_mul_f32 v[14:15], v[110:111], v[12:13] op_sel_hi:[1,0]
	v_pk_mul_f32 v[18:19], v[106:107], v[12:13] op_sel_hi:[1,0]
	v_pk_mul_f32 v[22:23], v[102:103], v[12:13] op_sel_hi:[1,0]
	v_pk_mul_f32 v[24:25], v[100:101], v[12:13] op_sel_hi:[1,0]
	v_pk_mul_f32 v[26:27], v[98:99], v[12:13] op_sel_hi:[1,0]
	v_pk_mul_f32 v[12:13], v[96:97], v[12:13] op_sel_hi:[1,0]
	v_med3_f32 v16, v16, s55, v192
	v_med3_f32 v20, v20, s55, v192
	v_med3_f32 v17, v17, s55, v192
	v_med3_f32 v21, v21, s55, v192
	v_med3_f32 v24, v24, s55, v192
	v_med3_f32 v12, v12, s55, v192
	v_med3_f32 v25, v25, s55, v192
	v_med3_f32 v13, v13, s55, v192
	v_cvt_pk_fp8_f32 v8, v16, v17
	v_cvt_pk_fp8_f32 v9, v20, v21
	v_cvt_pk_fp8_f32 v10, v24, v25
	v_cvt_pk_fp8_f32 v11, v12, v13
	v_med3_f32 v14, v14, s55, v192
	v_med3_f32 v18, v18, s55, v192
	v_med3_f32 v15, v15, s55, v192
	v_med3_f32 v19, v19, s55, v192
	v_med3_f32 v22, v22, s55, v192
	v_med3_f32 v26, v26, s55, v192
	v_med3_f32 v23, v23, s55, v192
	v_med3_f32 v27, v27, s55, v192
	v_cvt_pk_fp8_f32 v8, v14, v15 op_sel:[0,0,1]
	v_cvt_pk_fp8_f32 v9, v18, v19 op_sel:[0,0,1]
	v_cvt_pk_fp8_f32 v10, v22, v23 op_sel:[0,0,1]
	v_cvt_pk_fp8_f32 v11, v26, v27 op_sel:[0,0,1]
	global_store_dwordx2 v[4:5], v[8:9], off
	global_store_dwordx2 v[4:5], v[10:11], off offset:128
	v_mov_b32_e32 v4, 0
	v_mov_b32_e32 v5, 0
	v_lshl_add_u64 v[8:9], v[0:1], 0, s[2:3]
	s_mov_b64 s[2:3], 0x24000
	v_mul_f32_e32 v10, 0x3d000000, v197
	v_mul_f32_e32 v10, 0x42000000, v10
	v_pk_mul_f32 v[14:15], v[92:93], v[10:11] op_sel_hi:[1,0]
	v_pk_mul_f32 v[18:19], v[88:89], v[10:11] op_sel_hi:[1,0]
	v_pk_mul_f32 v[12:13], v[94:95], v[10:11] op_sel_hi:[1,0]
	v_pk_mul_f32 v[16:17], v[90:91], v[10:11] op_sel_hi:[1,0]
	v_pk_mul_f32 v[20:21], v[86:87], v[10:11] op_sel_hi:[1,0]
	v_pk_mul_f32 v[22:23], v[84:85], v[10:11] op_sel_hi:[1,0]
	v_pk_mul_f32 v[24:25], v[82:83], v[10:11] op_sel_hi:[1,0]
	v_pk_mul_f32 v[10:11], v[80:81], v[10:11] op_sel_hi:[1,0]
	v_med3_f32 v14, v14, s55, v192
	v_med3_f32 v18, v18, s55, v192
	v_med3_f32 v15, v15, s55, v192
	v_med3_f32 v19, v19, s55, v192
	v_med3_f32 v22, v22, s55, v192
	v_med3_f32 v10, v10, s55, v192
	v_med3_f32 v23, v23, s55, v192
	v_med3_f32 v11, v11, s55, v192
	v_cvt_pk_fp8_f32 v4, v14, v15
	v_cvt_pk_fp8_f32 v5, v18, v19
	v_cvt_pk_fp8_f32 v6, v22, v23
	v_cvt_pk_fp8_f32 v7, v10, v11
	v_med3_f32 v12, v12, s55, v192
	v_med3_f32 v16, v16, s55, v192
	v_med3_f32 v13, v13, s55, v192
	v_med3_f32 v17, v17, s55, v192
	v_med3_f32 v20, v20, s55, v192
	v_med3_f32 v24, v24, s55, v192
	v_med3_f32 v21, v21, s55, v192
	v_med3_f32 v25, v25, s55, v192
	v_cvt_pk_fp8_f32 v4, v12, v13 op_sel:[0,0,1]
	v_cvt_pk_fp8_f32 v5, v16, v17 op_sel:[0,0,1]
	v_cvt_pk_fp8_f32 v6, v20, v21 op_sel:[0,0,1]
	v_cvt_pk_fp8_f32 v7, v24, v25 op_sel:[0,0,1]
	v_add_co_u32_e32 v10, vcc, s0, v0
	s_mov_b32 s0, 0x24000
	s_nop 0
	v_addc_co_u32_e32 v11, vcc, 0, v1, vcc
	global_store_dwordx2 v[10:11], v[4:5], off
	global_store_dwordx2 v[8:9], v[6:7], off offset:128
	v_mov_b32_e32 v4, 0
	v_mov_b32_e32 v5, 0
	v_mov_b32_e32 v6, 0
	v_mov_b32_e32 v7, 0
	v_lshl_add_u64 v[8:9], v[0:1], 0, s[2:3]
	s_mov_b64 s[2:3], 0x28000
	v_mul_f32_e32 v10, 0x3d000000, v198
	v_mul_f32_e32 v10, 0x42000000, v10
	v_pk_mul_f32 v[14:15], v[76:77], v[10:11] op_sel_hi:[1,0]
	v_pk_mul_f32 v[18:19], v[72:73], v[10:11] op_sel_hi:[1,0]
	v_pk_mul_f32 v[12:13], v[78:79], v[10:11] op_sel_hi:[1,0]
	v_pk_mul_f32 v[16:17], v[74:75], v[10:11] op_sel_hi:[1,0]
	v_pk_mul_f32 v[20:21], v[70:71], v[10:11] op_sel_hi:[1,0]
	v_pk_mul_f32 v[22:23], v[68:69], v[10:11] op_sel_hi:[1,0]
	v_pk_mul_f32 v[24:25], v[66:67], v[10:11] op_sel_hi:[1,0]
	v_pk_mul_f32 v[10:11], v[64:65], v[10:11] op_sel_hi:[1,0]
	v_med3_f32 v14, v14, s55, v192
	v_med3_f32 v18, v18, s55, v192
	v_med3_f32 v15, v15, s55, v192
	v_med3_f32 v19, v19, s55, v192
	v_med3_f32 v22, v22, s55, v192
	v_med3_f32 v10, v10, s55, v192
	v_med3_f32 v23, v23, s55, v192
	v_med3_f32 v11, v11, s55, v192
	v_cvt_pk_fp8_f32 v4, v14, v15
	v_cvt_pk_fp8_f32 v5, v18, v19
	v_cvt_pk_fp8_f32 v6, v22, v23
	v_cvt_pk_fp8_f32 v7, v10, v11
	v_med3_f32 v12, v12, s55, v192
	v_med3_f32 v16, v16, s55, v192
	v_med3_f32 v13, v13, s55, v192
	v_med3_f32 v17, v17, s55, v192
	v_med3_f32 v20, v20, s55, v192
	v_med3_f32 v24, v24, s55, v192
	v_med3_f32 v21, v21, s55, v192
	v_med3_f32 v25, v25, s55, v192
	v_cvt_pk_fp8_f32 v4, v12, v13 op_sel:[0,0,1]
	v_cvt_pk_fp8_f32 v5, v16, v17 op_sel:[0,0,1]
	v_cvt_pk_fp8_f32 v6, v20, v21 op_sel:[0,0,1]
	v_cvt_pk_fp8_f32 v7, v24, v25 op_sel:[0,0,1]
	v_add_co_u32_e32 v10, vcc, s0, v0
	s_mov_b32 s0, 0x28000
	s_nop 0
	v_addc_co_u32_e32 v11, vcc, 0, v1, vcc
	global_store_dwordx2 v[10:11], v[4:5], off
	global_store_dwordx2 v[8:9], v[6:7], off offset:128
	v_mov_b32_e32 v4, 0
	v_mov_b32_e32 v5, 0
	v_mov_b32_e32 v6, 0
	v_mov_b32_e32 v7, 0
	v_lshl_add_u64 v[8:9], v[0:1], 0, s[2:3]
	s_mov_b64 s[2:3], s[20:21]
	v_mul_f32_e32 v10, 0x3d000000, v199
	v_mul_f32_e32 v10, 0x42000000, v10
	v_pk_mul_f32 v[14:15], v[60:61], v[10:11] op_sel_hi:[1,0]
	v_pk_mul_f32 v[18:19], v[56:57], v[10:11] op_sel_hi:[1,0]
	v_pk_mul_f32 v[12:13], v[62:63], v[10:11] op_sel_hi:[1,0]
	v_pk_mul_f32 v[16:17], v[58:59], v[10:11] op_sel_hi:[1,0]
	v_pk_mul_f32 v[20:21], v[54:55], v[10:11] op_sel_hi:[1,0]
	v_pk_mul_f32 v[22:23], v[52:53], v[10:11] op_sel_hi:[1,0]
	v_pk_mul_f32 v[24:25], v[50:51], v[10:11] op_sel_hi:[1,0]
	v_pk_mul_f32 v[10:11], v[48:49], v[10:11] op_sel_hi:[1,0]
	v_med3_f32 v14, v14, s55, v192
	v_med3_f32 v18, v18, s55, v192
	v_med3_f32 v15, v15, s55, v192
	v_med3_f32 v19, v19, s55, v192
	v_med3_f32 v22, v22, s55, v192
	v_med3_f32 v10, v10, s55, v192
	v_med3_f32 v23, v23, s55, v192
	v_med3_f32 v11, v11, s55, v192
	v_cvt_pk_fp8_f32 v4, v14, v15
	v_cvt_pk_fp8_f32 v5, v18, v19
	v_cvt_pk_fp8_f32 v6, v22, v23
	v_cvt_pk_fp8_f32 v7, v10, v11
	v_med3_f32 v12, v12, s55, v192
	v_med3_f32 v16, v16, s55, v192
	v_med3_f32 v13, v13, s55, v192
	v_med3_f32 v17, v17, s55, v192
	v_med3_f32 v20, v20, s55, v192
	v_med3_f32 v24, v24, s55, v192
	v_med3_f32 v21, v21, s55, v192
	v_med3_f32 v25, v25, s55, v192
	v_cvt_pk_fp8_f32 v4, v12, v13 op_sel:[0,0,1]
	v_cvt_pk_fp8_f32 v5, v16, v17 op_sel:[0,0,1]
	v_cvt_pk_fp8_f32 v6, v20, v21 op_sel:[0,0,1]
	v_cvt_pk_fp8_f32 v7, v24, v25 op_sel:[0,0,1]
	v_add_co_u32_e32 v10, vcc, s0, v0
	s_mov_b32 s0, s18
	s_nop 0
	v_addc_co_u32_e32 v11, vcc, 0, v1, vcc
	global_store_dwordx2 v[10:11], v[4:5], off
	global_store_dwordx2 v[8:9], v[6:7], off offset:128
	v_mov_b32_e32 v2, 0
	v_mov_b32_e32 v3, 0
	v_mov_b32_e32 v4, 0
	v_mov_b32_e32 v5, 0
	v_lshl_add_u64 v[6:7], v[0:1], 0, s[6:7]
	v_add_co_u32_e64 v0, s[6:7], s13, v0
	s_and_b64 vcc, exec, s[14:15]
	s_nop 0
	v_addc_co_u32_e64 v1, s[6:7], 0, v1, s[6:7]
	v_mul_f32_e32 v8, 0x3d000000, v200
	v_mul_f32_e32 v8, 0x42000000, v8
	v_pk_mul_f32 v[12:13], v[44:45], v[8:9] op_sel_hi:[1,0]
	v_pk_mul_f32 v[16:17], v[40:41], v[8:9] op_sel_hi:[1,0]
	v_pk_mul_f32 v[10:11], v[46:47], v[8:9] op_sel_hi:[1,0]
	v_pk_mul_f32 v[14:15], v[42:43], v[8:9] op_sel_hi:[1,0]
	v_pk_mul_f32 v[18:19], v[38:39], v[8:9] op_sel_hi:[1,0]
	v_pk_mul_f32 v[20:21], v[36:37], v[8:9] op_sel_hi:[1,0]
	v_pk_mul_f32 v[22:23], v[34:35], v[8:9] op_sel_hi:[1,0]
	v_pk_mul_f32 v[8:9], v[32:33], v[8:9] op_sel_hi:[1,0]
	v_med3_f32 v12, v12, s55, v192
	v_med3_f32 v16, v16, s55, v192
	v_med3_f32 v13, v13, s55, v192
	v_med3_f32 v17, v17, s55, v192
	v_med3_f32 v20, v20, s55, v192
	v_med3_f32 v8, v8, s55, v192
	v_med3_f32 v21, v21, s55, v192
	v_med3_f32 v9, v9, s55, v192
	v_cvt_pk_fp8_f32 v2, v12, v13
	v_cvt_pk_fp8_f32 v3, v16, v17
	v_cvt_pk_fp8_f32 v4, v20, v21
	v_cvt_pk_fp8_f32 v5, v8, v9
	v_med3_f32 v10, v10, s55, v192
	v_med3_f32 v14, v14, s55, v192
	v_med3_f32 v11, v11, s55, v192
	v_med3_f32 v15, v15, s55, v192
	v_med3_f32 v18, v18, s55, v192
	v_med3_f32 v22, v22, s55, v192
	v_med3_f32 v19, v19, s55, v192
	v_med3_f32 v23, v23, s55, v192
	v_cvt_pk_fp8_f32 v2, v10, v11 op_sel:[0,0,1]
	v_cvt_pk_fp8_f32 v3, v14, v15 op_sel:[0,0,1]
	v_cvt_pk_fp8_f32 v4, v18, v19 op_sel:[0,0,1]
	v_cvt_pk_fp8_f32 v5, v22, v23 op_sel:[0,0,1]
	global_store_dwordx2 v[0:1], v[2:3], off
	global_store_dwordx2 v[6:7], v[4:5], off offset:128
	s_cbranch_vccz .LBB0_2056
	s_waitcnt vmcnt(0)
	v_readlane_b32 s54, v242, 34
	s_cmpk_gt_u32 s34, 0xff
	v_readlane_b32 s55, v242, 35
	s_cbranch_scc1 .LBB0_2063
	s_barrier

.LBB0_2282:
	s_or_b64 exec, exec, s[0:1]
	v_mov_b32_e32 v24, v208
	s_waitcnt lgkmcnt(0)
	s_barrier
	s_nop 0
	s_mov_b32 s0, 0
	v_readlane_b32 s2, v242, 25
	v_lshrrev_b32_e32 v0, 4, v24
	v_ashrrev_i32_e32 v22, 8, v24
	v_bfe_u32 v1, v0, 1, 1
	v_cmp_eq_u32_e32 vcc, v1, v22
	v_readlane_b32 s3, v242, 26
	s_nop 0
	v_cndmask_b32_e64 v7, 0, -1, vcc
	s_and_b64 vcc, exec, s[2:3]
	s_cbranch_vccnz .LBB0_2303
	v_readlane_b32 s2, v242, 1
	v_readlane_b32 s3, v242, 2
	s_load_dwordx4 s[4:7], s[2:3], s0 offset:0x60
	s_nop 0
	s_load_dwordx2 s[0:1], s[2:3], s0 offset:0x108
	v_lshrrev_b32_e32 v28, 2, v24
	v_add_u32_e32 v2, 2, v22
	v_and_b32_e32 v86, 15, v24
	v_and_b32_e32 v20, 48, v28
	v_readlane_b32 s2, v242, 20
	v_ashrrev_i32_e32 v3, 31, v2
	v_lshlrev_b64 v[4:5], 14, v[2:3]
	v_or3_b32 v1, v86, s2, v20
	v_lshlrev_b32_e32 v0, 13, v0
	s_waitcnt lgkmcnt(0)
	v_lshl_add_u64 v[4:5], s[4:5], 0, v[4:5]
	v_lshlrev_b32_e32 v10, 2, v1
	v_mov_b32_e32 v11, 0
	v_and_b32_e32 v0, 0x2000, v0
	v_readlane_b32 s2, v242, 22
	v_lshl_add_u64 v[4:5], v[4:5], 0, v[10:11]
	v_mov_b32_e32 v1, v11
	s_mov_b32 s4, s2
	v_lshl_add_u64 v[0:1], v[4:5], 0, v[0:1]
	s_movk_i32 s2, 0x1000
	v_add_co_u32_e32 v12, vcc, s2, v0
	s_mov_b32 s5, 0
	s_nop 0
	v_addc_co_u32_e32 v13, vcc, 0, v1, vcc
	global_load_dword v4, v[0:1], off
	global_load_dword v8, v[0:1], off offset:1024
	global_load_dword v5, v[0:1], off offset:2048
	global_load_dword v9, v[0:1], off offset:3072
	global_load_dword v6, v[12:13], off
	global_load_dword v26, v[12:13], off offset:1024
	global_load_dword v25, v[12:13], off offset:2048
	global_load_dword v27, v[12:13], off offset:3072
	v_lshlrev_b64 v[0:1], 10, v[2:3]
	v_lshl_add_u64 v[0:1], s[6:7], 0, v[0:1]
	v_bfe_u32 v23, v24, 4, 2
	v_lshl_add_u64 v[0:1], v[0:1], 0, s[4:5]
	v_lshlrev_b32_e32 v10, 2, v20
	v_lshl_add_u64 v[0:1], v[0:1], 0, v[10:11]
	v_lshlrev_b32_e32 v10, 4, v23
	v_lshl_add_u64 v[0:1], v[0:1], 0, v[10:11]
	global_load_dwordx4 v[0:3], v[0:1], off
	v_readlane_b32 s3, v242, 23
	s_mov_b32 s2, s4
	v_writelane_b32 v242, s2, 22
	v_lshlrev_b32_e32 v30, 2, v23
	s_nop 0
	v_writelane_b32 v242, s3, 23
	s_nop 0
	v_readlane_b32 s2, v242, 0
	s_ashr_i32 s2, s2, 2
	s_mul_hi_i32 s3, s2, 0x78787879
	s_lshr_b32 s4, s3, 31
	s_ashr_i32 s3, s3, 5
	s_add_i32 s4, s3, s4
	s_mul_i32 s3, s4, 0x44
	s_sub_i32 s2, s2, s3
	s_lshl_b32 s6, s2, 6
	s_cmp_gt_i32 s2, 3
	s_cbranch_scc0 .LBB0_2285
	s_lshl_b32 s2, s4, 12
	s_add_i32 s2, s6, s2
	s_add_i32 s5, s2, 0xffffff00
	s_cbranch_execz .LBB0_2286
	s_branch .LBB0_2287

.LBB0_2355:
	s_or_b64 exec, exec, s[0:1]
	s_waitcnt lgkmcnt(0)
	v_mov_b32_e32 v0, v208
	v_readlane_b32 s0, v242, 6
	s_barrier
	s_nop 0
	s_mov_b32 s2, 0
	s_nop 0
	v_add_u32_e32 v44, s0, v0
	s_mov_b32 s0, 0x20000
	v_cmp_gt_i32_e32 vcc, s0, v44
	s_and_saveexec_b64 s[0:1], vcc
	s_cbranch_execz .LBB0_2364
	v_readlane_b32 s4, v242, 1
	v_readlane_b32 s5, v242, 2
	s_load_dwordx2 s[8:9], s[4:5], s2 offset:0x108
	v_readlane_b32 s10, v242, 11
	v_mov_b32_e32 v33, 0
	s_mov_b64 s[2:3], 0
	s_mov_b32 s12, 0x1ffff
	s_waitcnt lgkmcnt(0)
	s_add_u32 s4, s8, 0x32af000
	s_addc_u32 s5, s9, 0
	s_add_u32 s6, s8, 0x240ff000
	s_addc_u32 s7, s9, 0
	s_add_u32 s8, s8, 0x284ff000
	s_addc_u32 s9, s9, 0
	s_lshl_b32 s13, s10, 9
	s_mov_b32 s16, 0xc3e00000
	v_mov_b32_e32 v45, 5
	v_mov_b32_e32 v46, 0x43e00000
	v_mov_b32_e32 v47, 0
	v_mov_b32_e32 v48, 0
	v_mov_b32_e32 v49, 0
	v_mov_b32_e32 v50, 0
	v_readlane_b32 s11, v242, 12

.LBB0_2416:
	s_or_b64 exec, exec, s[0:1]
	v_readlane_b32 s6, v242, 1
	s_waitcnt lgkmcnt(0)
	s_barrier
	s_nop 0
	s_mov_b32 s4, 0
	v_readlane_b32 s7, v242, 2
	s_load_dwordx2 s[0:1], s[6:7], s4 offset:0x108
	s_load_dwordx2 s[2:3], s[6:7], s4 offset:0x70
	s_load_dwordx8 s[56:63], s[6:7], s4 offset:0x50
	v_mov_b32_e32 v40, v208
	v_readlane_b32 s6, v242, 20
	v_ashrrev_i32_e32 v37, 8, v40
	v_lshrrev_b32_e32 v38, 2, v40
	v_add_u32_e32 v2, 2, v37
	v_lshrrev_b32_e32 v0, 4, v40
	v_and_b32_e32 v112, 15, v40
	v_and_b32_e32 v36, 48, v38
	v_ashrrev_i32_e32 v3, 31, v2
	v_bfe_u32 v0, v0, 1, 1
	v_or3_b32 v1, v112, s6, v36
	v_lshlrev_b64 v[4:5], 14, v[2:3]
	v_cmp_eq_u32_e32 vcc, v0, v37
	v_lshlrev_b32_e32 v0, 9, v40
	s_waitcnt lgkmcnt(0)
	v_lshl_add_u64 v[4:5], s[60:61], 0, v[4:5]
	v_lshlrev_b32_e32 v32, 2, v1
	v_mov_b32_e32 v33, 0
	s_add_u32 s10, s0, 0x11fff000
	v_and_b32_e32 v0, 0x2000, v0
	v_readlane_b32 s6, v242, 22
	v_lshl_add_u64 v[4:5], v[4:5], 0, v[32:33]
	v_mov_b32_e32 v1, v33
	s_addc_u32 s11, s1, 0
	s_mov_b32 s8, s6
	v_lshl_add_u64 v[0:1], v[4:5], 0, v[0:1]
	s_movk_i32 s6, 0x1000
	s_add_u32 s4, s0, 0x284ff000
	s_waitcnt vmcnt(5)
	v_cndmask_b32_e64 v11, 0, -1, vcc
	v_add_co_u32_e32 v4, vcc, s6, v0
	v_readlane_b32 s6, v242, 24
	s_addc_u32 s5, s1, 0
	v_addc_co_u32_e32 v5, vcc, 0, v1, vcc
	global_load_dword v9, v[0:1], off
	global_load_dword v39, v[0:1], off offset:1024
	global_load_dword v10, v[0:1], off offset:2048
	global_load_dword v44, v[0:1], off offset:3072
	global_load_dword v45, v[4:5], off
	global_load_dword v47, v[4:5], off offset:1024
	global_load_dword v46, v[4:5], off offset:2048
	global_load_dword v48, v[4:5], off offset:3072
	v_lshlrev_b64 v[0:1], 10, v[2:3]
	s_lshl_b32 s6, s6, 2
	s_mov_b32 s9, 0
	v_lshl_add_u64 v[0:1], s[62:63], 0, v[0:1]
	s_add_u32 s2, s2, s6
	v_bfe_u32 v8, v40, 4, 2
	v_lshl_add_u64 v[0:1], v[0:1], 0, s[8:9]
	v_lshlrev_b32_e32 v32, 2, v36
	v_lshlrev_b32_e32 v34, 6, v37
	s_addc_u32 s3, s3, 0
	v_lshlrev_b32_e32 v4, 2, v112
	v_mov_b32_e32 v5, v33
	v_lshl_add_u64 v[0:1], v[0:1], 0, v[32:33]
	v_lshlrev_b32_e32 v32, 4, v8
	v_lshl_add_u64 v[4:5], s[2:3], 0, v[4:5]
	v_ashrrev_i32_e32 v35, 31, v34
	v_lshl_add_u64 v[0:1], v[0:1], 0, v[32:33]
	v_lshl_add_u64 v[4:5], v[34:35], 2, v[4:5]
	global_load_dwordx4 v[0:3], v[0:1], off
	s_nop 0
	global_load_dword v113, v[4:5], off offset:2048
	global_load_dword v114, v[4:5], off offset:2112
	global_load_dword v115, v[4:5], off offset:2176
	global_load_dword v116, v[4:5], off offset:2240
	v_readlane_b32 s2, v242, 25
	v_readlane_b32 s3, v242, 26
	s_and_b64 vcc, exec, s[2:3]
	v_readlane_b32 s7, v242, 23
	s_cbranch_vccnz .LBB0_2419
	v_readlane_b32 s2, v242, 0
	s_ashr_i32 s2, s2, 2
	s_mul_hi_i32 s3, s2, 0x78787879
	s_lshr_b32 s6, s3, 31
	s_ashr_i32 s7, s3, 5
	s_add_i32 s7, s7, s6
	s_mul_i32 s3, s7, 0x44
	s_sub_i32 s6, s2, s3
	s_lshl_b32 s9, s6, 6
	s_cmp_gt_i32 s6, 3
	s_cbranch_scc0 .LBB0_2420
	s_lshl_b32 s2, s7, 12
	s_add_i32 s2, s9, s2
	s_add_i32 s8, s2, 0xffffff00
	s_cbranch_execz .LBB0_2421
	s_branch .LBB0_2422

.LBB0_2516:
	s_or_b64 exec, exec, s[0:1]
	v_readlane_b32 s2, v242, 1
	v_readlane_b32 s3, v242, 2
	s_waitcnt lgkmcnt(0)
	s_barrier
	s_nop 0
	s_mov_b32 s1, 0
	s_load_dwordx2 s[8:9], s[2:3], s1 offset:0x108
	v_readlane_b32 s2, v242, 27
	v_mov_b32_e32 v164, v208
	v_readlane_b32 s3, v242, 28
	s_and_b64 vcc, exec, s[2:3]
	v_readfirstlane_b32 s42, v164
	s_cbranch_vccnz .LBB0_2518
	v_readlane_b32 s3, v242, 0
	s_ashr_i32 s0, s3, 31
	s_lshr_b32 s0, s0, 29
	s_add_i32 s0, s3, s0
	s_ashr_i32 s2, s0, 3
	s_and_b32 s0, s0, -8
	s_sub_i32 s0, s3, s0
	s_lshr_b32 s3, s0, 31
	s_or_b32 s3, s3, 0x44
	s_mul_i32 s0, s3, s0
	s_add_i32 s0, s0, s2
	s_ashr_i32 s2, s0, 31
	s_lshr_b32 s2, s2, 27
	s_add_i32 s2, s0, s2
	s_ashr_i32 s2, s2, 5
	s_lshl_b32 s4, s2, 3
	s_sub_i32 s3, 0x88, s4
	s_lshl_b32 s2, s2, 5
	s_min_u32 s5, s3, 8
	s_sub_i32 s0, s0, s2
	s_sext_i32_i8 s2, s0
	v_cvt_f32_ubyte0_e32 v1, s5
	v_cvt_f32_i32_e32 v0, s2
	v_rcp_iflag_f32_e32 v2, v1
	s_ashr_i32 s2, s2, 30
	s_or_b32 s6, s2, 1
	v_mul_f32_e32 v2, v0, v2
	v_trunc_f32_e32 v2, v2
	v_fma_f32 v0, -v2, v1, v0
	v_cvt_i32_f32_e32 v2, v2
	v_cmp_ge_f32_e64 s[2:3], |v0|, v1
	s_and_b64 s[2:3], s[2:3], exec
	s_cselect_b32 s2, s6, 0
	v_readfirstlane_b32 s3, v2
	s_add_i32 s2, s3, s2
	s_sext_i32_i8 s12, s2
	s_mul_i32 s2, s2, s5
	s_sub_i32 s0, s0, s2
	s_sext_i32_i8 s0, s0
	s_add_i32 s0, s4, s0

.LBB0_2720:
	s_or_b64 exec, exec, s[0:1]
	v_readlane_b32 s2, v242, 1
	s_waitcnt lgkmcnt(0)
	s_barrier
	s_nop 0
	s_mov_b32 s0, 0
	v_readlane_b32 s3, v242, 2
	s_load_dwordx4 s[92:95], s[2:3], s0 offset:0xe8
	s_load_dwordx2 s[4:5], s[2:3], s0 offset:0xf8
	s_load_dwordx2 s[14:15], s[2:3], s0 offset:0x108
	v_readlane_b32 s0, v242, 59
	s_waitcnt vmcnt(7)
	v_mov_b32_e32 v6, v208
	v_readlane_b32 s1, v242, 60
	s_and_b64 vcc, exec, s[0:1]
	s_waitcnt vmcnt(5)
	v_and_b32_e32 v14, 63, v6
	v_ashrrev_i32_e32 v4, 6, v6
	s_waitcnt vmcnt(4)
	v_lshlrev_b32_e32 v8, 3, v6
	s_cbranch_vccnz .LBB0_2870
	v_lshlrev_b32_e32 v5, 2, v6
	s_waitcnt vmcnt(2)
	v_or_b32_e32 v18, 3, v5
	s_waitcnt lgkmcnt(0)
	s_add_u32 s0, s14, 0x907000
	v_lshlrev_b32_e32 v0, 2, v18
	v_writelane_b32 v242, s0, 34
	s_addc_u32 s0, s15, 0
	v_sub_u32_e32 v19, 0, v0
	v_add_u32_e32 v0, 0xfc, v5
	s_add_u32 s8, s14, 0xd47000
	v_and_b32_e32 v20, 0xfc, v0
	v_add_u32_e32 v0, 0xf8, v5
	s_addc_u32 s9, s15, 0
	v_and_b32_e32 v21, 0xfc, v0
	v_add_u32_e32 v0, 0xf0, v5
	v_writelane_b32 v242, s0, 21
	s_add_u32 s0, s14, 0xd8b000
	v_and_b32_e32 v22, 0xfc, v0
	v_add_u32_e32 v0, 0xe0, v5
	s_addc_u32 s1, s15, 0
	s_movk_i32 s6, 0x100
	v_and_b32_e32 v23, 0xfc, v0
	v_add_u32_e32 v0, 0xc0, v5
	s_add_u32 s2, s14, 0xdcf000
	v_writelane_b32 v242, s14, 51
	v_cmp_gt_i32_e64 s[10:11], s6, v6
	s_waitcnt vmcnt(0)
	v_and_b32_e32 v24, 0xfc, v0
	s_movk_i32 s6, 0x80
	v_bfrev_b32_e32 v0, 0.5
	v_writelane_b32 v242, s15, 52
	v_bitop3_b32 v26, v5, s6, v0 bitop3:0x6c
	v_cmp_eq_u32_e64 s[6:7], 63, v14
	v_or_b32_e32 v0, 1, v8
	s_addc_u32 s3, s15, 0
	v_writelane_b32 v242, s6, 41
	v_ashrrev_i32_e32 v7, 31, v6
	v_cmp_gt_u32_e64 s[12:13], 64, v6
	v_writelane_b32 v242, s7, 42
	v_cmp_lt_i32_e64 s[6:7], 0, v4
	v_add_u32_e32 v15, 0, v5
	v_or_b32_e32 v16, 1, v5
	v_writelane_b32 v242, s6, 43
	v_or_b32_e32 v17, 2, v5
	v_cmp_eq_u32_e64 s[14:15], 0, v14
	v_writelane_b32 v242, s7, 44
	v_cmp_lt_i32_e64 s[6:7], 1, v4
	v_cmp_gt_u32_e64 s[16:17], 2, v14
	v_cmp_gt_u32_e64 s[18:19], 4, v14
	v_writelane_b32 v242, s6, 47
	v_cmp_gt_u32_e64 s[20:21], 8, v14
	v_cmp_gt_u32_e64 s[22:23], 16, v14
	v_writelane_b32 v242, s7, 48
	v_cmp_lt_i32_e64 s[6:7], 2, v4
	v_xor_b32_e32 v25, 0x80, v5
	v_cmp_gt_u32_e64 s[24:25], 32, v14
	v_writelane_b32 v242, s6, 49
	v_mov_b32_e32 v27, 0
	v_lshl_add_u32 v28, v4, 2, 0
	v_writelane_b32 v242, s7, 50
	s_movk_i32 s6, 0x200
	v_cmp_gt_i32_e64 s[46:47], s6, v6
	s_movk_i32 s6, 0x1000
	v_cmp_gt_i32_e64 s[48:49], s6, v0
	v_or_b32_e32 v0, 2, v8
	v_cmp_gt_i32_e64 s[50:51], s6, v0
	v_or_b32_e32 v0, 3, v8
	v_cmp_gt_i32_e64 s[52:53], s6, v0
	v_or_b32_e32 v0, 4, v8
	v_cmp_gt_i32_e64 s[54:55], s6, v0
	v_or_b32_e32 v0, 5, v8
	v_cmp_gt_i32_e64 s[56:57], s6, v0
	v_or_b32_e32 v0, 6, v8
	v_cmp_gt_i32_e64 s[58:59], s6, v0
	v_or_b32_e32 v0, 7, v8
	v_cmp_lt_i32_e64 s[36:37], 3, v4
	v_cmp_lt_i32_e64 s[38:39], 4, v4
	v_cmp_lt_i32_e64 s[40:41], 5, v4
	v_cmp_lt_i32_e64 s[42:43], 6, v4
	v_cmp_lt_i32_e64 s[44:45], 7, v4
	v_ashrrev_i32_e32 v9, 31, v8
	v_cmp_gt_i32_e64 s[60:61], s6, v0
	v_mov_b32_e32 v29, 1
	s_movk_i32 s33, 0x400
	v_readlane_b32 s30, v242, 0
	s_branch .LBB0_2725

.LBB0_2962:
	s_add_i32 s22, s20, 0xf2401100
	s_and_b32 s55, s22, 0x300
	s_add_u32 s24, s2, s55
	s_addc_u32 s25, s3, 0
	s_and_b64 s[22:23], s[26:27], exec
	s_cselect_b32 s23, s17, s25
	s_cselect_b32 s22, s53, s24
	s_mov_b64 s[24:25], s[22:23]
	s_mov_b32 m0, s34
	ds_read_b128 v[16:19], v217
	ds_read_b128 v[20:23], v218
	ds_read_b128 v[24:27], v225
	ds_read_b128 v[28:31], v226
	v_mov_b32_e32 v203, v197
	global_load_lds_dwordx4 v194, s[24:25]
	v_lshl_add_u64 v[236:237], s[24:25], 0, v[192:193]
	s_mov_b32 m0, s35
	s_add_u32 s24, s22, 0x80
	global_load_lds_dwordx4 v[236:237], off
	s_barrier
	s_waitcnt lgkmcnt(0)
	s_addc_u32 s25, s23, 0
	s_and_b64 s[26:27], s[26:27], exec
	s_cselect_b32 s27, 0, 0
	s_cselect_b32 s26, 0, s55
	s_setprio 1
	s_waitcnt lgkmcnt(0)
	v_mfma_scale_f32_16x16x128_f8f6f4 v[184:187], v[16:23], v[56:63], v[184:187], v212, v212 op_sel_hi:[0,0,0]
	v_mfma_scale_f32_16x16x128_f8f6f4 v[176:179], v[24:31], v[56:63], v[176:179], v212, v212 op_sel_hi:[0,0,0]
	v_mfma_scale_f32_16x16x128_f8f6f4 v[168:171], v[16:23], v[48:55], v[168:171], v212, v212 op_sel_hi:[0,0,0]
	v_mfma_scale_f32_16x16x128_f8f6f4 v[160:163], v[24:31], v[48:55], v[160:163], v212, v212 op_sel_hi:[0,0,0]
	v_mfma_scale_f32_16x16x128_f8f6f4 v[152:155], v[16:23], v[40:47], v[152:155], v212, v212 op_sel_hi:[0,0,0]
	v_mfma_scale_f32_16x16x128_f8f6f4 v[144:147], v[24:31], v[40:47], v[144:147], v212, v212 op_sel_hi:[0,0,0]
	v_mfma_scale_f32_16x16x128_f8f6f4 v[136:139], v[16:23], v[32:39], v[136:139], v212, v212 op_sel_hi:[0,0,0]
	v_mfma_scale_f32_16x16x128_f8f6f4 v[128:131], v[24:31], v[32:39], v[128:131], v212, v212 op_sel_hi:[0,0,0]
	s_setprio 0
	s_add_u32 s26, s6, s26
	s_addc_u32 s27, s7, s27
	s_mov_b64 s[56:57], s[26:27]
	s_mov_b32 m0, s1
	s_barrier
	ds_read_b128 v[32:35], v231 offset:16384
	ds_read_b128 v[40:43], v231 offset:18432
	ds_read_b128 v[36:39], v232 offset:16384
	ds_read_b128 v[44:47], v232 offset:18432
	ds_read_b128 v[48:51], v231 offset:20480
	ds_read_b128 v[56:59], v231 offset:22528
	ds_read_b128 v[52:55], v232 offset:20480
	ds_read_b128 v[60:63], v232 offset:22528
	s_nop 0
	global_load_lds_dwordx4 v198, s[56:57]
	s_mov_b32 m0, s36
	s_nop 0
	global_load_lds_dwordx4 v200, s[56:57]
	s_nop 0
	s_barrier
	s_waitcnt lgkmcnt(0)
	s_setprio 1
	s_waitcnt lgkmcnt(0)
	v_mfma_scale_f32_16x16x128_f8f6f4 v[124:127], v[0:7], v[32:39], v[124:127], v212, v212 op_sel_hi:[0,0,0]
	v_mfma_scale_f32_16x16x128_f8f6f4 v[116:119], v[8:15], v[32:39], v[116:119], v212, v212 op_sel_hi:[0,0,0]
	v_mfma_scale_f32_16x16x128_f8f6f4 v[108:111], v[0:7], v[40:47], v[108:111], v212, v212 op_sel_hi:[0,0,0]
	v_mfma_scale_f32_16x16x128_f8f6f4 v[100:103], v[8:15], v[40:47], v[100:103], v212, v212 op_sel_hi:[0,0,0]
	v_mfma_scale_f32_16x16x128_f8f6f4 v[92:95], v[0:7], v[48:55], v[92:95], v212, v212 op_sel_hi:[0,0,0]
	v_mfma_scale_f32_16x16x128_f8f6f4 v[84:87], v[8:15], v[48:55], v[84:87], v212, v212 op_sel_hi:[0,0,0]
	v_mfma_scale_f32_16x16x128_f8f6f4 v[76:79], v[0:7], v[56:63], v[76:79], v212, v212 op_sel_hi:[0,0,0]
	v_mfma_scale_f32_16x16x128_f8f6f4 v[68:71], v[8:15], v[56:63], v[68:71], v212, v212 op_sel_hi:[0,0,0]
	s_setprio 0
	s_barrier
	s_add_u32 s56, s22, 0x20000
	s_addc_u32 s57, s23, 0
	s_mov_b32 m0, s37
	s_nop 0
	global_load_lds_dwordx4 v194, s[56:57]
	s_mov_b32 m0, s38
	s_nop 0
	global_load_lds_dwordx4 v192, s[56:57]
	s_waitcnt vmcnt(6)
	s_barrier
	s_setprio 1
	v_mfma_scale_f32_16x16x128_f8f6f4 v[120:123], v[16:23], v[32:39], v[120:123], v212, v212 op_sel_hi:[0,0,0]
	v_mfma_scale_f32_16x16x128_f8f6f4 v[112:115], v[24:31], v[32:39], v[112:115], v212, v212 op_sel_hi:[0,0,0]
	v_mfma_scale_f32_16x16x128_f8f6f4 v[104:107], v[16:23], v[40:47], v[104:107], v212, v212 op_sel_hi:[0,0,0]
	v_mfma_scale_f32_16x16x128_f8f6f4 v[96:99], v[24:31], v[40:47], v[96:99], v212, v212 op_sel_hi:[0,0,0]
	v_mfma_scale_f32_16x16x128_f8f6f4 v[88:91], v[16:23], v[48:55], v[88:91], v212, v212 op_sel_hi:[0,0,0]
	v_mfma_scale_f32_16x16x128_f8f6f4 v[80:83], v[24:31], v[48:55], v[80:83], v212, v212 op_sel_hi:[0,0,0]
	v_mfma_scale_f32_16x16x128_f8f6f4 v[72:75], v[16:23], v[56:63], v[72:75], v212, v212 op_sel_hi:[0,0,0]
	v_mfma_scale_f32_16x16x128_f8f6f4 v[64:67], v[24:31], v[56:63], v[64:67], v212, v212 op_sel_hi:[0,0,0]
	s_setprio 0
	s_barrier
	ds_read_b128 v[0:3], v219
	ds_read_b128 v[4:7], v220
	ds_read_b128 v[8:11], v227
	ds_read_b128 v[12:15], v228
	s_mov_b64 s[56:57], s[26:27]
	s_mov_b32 m0, s39
	ds_read_b128 v[16:19], v231 offset:32768
	ds_read_b128 v[24:27], v231 offset:34816
	ds_read_b128 v[20:23], v232 offset:32768
	ds_read_b128 v[28:31], v232 offset:34816
	ds_read_b128 v[32:35], v231 offset:36864
	ds_read_b128 v[40:43], v231 offset:38912
	ds_read_b128 v[36:39], v232 offset:36864
	ds_read_b128 v[44:47], v232 offset:38912
	s_nop 0
	global_load_lds_dwordx4 v196, s[56:57]
	s_mov_b32 m0, s40
	s_nop 0
	global_load_lds_dwordx4 v202, s[56:57]
	s_waitcnt lgkmcnt(8)
	s_barrier
	s_waitcnt lgkmcnt(0)
	s_setprio 1
	s_waitcnt lgkmcnt(0)
	v_mfma_scale_f32_16x16x128_f8f6f4 v[188:191], v[0:7], v[16:23], v[188:191], v212, v212 op_sel_hi:[0,0,0]
	v_mfma_scale_f32_16x16x128_f8f6f4 v[180:183], v[8:15], v[16:23], v[180:183], v212, v212 op_sel_hi:[0,0,0]
	v_mfma_scale_f32_16x16x128_f8f6f4 v[172:175], v[0:7], v[24:31], v[172:175], v212, v212 op_sel_hi:[0,0,0]
	v_mfma_scale_f32_16x16x128_f8f6f4 v[164:167], v[8:15], v[24:31], v[164:167], v212, v212 op_sel_hi:[0,0,0]
	v_mfma_scale_f32_16x16x128_f8f6f4 v[156:159], v[0:7], v[32:39], v[156:159], v212, v212 op_sel_hi:[0,0,0]
	v_mfma_scale_f32_16x16x128_f8f6f4 v[148:151], v[8:15], v[32:39], v[148:151], v212, v212 op_sel_hi:[0,0,0]
	v_mfma_scale_f32_16x16x128_f8f6f4 v[140:143], v[0:7], v[40:47], v[140:143], v212, v212 op_sel_hi:[0,0,0]
	v_mfma_scale_f32_16x16x128_f8f6f4 v[132:135], v[8:15], v[40:47], v[132:135], v212, v212 op_sel_hi:[0,0,0]
	s_setprio 0
	s_barrier
	s_mov_b32 m0, s42
	ds_read_b128 v[48:51], v221
	ds_read_b128 v[52:55], v222
	ds_read_b128 v[56:59], v229
	ds_read_b128 v[60:63], v230
	s_nop 0
	global_load_lds_dwordx4 v194, s[24:25]
	s_mov_b32 m0, s43
	s_nop 0
	global_load_lds_dwordx4 v192, s[24:25]
	s_barrier
	s_waitcnt lgkmcnt(0)
	s_setprio 1
	s_waitcnt lgkmcnt(0)
	v_mfma_scale_f32_16x16x128_f8f6f4 v[184:187], v[48:55], v[16:23], v[184:187], v212, v212 op_sel_hi:[0,0,0]
	v_mfma_scale_f32_16x16x128_f8f6f4 v[176:179], v[56:63], v[16:23], v[176:179], v212, v212 op_sel_hi:[0,0,0]
	v_mfma_scale_f32_16x16x128_f8f6f4 v[168:171], v[48:55], v[24:31], v[168:171], v212, v212 op_sel_hi:[0,0,0]
	v_mfma_scale_f32_16x16x128_f8f6f4 v[160:163], v[56:63], v[24:31], v[160:163], v212, v212 op_sel_hi:[0,0,0]
	v_mfma_scale_f32_16x16x128_f8f6f4 v[152:155], v[48:55], v[32:39], v[152:155], v212, v212 op_sel_hi:[0,0,0]
	v_mfma_scale_f32_16x16x128_f8f6f4 v[144:147], v[56:63], v[32:39], v[144:147], v212, v212 op_sel_hi:[0,0,0]
	v_mfma_scale_f32_16x16x128_f8f6f4 v[136:139], v[48:55], v[40:47], v[136:139], v212, v212 op_sel_hi:[0,0,0]
	v_mfma_scale_f32_16x16x128_f8f6f4 v[128:131], v[56:63], v[40:47], v[128:131], v212, v212 op_sel_hi:[0,0,0]
	s_setprio 0
	s_add_u32 s24, s26, 0x80
	s_addc_u32 s25, s27, 0
	s_mov_b32 m0, s44
	s_barrier
	ds_read_b128 v[16:19], v231 offset:49152
	ds_read_b128 v[24:27], v231 offset:51200
	ds_read_b128 v[20:23], v232 offset:49152
	ds_read_b128 v[28:31], v232 offset:51200
	ds_read_b128 v[32:35], v231 offset:53248
	ds_read_b128 v[40:43], v231 offset:55296
	ds_read_b128 v[36:39], v232 offset:53248
	ds_read_b128 v[44:47], v232 offset:55296
	s_nop 0
	global_load_lds_dwordx4 v198, s[24:25]
	s_mov_b32 m0, s45
	s_nop 0
	global_load_lds_dwordx4 v200, s[24:25]
	s_nop 0
	s_barrier
	s_waitcnt lgkmcnt(0)
	s_setprio 1
	s_waitcnt lgkmcnt(0)
	v_mfma_scale_f32_16x16x128_f8f6f4 v[124:127], v[0:7], v[16:23], v[124:127], v212, v212 op_sel_hi:[0,0,0]
	v_mfma_scale_f32_16x16x128_f8f6f4 v[116:119], v[8:15], v[16:23], v[116:119], v212, v212 op_sel_hi:[0,0,0]
	v_mfma_scale_f32_16x16x128_f8f6f4 v[108:111], v[0:7], v[24:31], v[108:111], v212, v212 op_sel_hi:[0,0,0]
	v_mfma_scale_f32_16x16x128_f8f6f4 v[100:103], v[8:15], v[24:31], v[100:103], v212, v212 op_sel_hi:[0,0,0]
	v_mfma_scale_f32_16x16x128_f8f6f4 v[92:95], v[0:7], v[32:39], v[92:95], v212, v212 op_sel_hi:[0,0,0]
	v_mfma_scale_f32_16x16x128_f8f6f4 v[84:87], v[8:15], v[32:39], v[84:87], v212, v212 op_sel_hi:[0,0,0]
	v_mfma_scale_f32_16x16x128_f8f6f4 v[76:79], v[0:7], v[40:47], v[76:79], v212, v212 op_sel_hi:[0,0,0]
	v_mfma_scale_f32_16x16x128_f8f6f4 v[68:71], v[8:15], v[40:47], v[68:71], v212, v212 op_sel_hi:[0,0,0]
	s_setprio 0
	s_barrier
	s_add_u32 s22, s22, 0x20080
	s_addc_u32 s23, s23, 0
	s_mov_b32 m0, s46
	s_nop 0
	global_load_lds_dwordx4 v194, s[22:23]
	s_mov_b32 m0, s47
	s_nop 0
	global_load_lds_dwordx4 v192, s[22:23]
	s_waitcnt vmcnt(6)
	s_barrier
	s_setprio 1
	v_mfma_scale_f32_16x16x128_f8f6f4 v[120:123], v[48:55], v[16:23], v[120:123], v212, v212 op_sel_hi:[0,0,0]
	v_mfma_scale_f32_16x16x128_f8f6f4 v[112:115], v[56:63], v[16:23], v[112:115], v212, v212 op_sel_hi:[0,0,0]
	v_mfma_scale_f32_16x16x128_f8f6f4 v[104:107], v[48:55], v[24:31], v[104:107], v212, v212 op_sel_hi:[0,0,0]
	v_mfma_scale_f32_16x16x128_f8f6f4 v[96:99], v[56:63], v[24:31], v[96:99], v212, v212 op_sel_hi:[0,0,0]
	v_mfma_scale_f32_16x16x128_f8f6f4 v[88:91], v[48:55], v[32:39], v[88:91], v212, v212 op_sel_hi:[0,0,0]
	v_mfma_scale_f32_16x16x128_f8f6f4 v[80:83], v[56:63], v[32:39], v[80:83], v212, v212 op_sel_hi:[0,0,0]
	v_mfma_scale_f32_16x16x128_f8f6f4 v[72:75], v[48:55], v[40:47], v[72:75], v212, v212 op_sel_hi:[0,0,0]
	v_mfma_scale_f32_16x16x128_f8f6f4 v[64:67], v[56:63], v[40:47], v[64:67], v212, v212 op_sel_hi:[0,0,0]
	s_setprio 0
	s_add_i32 s54, s54, 2
	s_add_u32 s20, s20, 0x100
	s_addc_u32 s21, s21, 0
	s_cmp_gt_u32 s54, 5
	s_barrier
	s_cbranch_scc1 .LBB0_2958

.LBB0_3020:
	s_or_b64 exec, exec, s[0:1]
	v_readlane_b32 s2, v242, 37
	v_mov_b32_e32 v172, v208
	v_readlane_b32 s3, v242, 38
	s_waitcnt lgkmcnt(0)
	s_barrier
	s_nop 0
	s_mov_b32 s0, 0
	s_and_b64 vcc, exec, s[2:3]
	v_readfirstlane_b32 s40, v172
	s_cbranch_vccnz .LBB0_3032
	v_lshlrev_b32_e32 v0, 4, v172
	v_add_u32_e32 v1, 0x2000, v0
	v_ashrrev_i32_e32 v2, 31, v1
	v_lshrrev_b32_e32 v2, 22, v2
	v_add_u32_e32 v2, v1, v2
	v_ashrrev_i32_e32 v2, 10, v2
	v_mul_i32_i24_e32 v3, 0x400, v2
	v_sub_u32_e32 v1, v1, v3
	v_lshrrev_b32_e32 v3, 4, v1
	v_bitop3_b32 v1, v3, v1, 32 bitop3:0x6c
	v_ashrrev_i32_e32 v3, 31, v1
	v_lshrrev_b32_e32 v3, 26, v3
	v_add_u32_e32 v3, v1, v3
	v_lshlrev_b32_e32 v5, 3, v2
	v_readlane_b32 s2, v242, 1
	v_ashrrev_i32_e32 v4, 6, v3
	v_and_b32_e32 v5, -16, v5
	v_and_b32_e32 v3, 0xc0, v3
	v_readlane_b32 s3, v242, 2
	v_add_u32_e32 v5, v4, v5
	v_sub_u32_e32 v1, v1, v3
	v_mov_b32_e32 v3, 1
	s_load_dwordx2 s[6:7], s[2:3], s0 offset:0x108
	v_and_b32_e32 v4, 3, v4
	s_mov_b32 s0, 0x3fffe0
	v_lshrrev_b32_e32 v6, 2, v5
	v_lshlrev_b32_e32 v7, 1, v5
	v_lshlrev_b32_e32 v2, 5, v2
	v_ashrrev_i16_sdwa v1, v3, sext(v1) dst_sel:DWORD dst_unused:UNUSED_PAD src0_sel:DWORD src1_sel:BYTE_0
	v_and_or_b32 v4, v5, s0, v4
	v_and_b32_e32 v6, 4, v6
	v_and_b32_e32 v7, 24, v7
	v_and_b32_e32 v2, 32, v2
	v_bfe_i32 v1, v1, 0, 16
	v_or3_b32 v4, v4, v6, v7
	v_add_lshl_u32 v1, v2, v1, 1
	v_lshl_add_u32 v160, v4, 10, v1
	v_lshl_add_u32 v162, v5, 10, v1
	v_bfe_i32 v1, v172, 27, 1
	v_lshrrev_b32_e32 v1, 22, v1
	v_add_u32_e32 v1, v0, v1
	v_and_b32_e32 v1, 0xfffffc00, v1
	v_sub_u32_e32 v0, v0, v1
	v_lshrrev_b32_e32 v1, 4, v0
	v_ashrrev_i32_e32 v4, 31, v172
	v_bitop3_b32 v0, v1, v0, 32 bitop3:0x6c
	v_lshrrev_b32_e32 v4, 26, v4
	v_ashrrev_i32_e32 v1, 31, v0
	v_add_u32_e32 v4, v172, v4
	s_waitcnt lgkmcnt(0)
	s_add_u32 s41, s6, 0xbbff000
	v_lshrrev_b32_e32 v1, 26, v1
	v_ashrrev_i32_e32 v4, 6, v4
	s_addc_u32 s42, s7, 0
	v_add_u32_e32 v1, v0, v1
	v_lshlrev_b32_e32 v5, 3, v4
	s_add_u32 s43, s6, 0x1a7ff000
	v_ashrrev_i32_e32 v2, 6, v1
	v_and_b32_e32 v5, -16, v5
	v_readlane_b32 s2, v242, 0
	s_addc_u32 s44, s7, 0
	v_add_u32_e32 v5, v2, v5
	v_and_b32_e32 v2, 3, v2
	s_ashr_i32 s45, s2, 31
	v_and_or_b32 v2, v5, s0, v2
	s_lshr_b32 s0, s45, 29
	s_add_i32 s0, s2, s0
	s_ashr_i32 s10, s40, 6
	s_ashr_i32 s1, s0, 3
	s_and_b32 s0, s0, -8
	s_ashr_i32 s11, s40, 8
	s_lshl_b32 s12, s10, 10
	s_sub_i32 s0, s2, s0
	s_cmp_lt_i32 s0, 0
	s_movk_i32 s46, 0x89
	s_cselect_b32 s2, s46, 0x88
	s_mul_i32 s0, s2, s0
	s_add_i32 s0, s0, s1
	s_mul_hi_i32 s1, s0, 0x78787879
	s_lshr_b32 s2, s1, 31
	s_ashr_i32 s1, s1, 5
	s_add_i32 s3, s1, s2
	s_mul_i32 s1, s3, 0x44
	s_sub_i32 s0, s0, s1
	s_bfe_i32 s1, s0, 0x80000
	s_bfe_u32 s1, s1, 0x5000a
	s_add_i32 s1, s0, s1
	s_bfe_i32 s2, s1, 0x80000
	v_and_b32_e32 v1, 0xc0, v1
	s_sext_i32_i16 s2, s2
	v_sub_u32_e32 v0, v0, v1
	s_ashr_i32 s2, s2, 5
	v_lshrrev_b32_e32 v6, 2, v5
	v_lshlrev_b32_e32 v7, 1, v5
	v_lshlrev_b32_e32 v4, 5, v4
	v_ashrrev_i16_sdwa v0, v3, sext(v0) dst_sel:DWORD dst_unused:UNUSED_PAD src0_sel:DWORD src1_sel:BYTE_0
	s_lshl_b32 s2, s2, 3
	v_and_b32_e32 v6, 4, v6
	v_and_b32_e32 v7, 24, v7
	v_and_b32_e32 v4, 32, v4
	v_bfe_i32 v0, v0, 0, 16
	s_sub_i32 s4, 17, s2
	s_and_b32 s1, s1, 0xffe0
	v_or3_b32 v2, v2, v6, v7
	v_add_lshl_u32 v0, v4, v0, 1
	s_min_u32 s4, s4, 8
	s_sub_i32 s5, s0, s1
	v_lshl_add_u32 v164, v2, 10, v0
	s_sext_i32_i8 s0, s5
	v_cvt_f32_ubyte0_e32 v2, s4
	v_cvt_f32_i32_e32 v1, s0
	v_rcp_iflag_f32_e32 v3, v2
	v_lshl_add_u32 v166, v5, 10, v0
	s_ashr_i32 s0, s0, 30
	s_or_b32 s8, s0, 1
	v_mul_f32_e32 v0, v1, v3
	v_trunc_f32_e32 v0, v0
	v_fma_f32 v1, -v0, v2, v1
	v_cvt_i32_f32_e32 v0, v0
	v_cmp_ge_f32_e64 s[0:1], |v1|, v2
	s_and_b64 s[0:1], s[0:1], exec
	s_cselect_b32 s0, s8, 0
	v_readfirstlane_b32 s1, v0
	s_add_i32 s0, s1, s0
	s_sext_i32_i8 s1, s0
	s_mul_i32 s0, s0, s4
	s_sub_i32 s0, s5, s0
	s_mul_i32 s4, s3, 17
	s_sext_i32_i8 s0, s0
	s_add_i32 s2, s2, s4
	s_add_i32 s2, s2, s0
	s_lshl_b32 s0, s3, 2
	s_add_i32 s0, s0, s1
	s_ashr_i32 s3, s2, 31
	s_ashr_i32 s1, s0, 31
	s_lshl_b64 s[4:5], s[2:3], 18
	s_lshl_b64 s[8:9], s[0:1], 18
	s_add_u32 s26, s41, s8
	s_addc_u32 s27, s42, s9
	s_add_i32 s1, s12, 0
	s_add_i32 s3, s1, 0x10000
	s_add_i32 s47, s1, 0x12000
	v_mov_b32_e32 v173, 0x7f
	s_mov_b64 s[8:9], s[26:27]
	s_mov_b32 m0, s3
	s_add_u32 s28, s43, s4
	s_addc_u32 s29, s44, s5
	global_load_lds_dwordx4 v164, s[8:9]
	s_mov_b32 m0, s47
	s_mov_b64 s[4:5], s[28:29]
	global_load_lds_dwordx4 v160, s[8:9]
	s_mov_b32 m0, s1
	s_add_i32 s48, s1, 0x2000
	v_mov_b32_e32 v165, 0
	global_load_lds_dwordx4 v166, s[4:5]
	s_mov_b32 m0, s48
	s_mov_b32 s53, 0
	global_load_lds_dwordx4 v162, s[4:5]
	s_add_u32 s4, s26, 0x20000
	s_addc_u32 s5, s27, 0
	s_add_i32 s49, s1, 0x14000
	s_mov_b32 m0, s49
	s_add_i32 s50, s1, 0x16000
	v_mov_b32_e32 v161, v165
	global_load_lds_dwordx4 v164, s[4:5]
	s_mov_b32 m0, s50
	v_mov_b32_e32 v167, v165
	global_load_lds_dwordx4 v160, s[4:5]
	s_add_u32 s4, s28, 0x20000
	s_addc_u32 s5, s29, 0
	s_add_i32 s51, s1, 0x4000
	s_mov_b32 m0, s51
	s_add_i32 s52, s1, 0x6000
	s_cmp_lg_u32 s11, 1
	global_load_lds_dwordx4 v166, s[4:5]
	s_mov_b32 m0, s52
	v_mov_b32_e32 v163, v165
	global_load_lds_dwordx4 v162, s[4:5]
	s_cbranch_scc1 .LBB0_3023
	s_barrier

.LBB0_3027:
	s_add_u32 s30, s36, 0x100
	ds_read_b128 v[0:3], v174
	ds_read_b128 v[4:7], v175
	ds_read_b128 v[8:11], v182
	ds_read_b128 v[12:15], v183
	s_addc_u32 s31, s37, 0
	s_and_b32 s66, s30, 0x300
	s_add_u32 s65, s26, s66
	s_addc_u32 s67, s27, 0
	s_cmp_eq_u32 s33, 4
	s_cselect_b64 s[38:39], -1, 0
	s_and_b64 s[34:35], s[38:39], exec
	s_cselect_b32 s35, s21, s67
	s_cselect_b32 s34, s23, s65
	s_cselect_b32 s65, 0, 0
	s_cselect_b32 s66, 0, s66
	s_add_u32 s36, s28, s36
	s_addc_u32 s37, s29, s37
	s_add_u32 s36, s36, 0x20080
	s_addc_u32 s37, s37, 0
	ds_read_b128 v[194:197], v190
	ds_read_b128 v[210:213], v190 offset:2048
	ds_read_b128 v[198:201], v191
	ds_read_b128 v[214:217], v191 offset:2048
	ds_read_b128 v[218:221], v190 offset:4096
	ds_read_b128 v[226:229], v190 offset:6144
	ds_read_b128 v[222:225], v191 offset:4096
	ds_read_b128 v[230:233], v191 offset:6144
	s_add_i32 m0, s1, 0xc000
	s_nop 0
	global_load_lds_dwordx4 v166, s[36:37]
	s_add_i32 m0, s1, 0xe000
	s_nop 0
	global_load_lds_dwordx4 v162, s[36:37]
	s_waitcnt lgkmcnt(8)
	s_nop 0
	s_barrier
	s_waitcnt lgkmcnt(0)
	s_setprio 1
	s_waitcnt lgkmcnt(0)
	v_mfma_scale_f32_16x16x128_f8f6f4 v[156:159], v[0:7], v[194:201], v[156:159], v173, v173 op_sel_hi:[0,0,0]
	v_mfma_scale_f32_16x16x128_f8f6f4 v[152:155], v[8:15], v[194:201], v[152:155], v173, v173 op_sel_hi:[0,0,0]
	v_mfma_scale_f32_16x16x128_f8f6f4 v[140:143], v[0:7], v[210:217], v[140:143], v173, v173 op_sel_hi:[0,0,0]
	v_mfma_scale_f32_16x16x128_f8f6f4 v[136:139], v[8:15], v[210:217], v[136:139], v173, v173 op_sel_hi:[0,0,0]
	v_mfma_scale_f32_16x16x128_f8f6f4 v[124:127], v[0:7], v[218:225], v[124:127], v173, v173 op_sel_hi:[0,0,0]
	v_mfma_scale_f32_16x16x128_f8f6f4 v[120:123], v[8:15], v[218:225], v[120:123], v173, v173 op_sel_hi:[0,0,0]
	v_mfma_scale_f32_16x16x128_f8f6f4 v[108:111], v[0:7], v[226:233], v[108:111], v173, v173 op_sel_hi:[0,0,0]
	v_mfma_scale_f32_16x16x128_f8f6f4 v[104:107], v[8:15], v[226:233], v[104:107], v173, v173 op_sel_hi:[0,0,0]
	s_setprio 0
	s_barrier
	s_mov_b64 s[36:37], s[34:35]
	s_mov_b32 m0, s3
	ds_read_b128 v[16:19], v176
	ds_read_b128 v[20:23], v177
	ds_read_b128 v[24:27], v184
	ds_read_b128 v[28:31], v185
	s_nop 0
	global_load_lds_dwordx4 v164, s[36:37]
	s_mov_b32 m0, s47
	s_nop 0
	global_load_lds_dwordx4 v160, s[36:37]
	s_nop 0
	s_barrier
	s_waitcnt lgkmcnt(0)
	s_setprio 1
	s_waitcnt lgkmcnt(0)
	v_mfma_scale_f32_16x16x128_f8f6f4 v[148:151], v[16:23], v[194:201], v[148:151], v173, v173 op_sel_hi:[0,0,0]
	v_mfma_scale_f32_16x16x128_f8f6f4 v[144:147], v[24:31], v[194:201], v[144:147], v173, v173 op_sel_hi:[0,0,0]
	v_mfma_scale_f32_16x16x128_f8f6f4 v[132:135], v[16:23], v[210:217], v[132:135], v173, v173 op_sel_hi:[0,0,0]
	v_mfma_scale_f32_16x16x128_f8f6f4 v[128:131], v[24:31], v[210:217], v[128:131], v173, v173 op_sel_hi:[0,0,0]
	v_mfma_scale_f32_16x16x128_f8f6f4 v[116:119], v[16:23], v[218:225], v[116:119], v173, v173 op_sel_hi:[0,0,0]
	v_mfma_scale_f32_16x16x128_f8f6f4 v[112:115], v[24:31], v[218:225], v[112:115], v173, v173 op_sel_hi:[0,0,0]
	v_mfma_scale_f32_16x16x128_f8f6f4 v[100:103], v[16:23], v[226:233], v[100:103], v173, v173 op_sel_hi:[0,0,0]
	v_mfma_scale_f32_16x16x128_f8f6f4 v[96:99], v[24:31], v[226:233], v[96:99], v173, v173 op_sel_hi:[0,0,0]
	s_setprio 0
	s_and_b64 s[36:37], s[12:13], s[38:39]
	s_and_b64 s[36:37], s[36:37], exec
	s_cselect_b32 s36, s6, s28
	s_cselect_b32 s37, s7, s29
	s_add_u32 s36, s36, s66
	s_addc_u32 s37, s37, s65
	s_mov_b64 s[38:39], s[36:37]
	s_mov_b32 m0, s1
	s_barrier
	ds_read_b128 v[194:197], v190 offset:16384
	ds_read_b128 v[210:213], v190 offset:18432
	ds_read_b128 v[198:201], v191 offset:16384
	ds_read_b128 v[214:217], v191 offset:18432
	ds_read_b128 v[218:221], v190 offset:20480
	ds_read_b128 v[226:229], v190 offset:22528
	ds_read_b128 v[222:225], v191 offset:20480
	ds_read_b128 v[230:233], v191 offset:22528
	s_nop 0
	global_load_lds_dwordx4 v166, s[38:39]
	s_mov_b32 m0, s48
	s_nop 0
	global_load_lds_dwordx4 v162, s[38:39]
	s_nop 0
	s_barrier
	s_waitcnt lgkmcnt(0)
	s_setprio 1
	s_waitcnt lgkmcnt(0)
	v_mfma_scale_f32_16x16x128_f8f6f4 v[92:95], v[0:7], v[194:201], v[92:95], v173, v173 op_sel_hi:[0,0,0]
	v_mfma_scale_f32_16x16x128_f8f6f4 v[88:91], v[8:15], v[194:201], v[88:91], v173, v173 op_sel_hi:[0,0,0]
	v_mfma_scale_f32_16x16x128_f8f6f4 v[76:79], v[0:7], v[210:217], v[76:79], v173, v173 op_sel_hi:[0,0,0]
	v_mfma_scale_f32_16x16x128_f8f6f4 v[72:75], v[8:15], v[210:217], v[72:75], v173, v173 op_sel_hi:[0,0,0]
	v_mfma_scale_f32_16x16x128_f8f6f4 v[60:63], v[0:7], v[218:225], v[60:63], v173, v173 op_sel_hi:[0,0,0]
	v_mfma_scale_f32_16x16x128_f8f6f4 v[56:59], v[8:15], v[218:225], v[56:59], v173, v173 op_sel_hi:[0,0,0]
	v_mfma_scale_f32_16x16x128_f8f6f4 v[44:47], v[0:7], v[226:233], v[44:47], v173, v173 op_sel_hi:[0,0,0]
	v_mfma_scale_f32_16x16x128_f8f6f4 v[40:43], v[8:15], v[226:233], v[40:43], v173, v173 op_sel_hi:[0,0,0]
	s_setprio 0
	s_barrier
	s_add_u32 s38, s34, 0x20000
	s_addc_u32 s39, s35, 0
	s_mov_b32 m0, s49
	s_nop 0
	global_load_lds_dwordx4 v164, s[38:39]
	s_mov_b32 m0, s50
	s_nop 0
	global_load_lds_dwordx4 v160, s[38:39]
	s_waitcnt vmcnt(6)
	s_barrier
	s_setprio 1
	v_mfma_scale_f32_16x16x128_f8f6f4 v[84:87], v[16:23], v[194:201], v[84:87], v173, v173 op_sel_hi:[0,0,0]
	v_mfma_scale_f32_16x16x128_f8f6f4 v[80:83], v[24:31], v[194:201], v[80:83], v173, v173 op_sel_hi:[0,0,0]
	v_mfma_scale_f32_16x16x128_f8f6f4 v[68:71], v[16:23], v[210:217], v[68:71], v173, v173 op_sel_hi:[0,0,0]
	v_mfma_scale_f32_16x16x128_f8f6f4 v[64:67], v[24:31], v[210:217], v[64:67], v173, v173 op_sel_hi:[0,0,0]
	v_mfma_scale_f32_16x16x128_f8f6f4 v[52:55], v[16:23], v[218:225], v[52:55], v173, v173 op_sel_hi:[0,0,0]
	v_mfma_scale_f32_16x16x128_f8f6f4 v[48:51], v[24:31], v[218:225], v[48:51], v173, v173 op_sel_hi:[0,0,0]
	v_mfma_scale_f32_16x16x128_f8f6f4 v[36:39], v[16:23], v[226:233], v[36:39], v173, v173 op_sel_hi:[0,0,0]
	v_mfma_scale_f32_16x16x128_f8f6f4 v[32:35], v[24:31], v[226:233], v[32:35], v173, v173 op_sel_hi:[0,0,0]
	s_setprio 0
	s_barrier
	ds_read_b128 v[0:3], v178
	ds_read_b128 v[4:7], v179
	ds_read_b128 v[8:11], v186
	ds_read_b128 v[12:15], v187
	s_add_u32 s38, s36, 0x20000
	s_addc_u32 s39, s37, 0
	s_mov_b32 m0, s51
	ds_read_b128 v[16:19], v190 offset:32768
	ds_read_b128 v[24:27], v190 offset:34816
	ds_read_b128 v[20:23], v191 offset:32768
	ds_read_b128 v[28:31], v191 offset:34816
	ds_read_b128 v[194:197], v190 offset:36864
	ds_read_b128 v[210:213], v190 offset:38912
	ds_read_b128 v[198:201], v191 offset:36864
	ds_read_b128 v[214:217], v191 offset:38912
	s_nop 0
	global_load_lds_dwordx4 v166, s[38:39]
	s_mov_b32 m0, s52
	s_nop 0
	global_load_lds_dwordx4 v162, s[38:39]
	s_waitcnt lgkmcnt(8)
	s_barrier
	s_waitcnt lgkmcnt(0)
	s_setprio 1
	s_waitcnt lgkmcnt(0)
	v_mfma_scale_f32_16x16x128_f8f6f4 v[156:159], v[0:7], v[16:23], v[156:159], v173, v173 op_sel_hi:[0,0,0]
	v_mfma_scale_f32_16x16x128_f8f6f4 v[152:155], v[8:15], v[16:23], v[152:155], v173, v173 op_sel_hi:[0,0,0]
	v_mfma_scale_f32_16x16x128_f8f6f4 v[140:143], v[0:7], v[24:31], v[140:143], v173, v173 op_sel_hi:[0,0,0]
	v_mfma_scale_f32_16x16x128_f8f6f4 v[136:139], v[8:15], v[24:31], v[136:139], v173, v173 op_sel_hi:[0,0,0]
	v_mfma_scale_f32_16x16x128_f8f6f4 v[124:127], v[0:7], v[194:201], v[124:127], v173, v173 op_sel_hi:[0,0,0]
	v_mfma_scale_f32_16x16x128_f8f6f4 v[120:123], v[8:15], v[194:201], v[120:123], v173, v173 op_sel_hi:[0,0,0]
	v_mfma_scale_f32_16x16x128_f8f6f4 v[108:111], v[0:7], v[210:217], v[108:111], v173, v173 op_sel_hi:[0,0,0]
	v_mfma_scale_f32_16x16x128_f8f6f4 v[104:107], v[8:15], v[210:217], v[104:107], v173, v173 op_sel_hi:[0,0,0]
	s_setprio 0
	s_barrier
	s_add_u32 s38, s34, 0x80
	s_addc_u32 s39, s35, 0
	s_mov_b32 m0, s54
	ds_read_b128 v[218:221], v180
	ds_read_b128 v[222:225], v181
	ds_read_b128 v[226:229], v188
	ds_read_b128 v[230:233], v189
	s_nop 0
	global_load_lds_dwordx4 v164, s[38:39]
	s_mov_b32 m0, s55
	s_nop 0
	global_load_lds_dwordx4 v160, s[38:39]
	s_nop 0
	s_barrier
	s_waitcnt lgkmcnt(0)
	s_setprio 1
	s_waitcnt lgkmcnt(0)
	v_mfma_scale_f32_16x16x128_f8f6f4 v[148:151], v[218:225], v[16:23], v[148:151], v173, v173 op_sel_hi:[0,0,0]
	v_mfma_scale_f32_16x16x128_f8f6f4 v[144:147], v[226:233], v[16:23], v[144:147], v173, v173 op_sel_hi:[0,0,0]
	v_mfma_scale_f32_16x16x128_f8f6f4 v[132:135], v[218:225], v[24:31], v[132:135], v173, v173 op_sel_hi:[0,0,0]
	v_mfma_scale_f32_16x16x128_f8f6f4 v[128:131], v[226:233], v[24:31], v[128:131], v173, v173 op_sel_hi:[0,0,0]
	v_mfma_scale_f32_16x16x128_f8f6f4 v[116:119], v[218:225], v[194:201], v[116:119], v173, v173 op_sel_hi:[0,0,0]
	v_mfma_scale_f32_16x16x128_f8f6f4 v[112:115], v[226:233], v[194:201], v[112:115], v173, v173 op_sel_hi:[0,0,0]
	v_mfma_scale_f32_16x16x128_f8f6f4 v[100:103], v[218:225], v[210:217], v[100:103], v173, v173 op_sel_hi:[0,0,0]
	v_mfma_scale_f32_16x16x128_f8f6f4 v[96:99], v[226:233], v[210:217], v[96:99], v173, v173 op_sel_hi:[0,0,0]
	s_setprio 0
	s_add_u32 s36, s36, 0x80
	s_addc_u32 s37, s37, 0
	s_mov_b32 m0, s56
	s_barrier
	ds_read_b128 v[16:19], v190 offset:49152
	ds_read_b128 v[24:27], v190 offset:51200
	ds_read_b128 v[20:23], v191 offset:49152
	ds_read_b128 v[28:31], v191 offset:51200
	ds_read_b128 v[194:197], v190 offset:53248
	ds_read_b128 v[210:213], v190 offset:55296
	ds_read_b128 v[198:201], v191 offset:53248
	ds_read_b128 v[214:217], v191 offset:55296
	s_nop 0
	global_load_lds_dwordx4 v166, s[36:37]
	s_mov_b32 m0, s57
	s_nop 0
	global_load_lds_dwordx4 v162, s[36:37]
	s_nop 0
	s_barrier
	s_waitcnt lgkmcnt(0)
	s_setprio 1
	s_waitcnt lgkmcnt(0)
	v_mfma_scale_f32_16x16x128_f8f6f4 v[92:95], v[0:7], v[16:23], v[92:95], v173, v173 op_sel_hi:[0,0,0]
	v_mfma_scale_f32_16x16x128_f8f6f4 v[88:91], v[8:15], v[16:23], v[88:91], v173, v173 op_sel_hi:[0,0,0]
	v_mfma_scale_f32_16x16x128_f8f6f4 v[76:79], v[0:7], v[24:31], v[76:79], v173, v173 op_sel_hi:[0,0,0]
	v_mfma_scale_f32_16x16x128_f8f6f4 v[72:75], v[8:15], v[24:31], v[72:75], v173, v173 op_sel_hi:[0,0,0]
	v_mfma_scale_f32_16x16x128_f8f6f4 v[60:63], v[0:7], v[194:201], v[60:63], v173, v173 op_sel_hi:[0,0,0]
	v_mfma_scale_f32_16x16x128_f8f6f4 v[56:59], v[8:15], v[194:201], v[56:59], v173, v173 op_sel_hi:[0,0,0]
	v_mfma_scale_f32_16x16x128_f8f6f4 v[44:47], v[0:7], v[210:217], v[44:47], v173, v173 op_sel_hi:[0,0,0]
	v_mfma_scale_f32_16x16x128_f8f6f4 v[40:43], v[8:15], v[210:217], v[40:43], v173, v173 op_sel_hi:[0,0,0]
	s_setprio 0
	s_barrier
	s_add_u32 s34, s34, 0x20080
	s_addc_u32 s35, s35, 0
	s_mov_b32 m0, s58
	s_nop 0
	global_load_lds_dwordx4 v164, s[34:35]
	s_mov_b32 m0, s59
	s_nop 0
	global_load_lds_dwordx4 v160, s[34:35]
	s_waitcnt vmcnt(6)
	s_barrier
	s_setprio 1
	v_mfma_scale_f32_16x16x128_f8f6f4 v[84:87], v[218:225], v[16:23], v[84:87], v173, v173 op_sel_hi:[0,0,0]
	v_mfma_scale_f32_16x16x128_f8f6f4 v[80:83], v[226:233], v[16:23], v[80:83], v173, v173 op_sel_hi:[0,0,0]
	v_mfma_scale_f32_16x16x128_f8f6f4 v[68:71], v[218:225], v[24:31], v[68:71], v173, v173 op_sel_hi:[0,0,0]
	v_mfma_scale_f32_16x16x128_f8f6f4 v[64:67], v[226:233], v[24:31], v[64:67], v173, v173 op_sel_hi:[0,0,0]
	v_mfma_scale_f32_16x16x128_f8f6f4 v[52:55], v[218:225], v[194:201], v[52:55], v173, v173 op_sel_hi:[0,0,0]
	v_mfma_scale_f32_16x16x128_f8f6f4 v[48:51], v[226:233], v[194:201], v[48:51], v173, v173 op_sel_hi:[0,0,0]
	v_mfma_scale_f32_16x16x128_f8f6f4 v[36:39], v[218:225], v[210:217], v[36:39], v173, v173 op_sel_hi:[0,0,0]
	v_mfma_scale_f32_16x16x128_f8f6f4 v[32:35], v[226:233], v[210:217], v[32:35], v173, v173 op_sel_hi:[0,0,0]
	s_setprio 0
	s_add_i32 s33, s33, 2
	s_cmp_gt_u32 s33, 5
	s_mov_b64 s[36:37], s[30:31]
	s_barrier
	s_cbranch_scc0 .LBB0_3027
	v_mov_b32_e32 v2, v172
	v_mov_b32_e32 v8, 0
	v_ashrrev_i32_e32 v0, 2, v2
	v_and_b32_e32 v0, 0xffffffc0, v0
	v_lshl_add_u32 v0, s2, 8, v0
	v_and_or_b32 v6, v2, 15, v0
	v_ashrrev_i32_e32 v7, 31, v6
	v_lshl_add_u64 v[0:1], v[6:7], 2, s[4:5]
	global_load_dword v14, v[0:1], off
	global_load_dword v194, v[0:1], off offset:64
	global_load_dword v195, v[0:1], off offset:128
	global_load_dword v196, v[0:1], off offset:192
	global_load_dword v197, v[0:1], off offset:512
	global_load_dword v198, v[0:1], off offset:576
	global_load_dword v199, v[0:1], off offset:640
	global_load_dword v200, v[0:1], off offset:704
	s_ashr_i32 s2, s0, 31
	s_lshr_b32 s2, s2, 30
	s_add_i32 s2, s0, s2
	v_lshrrev_b32_e32 v2, 1, v2
	s_and_b32 s2, s2, 0xfffffc
	v_and_b32_e32 v2, 0x78, v2
	s_sub_i32 s0, s0, s2
	v_lshl_or_b32 v4, s0, 8, v2
	v_lshlrev_b64 v[2:3], 10, v[6:7]
	v_mov_b32_e32 v9, 0
	v_mov_b32_e32 v10, 0
	v_mov_b32_e32 v11, 0
	v_ashrrev_i32_e32 v5, 31, v4
	v_or_b32_e32 v12, 16, v6
	v_lshl_add_u64 v[2:3], s[8:9], 0, v[2:3]
	v_ashrrev_i32_e32 v13, 31, v12
	v_lshl_add_u64 v[2:3], v[2:3], 0, v[4:5]
	s_mov_b32 s0, 0x20000
	s_mov_b64 s[12:13], 0x20000
	s_mov_b64 s[28:29], s[6:7]
	s_mov_b64 s[26:27], s[24:25]
	s_mov_b32 s2, s20
	s_waitcnt vmcnt(0)
	v_mul_f32_e32 v7, 0x3d000000, v14
	v_mul_f32_e32 v14, 0x42000000, v7
	v_pk_mul_f32 v[18:19], v[156:157], v[14:15] op_sel_hi:[1,0]
	v_pk_mul_f32 v[22:23], v[152:153], v[14:15] op_sel_hi:[1,0]
	v_pk_mul_f32 v[16:17], v[158:159], v[14:15] op_sel_hi:[1,0]
	v_pk_mul_f32 v[20:21], v[154:155], v[14:15] op_sel_hi:[1,0]
	v_pk_mul_f32 v[24:25], v[150:151], v[14:15] op_sel_hi:[1,0]
	v_pk_mul_f32 v[26:27], v[148:149], v[14:15] op_sel_hi:[1,0]
	v_pk_mul_f32 v[28:29], v[146:147], v[14:15] op_sel_hi:[1,0]
	v_pk_mul_f32 v[14:15], v[144:145], v[14:15] op_sel_hi:[1,0]
	v_med3_f32 v7, v18, s61, v192
	v_med3_f32 v18, v22, s61, v192
	v_med3_f32 v19, v19, s61, v192
	v_med3_f32 v22, v23, s61, v192
	v_med3_f32 v23, v26, s61, v192
	v_med3_f32 v14, v14, s61, v192
	v_med3_f32 v26, v27, s61, v192
	v_med3_f32 v15, v15, s61, v192
	v_cvt_pk_fp8_f32 v8, v7, v19
	v_cvt_pk_fp8_f32 v9, v18, v22
	v_cvt_pk_fp8_f32 v10, v23, v26
	v_cvt_pk_fp8_f32 v11, v14, v15
	v_med3_f32 v16, v16, s61, v192
	v_med3_f32 v20, v20, s61, v192
	v_med3_f32 v17, v17, s61, v192
	v_med3_f32 v21, v21, s61, v192
	v_med3_f32 v24, v24, s61, v192
	v_med3_f32 v27, v28, s61, v192
	v_med3_f32 v25, v25, s61, v192
	v_med3_f32 v28, v29, s61, v192
	v_cvt_pk_fp8_f32 v8, v16, v17 op_sel:[0,0,1]
	v_cvt_pk_fp8_f32 v9, v20, v21 op_sel:[0,0,1]
	v_cvt_pk_fp8_f32 v10, v24, v25 op_sel:[0,0,1]
	v_cvt_pk_fp8_f32 v11, v27, v28 op_sel:[0,0,1]
	v_lshl_add_u64 v[14:15], v[12:13], 2, s[4:5]
	global_store_dwordx2 v[2:3], v[8:9], off
	global_store_dwordx2 v[2:3], v[10:11], off offset:128
	v_mov_b32_e32 v8, 0
	v_mov_b32_e32 v9, 0
	v_mov_b32_e32 v10, 0
	v_mov_b32_e32 v11, 0
	v_lshlrev_b64 v[12:13], 10, v[12:13]
	v_or_b32_e32 v14, 32, v6
	v_lshl_add_u64 v[12:13], s[8:9], 0, v[12:13]
	v_ashrrev_i32_e32 v15, 31, v14
	v_lshl_add_u64 v[12:13], v[12:13], 0, v[4:5]
	v_lshl_add_u64 v[16:17], v[14:15], 2, s[4:5]
	v_or_b32_e32 v6, 48, v6
	v_mul_f32_e32 v7, 0x3d000000, v194
	v_mul_f32_e32 v18, 0x42000000, v7
	v_pk_mul_f32 v[22:23], v[140:141], v[18:19] op_sel_hi:[1,0]
	v_pk_mul_f32 v[26:27], v[136:137], v[18:19] op_sel_hi:[1,0]
	v_pk_mul_f32 v[20:21], v[142:143], v[18:19] op_sel_hi:[1,0]
	v_pk_mul_f32 v[24:25], v[138:139], v[18:19] op_sel_hi:[1,0]
	v_pk_mul_f32 v[28:29], v[134:135], v[18:19] op_sel_hi:[1,0]
	v_pk_mul_f32 v[30:31], v[132:133], v[18:19] op_sel_hi:[1,0]
	v_pk_mul_f32 v[130:131], v[130:131], v[18:19] op_sel_hi:[1,0]
	v_pk_mul_f32 v[18:19], v[128:129], v[18:19] op_sel_hi:[1,0]
	v_med3_f32 v7, v22, s61, v192
	v_med3_f32 v22, v26, s61, v192
	v_med3_f32 v23, v23, s61, v192
	v_med3_f32 v26, v27, s61, v192
	v_med3_f32 v27, v30, s61, v192
	v_med3_f32 v18, v18, s61, v192
	v_med3_f32 v30, v31, s61, v192
	v_med3_f32 v19, v19, s61, v192
	v_cvt_pk_fp8_f32 v8, v7, v23
	v_cvt_pk_fp8_f32 v9, v22, v26
	v_cvt_pk_fp8_f32 v10, v27, v30
	v_cvt_pk_fp8_f32 v11, v18, v19
	v_med3_f32 v20, v20, s61, v192
	v_med3_f32 v24, v24, s61, v192
	v_med3_f32 v21, v21, s61, v192
	v_med3_f32 v25, v25, s61, v192
	v_med3_f32 v28, v28, s61, v192
	v_med3_f32 v31, v130, s61, v192
	v_med3_f32 v29, v29, s61, v192
	v_med3_f32 v128, v131, s61, v192
	v_cvt_pk_fp8_f32 v8, v20, v21 op_sel:[0,0,1]
	v_cvt_pk_fp8_f32 v9, v24, v25 op_sel:[0,0,1]
	v_cvt_pk_fp8_f32 v10, v28, v29 op_sel:[0,0,1]
	v_cvt_pk_fp8_f32 v11, v31, v128 op_sel:[0,0,1]
	global_store_dwordx2 v[12:13], v[8:9], off
	global_store_dwordx2 v[12:13], v[10:11], off offset:128
	v_mov_b32_e32 v8, 0
	v_mov_b32_e32 v9, 0
	v_mov_b32_e32 v10, 0
	v_mov_b32_e32 v11, 0
	v_lshlrev_b64 v[12:13], 10, v[14:15]
	v_lshl_add_u64 v[12:13], s[8:9], 0, v[12:13]
	v_ashrrev_i32_e32 v7, 31, v6
	v_lshl_add_u64 v[12:13], v[12:13], 0, v[4:5]
	v_lshl_add_u64 v[14:15], v[6:7], 2, s[4:5]
	v_lshlrev_b64 v[6:7], 10, v[6:7]
	v_lshl_add_u64 v[6:7], s[8:9], 0, v[6:7]
	v_lshl_add_u64 v[4:5], v[6:7], 0, v[4:5]
	v_mov_b32_e32 v6, 0
	v_mov_b32_e32 v7, 0
	v_mul_f32_e32 v16, 0x3d000000, v195
	v_mul_f32_e32 v16, 0x42000000, v16
	v_pk_mul_f32 v[20:21], v[124:125], v[16:17] op_sel_hi:[1,0]
	v_pk_mul_f32 v[24:25], v[120:121], v[16:17] op_sel_hi:[1,0]
	v_pk_mul_f32 v[18:19], v[126:127], v[16:17] op_sel_hi:[1,0]
	v_pk_mul_f32 v[22:23], v[122:123], v[16:17] op_sel_hi:[1,0]
	v_pk_mul_f32 v[26:27], v[118:119], v[16:17] op_sel_hi:[1,0]
	v_pk_mul_f32 v[28:29], v[116:117], v[16:17] op_sel_hi:[1,0]
	v_pk_mul_f32 v[30:31], v[114:115], v[16:17] op_sel_hi:[1,0]
	v_pk_mul_f32 v[16:17], v[112:113], v[16:17] op_sel_hi:[1,0]
	v_med3_f32 v20, v20, s61, v192
	v_med3_f32 v24, v24, s61, v192
	v_med3_f32 v21, v21, s61, v192
	v_med3_f32 v25, v25, s61, v192
	v_med3_f32 v28, v28, s61, v192
	v_med3_f32 v16, v16, s61, v192
	v_med3_f32 v29, v29, s61, v192
	v_med3_f32 v17, v17, s61, v192
	v_cvt_pk_fp8_f32 v8, v20, v21
	v_cvt_pk_fp8_f32 v9, v24, v25
	v_cvt_pk_fp8_f32 v10, v28, v29
	v_cvt_pk_fp8_f32 v11, v16, v17
	v_med3_f32 v18, v18, s61, v192
	v_med3_f32 v22, v22, s61, v192
	v_med3_f32 v19, v19, s61, v192
	v_med3_f32 v23, v23, s61, v192
	v_med3_f32 v26, v26, s61, v192
	v_med3_f32 v30, v30, s61, v192
	v_med3_f32 v27, v27, s61, v192
	v_med3_f32 v31, v31, s61, v192
	v_cvt_pk_fp8_f32 v8, v18, v19 op_sel:[0,0,1]
	v_cvt_pk_fp8_f32 v9, v22, v23 op_sel:[0,0,1]
	v_cvt_pk_fp8_f32 v10, v26, v27 op_sel:[0,0,1]
	v_cvt_pk_fp8_f32 v11, v30, v31 op_sel:[0,0,1]
	global_store_dwordx2 v[12:13], v[8:9], off
	global_store_dwordx2 v[12:13], v[10:11], off offset:128
	v_mov_b32_e32 v8, 0
	v_mov_b32_e32 v9, 0
	v_mov_b32_e32 v10, 0
	v_mov_b32_e32 v11, 0
	v_mul_f32_e32 v12, 0x3d000000, v196
	v_mul_f32_e32 v12, 0x42000000, v12
	v_pk_mul_f32 v[16:17], v[108:109], v[12:13] op_sel_hi:[1,0]
	v_pk_mul_f32 v[20:21], v[104:105], v[12:13] op_sel_hi:[1,0]
	v_pk_mul_f32 v[14:15], v[110:111], v[12:13] op_sel_hi:[1,0]
	v_pk_mul_f32 v[18:19], v[106:107], v[12:13] op_sel_hi:[1,0]
	v_pk_mul_f32 v[22:23], v[102:103], v[12:13] op_sel_hi:[1,0]
	v_pk_mul_f32 v[24:25], v[100:101], v[12:13] op_sel_hi:[1,0]
	v_pk_mul_f32 v[26:27], v[98:99], v[12:13] op_sel_hi:[1,0]
	v_pk_mul_f32 v[12:13], v[96:97], v[12:13] op_sel_hi:[1,0]
	v_med3_f32 v16, v16, s61, v192
	v_med3_f32 v20, v20, s61, v192
	v_med3_f32 v17, v17, s61, v192
	v_med3_f32 v21, v21, s61, v192
	v_med3_f32 v24, v24, s61, v192
	v_med3_f32 v12, v12, s61, v192
	v_med3_f32 v25, v25, s61, v192
	v_med3_f32 v13, v13, s61, v192
	v_cvt_pk_fp8_f32 v8, v16, v17
	v_cvt_pk_fp8_f32 v9, v20, v21
	v_cvt_pk_fp8_f32 v10, v24, v25
	v_cvt_pk_fp8_f32 v11, v12, v13
	v_med3_f32 v14, v14, s61, v192
	v_med3_f32 v18, v18, s61, v192
	v_med3_f32 v15, v15, s61, v192
	v_med3_f32 v19, v19, s61, v192
	v_med3_f32 v22, v22, s61, v192
	v_med3_f32 v26, v26, s61, v192
	v_med3_f32 v23, v23, s61, v192
	v_med3_f32 v27, v27, s61, v192
	v_cvt_pk_fp8_f32 v8, v14, v15 op_sel:[0,0,1]
	v_cvt_pk_fp8_f32 v9, v18, v19 op_sel:[0,0,1]
	v_cvt_pk_fp8_f32 v10, v22, v23 op_sel:[0,0,1]
	v_cvt_pk_fp8_f32 v11, v26, v27 op_sel:[0,0,1]
	global_store_dwordx2 v[4:5], v[8:9], off
	global_store_dwordx2 v[4:5], v[10:11], off offset:128
	v_mov_b32_e32 v4, 0
	v_mov_b32_e32 v5, 0
	v_lshl_add_u64 v[8:9], v[2:3], 0, s[12:13]
	v_mul_f32_e32 v10, 0x3d000000, v197
	v_mul_f32_e32 v10, 0x42000000, v10
	v_pk_mul_f32 v[14:15], v[92:93], v[10:11] op_sel_hi:[1,0]
	v_pk_mul_f32 v[18:19], v[88:89], v[10:11] op_sel_hi:[1,0]
	v_pk_mul_f32 v[12:13], v[94:95], v[10:11] op_sel_hi:[1,0]
	v_pk_mul_f32 v[16:17], v[90:91], v[10:11] op_sel_hi:[1,0]
	v_pk_mul_f32 v[20:21], v[86:87], v[10:11] op_sel_hi:[1,0]
	v_pk_mul_f32 v[22:23], v[84:85], v[10:11] op_sel_hi:[1,0]
	v_pk_mul_f32 v[24:25], v[82:83], v[10:11] op_sel_hi:[1,0]
	v_pk_mul_f32 v[10:11], v[80:81], v[10:11] op_sel_hi:[1,0]
	v_med3_f32 v14, v14, s61, v192
	v_med3_f32 v18, v18, s61, v192
	v_med3_f32 v15, v15, s61, v192
	v_med3_f32 v19, v19, s61, v192
	v_med3_f32 v22, v22, s61, v192
	v_med3_f32 v10, v10, s61, v192
	v_med3_f32 v23, v23, s61, v192
	v_med3_f32 v11, v11, s61, v192
	v_cvt_pk_fp8_f32 v4, v14, v15
	v_cvt_pk_fp8_f32 v5, v18, v19
	v_cvt_pk_fp8_f32 v6, v22, v23
	v_cvt_pk_fp8_f32 v7, v10, v11
	v_med3_f32 v12, v12, s61, v192
	v_med3_f32 v16, v16, s61, v192
	v_med3_f32 v13, v13, s61, v192
	v_med3_f32 v17, v17, s61, v192
	v_med3_f32 v20, v20, s61, v192
	v_med3_f32 v24, v24, s61, v192
	v_med3_f32 v21, v21, s61, v192
	v_med3_f32 v25, v25, s61, v192
	v_cvt_pk_fp8_f32 v4, v12, v13 op_sel:[0,0,1]
	v_cvt_pk_fp8_f32 v5, v16, v17 op_sel:[0,0,1]
	v_cvt_pk_fp8_f32 v6, v20, v21 op_sel:[0,0,1]
	v_cvt_pk_fp8_f32 v7, v24, v25 op_sel:[0,0,1]
	v_add_co_u32_e32 v10, vcc, s0, v2
	s_mov_b32 s0, s22
	s_nop 0
	v_addc_co_u32_e32 v11, vcc, 0, v3, vcc
	global_store_dwordx2 v[10:11], v[4:5], off
	global_store_dwordx2 v[8:9], v[6:7], off offset:128
	v_mov_b32_e32 v4, 0
	v_mov_b32_e32 v5, 0
	v_mov_b32_e32 v6, 0
	v_mov_b32_e32 v7, 0
	v_lshl_add_u64 v[8:9], v[2:3], 0, s[14:15]
	v_mul_f32_e32 v10, 0x3d000000, v198
	v_mul_f32_e32 v10, 0x42000000, v10
	v_pk_mul_f32 v[14:15], v[76:77], v[10:11] op_sel_hi:[1,0]
	v_pk_mul_f32 v[18:19], v[72:73], v[10:11] op_sel_hi:[1,0]
	v_pk_mul_f32 v[12:13], v[78:79], v[10:11] op_sel_hi:[1,0]
	v_pk_mul_f32 v[16:17], v[74:75], v[10:11] op_sel_hi:[1,0]
	v_pk_mul_f32 v[20:21], v[70:71], v[10:11] op_sel_hi:[1,0]
	v_pk_mul_f32 v[22:23], v[68:69], v[10:11] op_sel_hi:[1,0]
	v_pk_mul_f32 v[24:25], v[66:67], v[10:11] op_sel_hi:[1,0]
	v_pk_mul_f32 v[10:11], v[64:65], v[10:11] op_sel_hi:[1,0]
	v_med3_f32 v14, v14, s61, v192
	v_med3_f32 v18, v18, s61, v192
	v_med3_f32 v15, v15, s61, v192
	v_med3_f32 v19, v19, s61, v192
	v_med3_f32 v22, v22, s61, v192
	v_med3_f32 v10, v10, s61, v192
	v_med3_f32 v23, v23, s61, v192
	v_med3_f32 v11, v11, s61, v192
	v_cvt_pk_fp8_f32 v4, v14, v15
	v_cvt_pk_fp8_f32 v5, v18, v19
	v_cvt_pk_fp8_f32 v6, v22, v23
	v_cvt_pk_fp8_f32 v7, v10, v11
	v_med3_f32 v12, v12, s61, v192
	v_med3_f32 v16, v16, s61, v192
	v_med3_f32 v13, v13, s61, v192
	v_med3_f32 v17, v17, s61, v192
	v_med3_f32 v20, v20, s61, v192
	v_med3_f32 v24, v24, s61, v192
	v_med3_f32 v21, v21, s61, v192
	v_med3_f32 v25, v25, s61, v192
	v_cvt_pk_fp8_f32 v4, v12, v13 op_sel:[0,0,1]
	v_cvt_pk_fp8_f32 v5, v16, v17 op_sel:[0,0,1]
	v_cvt_pk_fp8_f32 v6, v20, v21 op_sel:[0,0,1]
	v_cvt_pk_fp8_f32 v7, v24, v25 op_sel:[0,0,1]
	v_add_co_u32_e32 v10, vcc, s62, v2
	s_nop 1
	v_addc_co_u32_e32 v11, vcc, 0, v3, vcc
	global_store_dwordx2 v[10:11], v[4:5], off
	global_store_dwordx2 v[8:9], v[6:7], off offset:128
	v_mov_b32_e32 v4, 0
	v_mov_b32_e32 v5, 0
	v_mov_b32_e32 v6, 0
	v_mov_b32_e32 v7, 0
	v_lshl_add_u64 v[8:9], v[2:3], 0, s[16:17]
	v_mul_f32_e32 v10, 0x3d000000, v199
	v_mul_f32_e32 v10, 0x42000000, v10
	v_pk_mul_f32 v[14:15], v[60:61], v[10:11] op_sel_hi:[1,0]
	v_pk_mul_f32 v[18:19], v[56:57], v[10:11] op_sel_hi:[1,0]
	v_pk_mul_f32 v[12:13], v[62:63], v[10:11] op_sel_hi:[1,0]
	v_pk_mul_f32 v[16:17], v[58:59], v[10:11] op_sel_hi:[1,0]
	v_pk_mul_f32 v[20:21], v[54:55], v[10:11] op_sel_hi:[1,0]
	v_pk_mul_f32 v[22:23], v[52:53], v[10:11] op_sel_hi:[1,0]
	v_pk_mul_f32 v[24:25], v[50:51], v[10:11] op_sel_hi:[1,0]
	v_pk_mul_f32 v[10:11], v[48:49], v[10:11] op_sel_hi:[1,0]
	v_med3_f32 v14, v14, s61, v192
	v_med3_f32 v18, v18, s61, v192
	v_med3_f32 v15, v15, s61, v192
	v_med3_f32 v19, v19, s61, v192
	v_med3_f32 v22, v22, s61, v192
	v_med3_f32 v10, v10, s61, v192
	v_med3_f32 v23, v23, s61, v192
	v_med3_f32 v11, v11, s61, v192
	v_cvt_pk_fp8_f32 v4, v14, v15
	v_cvt_pk_fp8_f32 v5, v18, v19
	v_cvt_pk_fp8_f32 v6, v22, v23
	v_cvt_pk_fp8_f32 v7, v10, v11
	v_med3_f32 v12, v12, s61, v192
	v_med3_f32 v16, v16, s61, v192
	v_med3_f32 v13, v13, s61, v192
	v_med3_f32 v17, v17, s61, v192
	v_med3_f32 v20, v20, s61, v192
	v_med3_f32 v24, v24, s61, v192
	v_med3_f32 v21, v21, s61, v192
	v_med3_f32 v25, v25, s61, v192
	v_cvt_pk_fp8_f32 v4, v12, v13 op_sel:[0,0,1]
	v_cvt_pk_fp8_f32 v5, v16, v17 op_sel:[0,0,1]
	v_cvt_pk_fp8_f32 v6, v20, v21 op_sel:[0,0,1]
	v_cvt_pk_fp8_f32 v7, v24, v25 op_sel:[0,0,1]
	v_add_co_u32_e32 v10, vcc, s63, v2
	s_nop 1
	v_addc_co_u32_e32 v11, vcc, 0, v3, vcc
	global_store_dwordx2 v[10:11], v[4:5], off
	global_store_dwordx2 v[8:9], v[6:7], off offset:128
	v_mov_b32_e32 v0, 0
	v_mov_b32_e32 v1, 0
	v_mov_b32_e32 v4, 0
	v_mov_b32_e32 v5, 0
	v_lshl_add_u64 v[6:7], v[2:3], 0, s[18:19]
	v_add_co_u32_e64 v2, s[6:7], s64, v2
	s_and_b64 vcc, exec, s[10:11]
	s_nop 0
	v_addc_co_u32_e64 v3, s[6:7], 0, v3, s[6:7]
	v_mul_f32_e32 v8, 0x3d000000, v200
	v_mul_f32_e32 v8, 0x42000000, v8
	v_pk_mul_f32 v[12:13], v[44:45], v[8:9] op_sel_hi:[1,0]
	v_pk_mul_f32 v[16:17], v[40:41], v[8:9] op_sel_hi:[1,0]
	v_pk_mul_f32 v[10:11], v[46:47], v[8:9] op_sel_hi:[1,0]
	v_pk_mul_f32 v[14:15], v[42:43], v[8:9] op_sel_hi:[1,0]
	v_pk_mul_f32 v[18:19], v[38:39], v[8:9] op_sel_hi:[1,0]
	v_pk_mul_f32 v[20:21], v[36:37], v[8:9] op_sel_hi:[1,0]
	v_pk_mul_f32 v[22:23], v[34:35], v[8:9] op_sel_hi:[1,0]
	v_pk_mul_f32 v[8:9], v[32:33], v[8:9] op_sel_hi:[1,0]
	v_med3_f32 v12, v12, s61, v192
	v_med3_f32 v16, v16, s61, v192
	v_med3_f32 v13, v13, s61, v192
	v_med3_f32 v17, v17, s61, v192
	v_med3_f32 v20, v20, s61, v192
	v_med3_f32 v8, v8, s61, v192
	v_med3_f32 v21, v21, s61, v192
	v_med3_f32 v9, v9, s61, v192
	v_cvt_pk_fp8_f32 v0, v12, v13
	v_cvt_pk_fp8_f32 v1, v16, v17
	v_cvt_pk_fp8_f32 v4, v20, v21
	v_cvt_pk_fp8_f32 v5, v8, v9
	v_med3_f32 v10, v10, s61, v192
	v_med3_f32 v14, v14, s61, v192
	v_med3_f32 v11, v11, s61, v192
	v_med3_f32 v15, v15, s61, v192
	v_med3_f32 v18, v18, s61, v192
	v_med3_f32 v22, v22, s61, v192
	v_med3_f32 v19, v19, s61, v192
	v_med3_f32 v23, v23, s61, v192
	v_cvt_pk_fp8_f32 v0, v10, v11 op_sel:[0,0,1]
	v_cvt_pk_fp8_f32 v1, v14, v15 op_sel:[0,0,1]
	v_cvt_pk_fp8_f32 v4, v18, v19 op_sel:[0,0,1]
	v_cvt_pk_fp8_f32 v5, v22, v23 op_sel:[0,0,1]
	global_store_dwordx2 v[2:3], v[0:1], off
	global_store_dwordx2 v[6:7], v[4:5], off offset:128
	s_cbranch_vccz .LBB0_3024
	s_waitcnt vmcnt(0)
	s_cmpk_gt_u32 s40, 0xff
	v_readlane_b32 s58, v242, 45
	v_readlane_b32 s59, v242, 46
	s_cbranch_scc1 .LBB0_3031
	s_barrier

.LBB0_3161:
	s_or_b64 exec, exec, s[0:1]
	v_readlane_b32 s0, v242, 1
	s_waitcnt lgkmcnt(0)
	s_barrier
	s_nop 0
	s_mov_b32 s2, 0
	v_readlane_b32 s1, v242, 2
	s_load_dwordx4 s[12:15], s[0:1], s2 offset:0xe8
	s_load_dwordx2 s[4:5], s[0:1], s2 offset:0xf8
	s_nop 0
	s_load_dwordx2 s[0:1], s[0:1], s2 offset:0x108
	v_readlane_b32 s2, v242, 37
	v_mov_b32_e32 v140, v208
	v_readlane_b32 s3, v242, 38
	s_and_b64 vcc, exec, s[2:3]
	v_readfirstlane_b32 s33, v140
	s_cbranch_vccnz .LBB0_3173
	v_lshlrev_b32_e32 v0, 4, v140
	v_add_u32_e32 v1, 0x2000, v0
	v_ashrrev_i32_e32 v2, 31, v1
	v_lshrrev_b32_e32 v2, 22, v2
	v_add_u32_e32 v2, v1, v2
	v_ashrrev_i32_e32 v2, 10, v2
	v_mul_i32_i24_e32 v3, 0x400, v2
	v_sub_u32_e32 v1, v1, v3
	v_lshrrev_b32_e32 v3, 4, v1
	v_bitop3_b32 v1, v3, v1, 32 bitop3:0x6c
	v_ashrrev_i32_e32 v3, 31, v1
	v_lshrrev_b32_e32 v3, 26, v3
	v_add_u32_e32 v3, v1, v3
	v_lshlrev_b32_e32 v5, 3, v2
	v_ashrrev_i32_e32 v4, 6, v3
	v_and_b32_e32 v5, -16, v5
	v_and_b32_e32 v3, 0xc0, v3
	v_add_u32_e32 v5, v4, v5
	v_sub_u32_e32 v1, v1, v3
	v_mov_b32_e32 v3, 1
	v_and_b32_e32 v4, 3, v4
	s_mov_b32 s2, 0x1fffe0
	v_lshrrev_b32_e32 v6, 2, v5
	v_lshlrev_b32_e32 v7, 1, v5
	v_lshlrev_b32_e32 v2, 5, v2
	v_ashrrev_i16_sdwa v1, v3, sext(v1) dst_sel:DWORD dst_unused:UNUSED_PAD src0_sel:DWORD src1_sel:BYTE_0
	v_and_or_b32 v4, v5, s2, v4
	v_and_b32_e32 v6, 4, v6
	v_and_b32_e32 v7, 24, v7
	v_and_b32_e32 v2, 32, v2
	v_bfe_i32 v1, v1, 0, 16
	v_or3_b32 v4, v4, v6, v7
	v_add_lshl_u32 v1, v2, v1, 1
	v_lshl_add_u32 v128, v4, 11, v1
	v_lshl_add_u32 v130, v5, 11, v1
	v_bfe_i32 v1, v140, 27, 1
	v_lshrrev_b32_e32 v1, 22, v1
	v_add_u32_e32 v1, v0, v1
	v_and_b32_e32 v1, 0xfffffc00, v1
	v_sub_u32_e32 v0, v0, v1
	v_lshrrev_b32_e32 v1, 4, v0
	v_ashrrev_i32_e32 v4, 31, v140
	v_bitop3_b32 v0, v1, v0, 32 bitop3:0x6c
	v_lshrrev_b32_e32 v4, 26, v4
	v_ashrrev_i32_e32 v1, 31, v0
	v_add_u32_e32 v4, v140, v4
	s_waitcnt lgkmcnt(0)
	s_add_u32 s42, s0, 0xdbff000
	v_lshrrev_b32_e32 v1, 26, v1
	v_ashrrev_i32_e32 v4, 6, v4
	s_addc_u32 s43, s1, 0
	v_add_u32_e32 v1, v0, v1
	v_lshlrev_b32_e32 v5, 3, v4
	s_add_u32 s44, s0, 0x20ef000
	v_ashrrev_i32_e32 v2, 6, v1
	v_and_b32_e32 v5, -16, v5
	v_readlane_b32 s6, v242, 0
	s_addc_u32 s45, s1, 0
	v_add_u32_e32 v5, v2, v5
	v_and_b32_e32 v2, 3, v2
	s_ashr_i32 s46, s6, 31
	v_and_or_b32 v2, v5, s2, v2
	s_lshr_b32 s2, s46, 29
	s_add_i32 s2, s6, s2
	s_ashr_i32 s7, s33, 6
	s_ashr_i32 s3, s2, 3
	s_and_b32 s2, s2, -8
	s_ashr_i32 s8, s33, 8
	s_lshl_b32 s9, s7, 10
	s_sub_i32 s2, s6, s2
	s_cmp_lt_i32 s2, 0
	s_movk_i32 s47, 0x89
	s_cselect_b32 s6, s47, 0x88
	s_mul_i32 s2, s6, s2
	s_add_i32 s2, s2, s3
	s_ashr_i32 s3, s2, 31
	s_lshr_b32 s3, s3, 26
	s_add_i32 s3, s2, s3
	s_ashr_i32 s6, s3, 6
	s_andn2_b32 s3, s3, 63
	s_sub_i32 s2, s2, s3
	s_bfe_i32 s3, s2, 0x80000
	s_bfe_u32 s3, s3, 0x3000c
	s_add_i32 s3, s2, s3
	s_lshl_b32 s10, s6, 3
	s_bfe_i32 s6, s3, 0x80000
	s_and_b32 s3, s3, 0xf8
	s_sub_i32 s2, s2, s3
	s_sext_i32_i16 s6, s6
	s_sext_i32_i8 s2, s2
	s_lshr_b32 s6, s6, 3
	s_add_i32 s18, s10, s2
	v_and_b32_e32 v1, 0xc0, v1
	s_ashr_i32 s19, s18, 31
	s_bfe_i64 s[10:11], s[6:7], 0x100000
	v_sub_u32_e32 v0, v0, v1
	s_lshl_b64 s[2:3], s[18:19], 19
	s_lshl_b64 s[10:11], s[10:11], 19
	v_lshrrev_b32_e32 v6, 2, v5
	v_lshlrev_b32_e32 v7, 1, v5
	v_lshlrev_b32_e32 v4, 5, v4
	v_ashrrev_i16_sdwa v0, v3, sext(v0) dst_sel:DWORD dst_unused:UNUSED_PAD src0_sel:DWORD src1_sel:BYTE_0
	s_add_u32 s20, s44, s10
	v_and_b32_e32 v6, 4, v6
	v_and_b32_e32 v7, 24, v7
	v_and_b32_e32 v4, 32, v4
	v_bfe_i32 v0, v0, 0, 16
	s_addc_u32 s21, s45, s11
	s_add_i32 s19, s9, 0
	v_or3_b32 v2, v2, v6, v7
	v_add_lshl_u32 v0, v4, v0, 1
	s_add_i32 s48, s19, 0x10000
	s_add_i32 s49, s19, 0x12000
	v_lshl_add_u32 v132, v2, 11, v0
	v_lshl_add_u32 v134, v5, 11, v0
	v_mov_b32_e32 v0, 0x7f
	s_mov_b64 s[10:11], s[20:21]
	s_mov_b32 m0, s48
	s_add_u32 s24, s42, s2
	s_addc_u32 s25, s43, s3
	global_load_lds_dwordx4 v132, s[10:11]
	s_mov_b32 m0, s49
	s_mov_b64 s[2:3], s[24:25]
	global_load_lds_dwordx4 v128, s[10:11]
	s_mov_b32 m0, s19
	s_add_i32 s50, s19, 0x2000
	v_mov_b32_e32 v133, 0
	global_load_lds_dwordx4 v134, s[2:3]
	s_mov_b32 m0, s50
	s_mov_b32 s55, 0
	global_load_lds_dwordx4 v130, s[2:3]
	s_add_u32 s2, s20, 0x40000
	s_addc_u32 s3, s21, 0
	s_add_i32 s51, s19, 0x14000
	s_mov_b32 m0, s51
	s_add_i32 s52, s19, 0x16000
	v_mov_b32_e32 v129, v133
	global_load_lds_dwordx4 v132, s[2:3]
	s_mov_b32 m0, s52
	v_mov_b32_e32 v135, v133
	global_load_lds_dwordx4 v128, s[2:3]
	s_add_u32 s2, s24, 0x40000
	s_addc_u32 s3, s25, 0
	s_add_i32 s53, s19, 0x4000
	s_mov_b32 m0, s53
	s_add_i32 s54, s19, 0x6000
	s_cmp_lg_u32 s8, 1
	global_load_lds_dwordx4 v134, s[2:3]
	s_mov_b32 m0, s54
	v_mov_b32_e32 v131, v133
	global_load_lds_dwordx4 v130, s[2:3]
	s_cbranch_scc1 .LBB0_3164
	s_barrier

.LBB0_3168:
	s_add_u32 s36, s34, 0x100
	ds_read_b128 v[158:161], v141
	ds_read_b128 v[162:165], v142
	ds_read_b128 v[166:169], v149
	ds_read_b128 v[170:173], v150
	s_addc_u32 s37, s35, 0
	s_and_b32 s68, s36, 0x700
	s_add_u32 s69, s20, s68
	s_addc_u32 s70, s21, 0
	s_cmp_eq_u32 s67, 12
	s_cselect_b64 s[40:41], -1, 0
	s_and_b64 s[38:39], s[40:41], exec
	s_cselect_b32 s39, s23, s70
	s_cselect_b32 s38, s27, s69
	s_cselect_b32 s69, 0, 0
	s_cselect_b32 s68, 0, s68
	s_add_u32 s34, s24, s34
	s_addc_u32 s35, s25, s35
	s_add_u32 s34, s34, 0x40080
	s_addc_u32 s35, s35, 0
	ds_read_b128 v[174:177], v157
	ds_read_b128 v[178:181], v157 offset:1024
	ds_read_b128 v[182:185], v157 offset:2048
	ds_read_b128 v[186:189], v157 offset:3072
	ds_read_b128 v[190:193], v157 offset:4096
	ds_read_b128 v[194:197], v157 offset:5120
	ds_read_b128 v[198:201], v157 offset:6144
	ds_read_b128 v[202:205], v157 offset:7168
	s_add_i32 m0, s19, 0xc000
	s_nop 0
	global_load_lds_dwordx4 v134, s[34:35]
	s_add_i32 m0, s19, 0xe000
	s_nop 0
	global_load_lds_dwordx4 v130, s[34:35]
	s_waitcnt lgkmcnt(8)
	s_nop 0
	s_barrier
	s_waitcnt lgkmcnt(0)
	s_setprio 1
	s_waitcnt lgkmcnt(0)
	v_mfma_f32_16x16x32_bf16 v[124:127], v[158:161], v[174:177], v[124:127]
	v_mfma_f32_16x16x32_bf16 v[120:123], v[166:169], v[174:177], v[120:123]
	v_mfma_f32_16x16x32_bf16 v[116:119], v[158:161], v[182:185], v[116:119]
	v_mfma_f32_16x16x32_bf16 v[108:111], v[166:169], v[182:185], v[108:111]
	v_mfma_f32_16x16x32_bf16 v[100:103], v[158:161], v[190:193], v[100:103]
	v_mfma_f32_16x16x32_bf16 v[92:95], v[166:169], v[190:193], v[92:95]
	v_mfma_f32_16x16x32_bf16 v[84:87], v[158:161], v[198:201], v[84:87]
	v_mfma_f32_16x16x32_bf16 v[76:79], v[166:169], v[198:201], v[76:79]
	v_mfma_f32_16x16x32_bf16 v[124:127], v[162:165], v[178:181], v[124:127]
	v_mfma_f32_16x16x32_bf16 v[120:123], v[170:173], v[178:181], v[120:123]
	v_mfma_f32_16x16x32_bf16 v[116:119], v[162:165], v[186:189], v[116:119]
	v_mfma_f32_16x16x32_bf16 v[108:111], v[170:173], v[186:189], v[108:111]
	v_mfma_f32_16x16x32_bf16 v[100:103], v[162:165], v[194:197], v[100:103]
	v_mfma_f32_16x16x32_bf16 v[92:95], v[170:173], v[194:197], v[92:95]
	v_mfma_f32_16x16x32_bf16 v[84:87], v[162:165], v[202:205], v[84:87]
	v_mfma_f32_16x16x32_bf16 v[76:79], v[170:173], v[202:205], v[76:79]
	s_setprio 0
	s_barrier
	s_mov_b64 s[34:35], s[38:39]
	s_mov_b32 m0, s48
	ds_read_b128 v[210:213], v143
	ds_read_b128 v[214:217], v144
	ds_read_b128 v[218:221], v151
	ds_read_b128 v[222:225], v152
	s_nop 0
	global_load_lds_dwordx4 v132, s[34:35]
	s_mov_b32 m0, s49
	s_nop 0
	global_load_lds_dwordx4 v128, s[34:35]
	s_nop 0
	s_barrier
	s_waitcnt lgkmcnt(0)
	s_setprio 1
	s_waitcnt lgkmcnt(0)
	v_mfma_f32_16x16x32_bf16 v[112:115], v[210:213], v[174:177], v[112:115]
	v_mfma_f32_16x16x32_bf16 v[104:107], v[218:221], v[174:177], v[104:107]
	v_mfma_f32_16x16x32_bf16 v[96:99], v[210:213], v[182:185], v[96:99]
	v_mfma_f32_16x16x32_bf16 v[88:91], v[218:221], v[182:185], v[88:91]
	v_mfma_f32_16x16x32_bf16 v[80:83], v[210:213], v[190:193], v[80:83]
	v_mfma_f32_16x16x32_bf16 v[72:75], v[218:221], v[190:193], v[72:75]
	v_mfma_f32_16x16x32_bf16 v[68:71], v[210:213], v[198:201], v[68:71]
	v_mfma_f32_16x16x32_bf16 v[64:67], v[218:221], v[198:201], v[64:67]
	v_mfma_f32_16x16x32_bf16 v[112:115], v[214:217], v[178:181], v[112:115]
	v_mfma_f32_16x16x32_bf16 v[104:107], v[222:225], v[178:181], v[104:107]
	v_mfma_f32_16x16x32_bf16 v[96:99], v[214:217], v[186:189], v[96:99]
	v_mfma_f32_16x16x32_bf16 v[88:91], v[222:225], v[186:189], v[88:91]
	v_mfma_f32_16x16x32_bf16 v[80:83], v[214:217], v[194:197], v[80:83]
	v_mfma_f32_16x16x32_bf16 v[72:75], v[222:225], v[194:197], v[72:75]
	v_mfma_f32_16x16x32_bf16 v[68:71], v[214:217], v[202:205], v[68:71]
	v_mfma_f32_16x16x32_bf16 v[64:67], v[222:225], v[202:205], v[64:67]
	s_setprio 0
	s_and_b64 s[34:35], s[10:11], s[40:41]
	s_and_b64 s[34:35], s[34:35], exec
	s_cselect_b32 s34, s28, s24
	s_cselect_b32 s35, s29, s25
	s_add_u32 s34, s34, s68
	s_addc_u32 s35, s35, s69
	s_mov_b64 s[40:41], s[34:35]
	s_mov_b32 m0, s19
	s_barrier
	ds_read_b128 v[174:177], v157 offset:16384
	ds_read_b128 v[178:181], v157 offset:17408
	ds_read_b128 v[182:185], v157 offset:18432
	ds_read_b128 v[186:189], v157 offset:19456
	ds_read_b128 v[190:193], v157 offset:20480
	ds_read_b128 v[194:197], v157 offset:21504
	ds_read_b128 v[198:201], v157 offset:22528
	ds_read_b128 v[202:205], v157 offset:23552
	s_nop 0
	global_load_lds_dwordx4 v134, s[40:41]
	s_mov_b32 m0, s50
	s_nop 0
	global_load_lds_dwordx4 v130, s[40:41]
	s_nop 0
	s_barrier
	s_waitcnt lgkmcnt(0)
	s_setprio 1
	s_waitcnt lgkmcnt(0)
	v_mfma_f32_16x16x32_bf16 v[60:63], v[158:161], v[174:177], v[60:63]
	v_mfma_f32_16x16x32_bf16 v[56:59], v[166:169], v[174:177], v[56:59]
	v_mfma_f32_16x16x32_bf16 v[52:55], v[158:161], v[182:185], v[52:55]
	v_mfma_f32_16x16x32_bf16 v[48:51], v[166:169], v[182:185], v[48:51]
	v_mfma_f32_16x16x32_bf16 v[36:39], v[158:161], v[190:193], v[36:39]
	v_mfma_f32_16x16x32_bf16 v[32:35], v[166:169], v[190:193], v[32:35]
	v_mfma_f32_16x16x32_bf16 v[20:23], v[158:161], v[198:201], v[20:23]
	v_mfma_f32_16x16x32_bf16 v[16:19], v[166:169], v[198:201], v[16:19]
	v_mfma_f32_16x16x32_bf16 v[60:63], v[162:165], v[178:181], v[60:63]
	v_mfma_f32_16x16x32_bf16 v[56:59], v[170:173], v[178:181], v[56:59]
	v_mfma_f32_16x16x32_bf16 v[52:55], v[162:165], v[186:189], v[52:55]
	v_mfma_f32_16x16x32_bf16 v[48:51], v[170:173], v[186:189], v[48:51]
	v_mfma_f32_16x16x32_bf16 v[36:39], v[162:165], v[194:197], v[36:39]
	v_mfma_f32_16x16x32_bf16 v[32:35], v[170:173], v[194:197], v[32:35]
	v_mfma_f32_16x16x32_bf16 v[20:23], v[162:165], v[202:205], v[20:23]
	v_mfma_f32_16x16x32_bf16 v[16:19], v[170:173], v[202:205], v[16:19]
	s_setprio 0
	s_barrier
	s_add_u32 s40, s38, 0x40000
	s_addc_u32 s41, s39, 0
	s_mov_b32 m0, s51
	s_nop 0
	global_load_lds_dwordx4 v132, s[40:41]
	s_mov_b32 m0, s52
	s_nop 0
	global_load_lds_dwordx4 v128, s[40:41]
	s_waitcnt vmcnt(6)
	s_barrier
	s_setprio 1
	v_mfma_f32_16x16x32_bf16 v[44:47], v[210:213], v[174:177], v[44:47]
	v_mfma_f32_16x16x32_bf16 v[40:43], v[218:221], v[174:177], v[40:43]
	v_mfma_f32_16x16x32_bf16 v[28:31], v[210:213], v[182:185], v[28:31]
	v_mfma_f32_16x16x32_bf16 v[24:27], v[218:221], v[182:185], v[24:27]
	v_mfma_f32_16x16x32_bf16 v[12:15], v[210:213], v[190:193], v[12:15]
	v_mfma_f32_16x16x32_bf16 v[8:11], v[218:221], v[190:193], v[8:11]
	v_mfma_f32_16x16x32_bf16 v[4:7], v[210:213], v[198:201], v[4:7]
	v_mfma_f32_16x16x32_bf16 v[0:3], v[218:221], v[198:201], v[0:3]
	v_mfma_f32_16x16x32_bf16 v[44:47], v[214:217], v[178:181], v[44:47]
	v_mfma_f32_16x16x32_bf16 v[40:43], v[222:225], v[178:181], v[40:43]
	v_mfma_f32_16x16x32_bf16 v[28:31], v[214:217], v[186:189], v[28:31]
	v_mfma_f32_16x16x32_bf16 v[24:27], v[222:225], v[186:189], v[24:27]
	v_mfma_f32_16x16x32_bf16 v[12:15], v[214:217], v[194:197], v[12:15]
	v_mfma_f32_16x16x32_bf16 v[8:11], v[222:225], v[194:197], v[8:11]
	v_mfma_f32_16x16x32_bf16 v[4:7], v[214:217], v[202:205], v[4:7]
	v_mfma_f32_16x16x32_bf16 v[0:3], v[222:225], v[202:205], v[0:3]
	s_setprio 0
	s_barrier
	ds_read_b128 v[158:161], v145
	ds_read_b128 v[162:165], v146
	ds_read_b128 v[166:169], v153
	ds_read_b128 v[170:173], v154
	s_add_u32 s40, s34, 0x40000
	s_addc_u32 s41, s35, 0
	s_mov_b32 m0, s53
	ds_read_b128 v[174:177], v157 offset:32768
	ds_read_b128 v[178:181], v157 offset:33792
	ds_read_b128 v[182:185], v157 offset:34816
	ds_read_b128 v[186:189], v157 offset:35840
	ds_read_b128 v[190:193], v157 offset:36864
	ds_read_b128 v[194:197], v157 offset:37888
	ds_read_b128 v[198:201], v157 offset:38912
	ds_read_b128 v[202:205], v157 offset:39936
	s_nop 0
	global_load_lds_dwordx4 v134, s[40:41]
	s_mov_b32 m0, s54
	s_nop 0
	global_load_lds_dwordx4 v130, s[40:41]
	s_waitcnt lgkmcnt(8)
	s_barrier
	s_waitcnt lgkmcnt(0)
	s_setprio 1
	s_waitcnt lgkmcnt(0)
	v_mfma_f32_16x16x32_bf16 v[124:127], v[158:161], v[174:177], v[124:127]
	v_mfma_f32_16x16x32_bf16 v[120:123], v[166:169], v[174:177], v[120:123]
	v_mfma_f32_16x16x32_bf16 v[116:119], v[158:161], v[182:185], v[116:119]
	v_mfma_f32_16x16x32_bf16 v[108:111], v[166:169], v[182:185], v[108:111]
	v_mfma_f32_16x16x32_bf16 v[100:103], v[158:161], v[190:193], v[100:103]
	v_mfma_f32_16x16x32_bf16 v[92:95], v[166:169], v[190:193], v[92:95]
	v_mfma_f32_16x16x32_bf16 v[84:87], v[158:161], v[198:201], v[84:87]
	v_mfma_f32_16x16x32_bf16 v[76:79], v[166:169], v[198:201], v[76:79]
	v_mfma_f32_16x16x32_bf16 v[124:127], v[162:165], v[178:181], v[124:127]
	v_mfma_f32_16x16x32_bf16 v[120:123], v[170:173], v[178:181], v[120:123]
	v_mfma_f32_16x16x32_bf16 v[116:119], v[162:165], v[186:189], v[116:119]
	v_mfma_f32_16x16x32_bf16 v[108:111], v[170:173], v[186:189], v[108:111]
	v_mfma_f32_16x16x32_bf16 v[100:103], v[162:165], v[194:197], v[100:103]
	v_mfma_f32_16x16x32_bf16 v[92:95], v[170:173], v[194:197], v[92:95]
	v_mfma_f32_16x16x32_bf16 v[84:87], v[162:165], v[202:205], v[84:87]
	v_mfma_f32_16x16x32_bf16 v[76:79], v[170:173], v[202:205], v[76:79]
	s_setprio 0
	s_barrier
	s_add_u32 s40, s38, 0x80
	s_addc_u32 s41, s39, 0
	s_mov_b32 m0, s56
	ds_read_b128 v[210:213], v147
	ds_read_b128 v[214:217], v148
	ds_read_b128 v[218:221], v155
	ds_read_b128 v[222:225], v156
	s_nop 0
	global_load_lds_dwordx4 v132, s[40:41]
	s_mov_b32 m0, s57
	s_nop 0
	global_load_lds_dwordx4 v128, s[40:41]
	s_nop 0
	s_barrier
	s_waitcnt lgkmcnt(0)
	s_setprio 1
	s_waitcnt lgkmcnt(0)
	v_mfma_f32_16x16x32_bf16 v[112:115], v[210:213], v[174:177], v[112:115]
	v_mfma_f32_16x16x32_bf16 v[104:107], v[218:221], v[174:177], v[104:107]
	v_mfma_f32_16x16x32_bf16 v[96:99], v[210:213], v[182:185], v[96:99]
	v_mfma_f32_16x16x32_bf16 v[88:91], v[218:221], v[182:185], v[88:91]
	v_mfma_f32_16x16x32_bf16 v[80:83], v[210:213], v[190:193], v[80:83]
	v_mfma_f32_16x16x32_bf16 v[72:75], v[218:221], v[190:193], v[72:75]
	v_mfma_f32_16x16x32_bf16 v[68:71], v[210:213], v[198:201], v[68:71]
	v_mfma_f32_16x16x32_bf16 v[64:67], v[218:221], v[198:201], v[64:67]
	v_mfma_f32_16x16x32_bf16 v[112:115], v[214:217], v[178:181], v[112:115]
	v_mfma_f32_16x16x32_bf16 v[104:107], v[222:225], v[178:181], v[104:107]
	v_mfma_f32_16x16x32_bf16 v[96:99], v[214:217], v[186:189], v[96:99]
	v_mfma_f32_16x16x32_bf16 v[88:91], v[222:225], v[186:189], v[88:91]
	v_mfma_f32_16x16x32_bf16 v[80:83], v[214:217], v[194:197], v[80:83]
	v_mfma_f32_16x16x32_bf16 v[72:75], v[222:225], v[194:197], v[72:75]
	v_mfma_f32_16x16x32_bf16 v[68:71], v[214:217], v[202:205], v[68:71]
	v_mfma_f32_16x16x32_bf16 v[64:67], v[222:225], v[202:205], v[64:67]
	s_setprio 0
	s_add_u32 s34, s34, 0x80
	s_addc_u32 s35, s35, 0
	s_mov_b32 m0, s58
	s_barrier
	ds_read_b128 v[174:177], v157 offset:49152
	ds_read_b128 v[178:181], v157 offset:50176
	ds_read_b128 v[182:185], v157 offset:51200
	ds_read_b128 v[186:189], v157 offset:52224
	ds_read_b128 v[190:193], v157 offset:53248
	ds_read_b128 v[194:197], v157 offset:54272
	ds_read_b128 v[198:201], v157 offset:55296
	ds_read_b128 v[202:205], v157 offset:56320
	s_nop 0
	global_load_lds_dwordx4 v134, s[34:35]
	s_mov_b32 m0, s59
	s_nop 0
	global_load_lds_dwordx4 v130, s[34:35]
	s_nop 0
	s_barrier
	s_waitcnt lgkmcnt(0)
	s_setprio 1
	s_waitcnt lgkmcnt(0)
	v_mfma_f32_16x16x32_bf16 v[60:63], v[158:161], v[174:177], v[60:63]
	v_mfma_f32_16x16x32_bf16 v[56:59], v[166:169], v[174:177], v[56:59]
	v_mfma_f32_16x16x32_bf16 v[52:55], v[158:161], v[182:185], v[52:55]
	v_mfma_f32_16x16x32_bf16 v[48:51], v[166:169], v[182:185], v[48:51]
	v_mfma_f32_16x16x32_bf16 v[36:39], v[158:161], v[190:193], v[36:39]
	v_mfma_f32_16x16x32_bf16 v[32:35], v[166:169], v[190:193], v[32:35]
	v_mfma_f32_16x16x32_bf16 v[20:23], v[158:161], v[198:201], v[20:23]
	v_mfma_f32_16x16x32_bf16 v[16:19], v[166:169], v[198:201], v[16:19]
	v_mfma_f32_16x16x32_bf16 v[60:63], v[162:165], v[178:181], v[60:63]
	v_mfma_f32_16x16x32_bf16 v[56:59], v[170:173], v[178:181], v[56:59]
	v_mfma_f32_16x16x32_bf16 v[52:55], v[162:165], v[186:189], v[52:55]
	v_mfma_f32_16x16x32_bf16 v[48:51], v[170:173], v[186:189], v[48:51]
	v_mfma_f32_16x16x32_bf16 v[36:39], v[162:165], v[194:197], v[36:39]
	v_mfma_f32_16x16x32_bf16 v[32:35], v[170:173], v[194:197], v[32:35]
	v_mfma_f32_16x16x32_bf16 v[20:23], v[162:165], v[202:205], v[20:23]
	v_mfma_f32_16x16x32_bf16 v[16:19], v[170:173], v[202:205], v[16:19]
	s_setprio 0
	s_barrier
	s_add_u32 s34, s38, 0x40080
	s_addc_u32 s35, s39, 0
	s_mov_b32 m0, s60
	s_nop 0
	global_load_lds_dwordx4 v132, s[34:35]
	s_mov_b32 m0, s61
	s_nop 0
	global_load_lds_dwordx4 v128, s[34:35]
	s_waitcnt vmcnt(6)
	s_barrier
	s_setprio 1
	v_mfma_f32_16x16x32_bf16 v[44:47], v[210:213], v[174:177], v[44:47]
	v_mfma_f32_16x16x32_bf16 v[40:43], v[218:221], v[174:177], v[40:43]
	v_mfma_f32_16x16x32_bf16 v[28:31], v[210:213], v[182:185], v[28:31]
	v_mfma_f32_16x16x32_bf16 v[24:27], v[218:221], v[182:185], v[24:27]
	v_mfma_f32_16x16x32_bf16 v[12:15], v[210:213], v[190:193], v[12:15]
	v_mfma_f32_16x16x32_bf16 v[8:11], v[218:221], v[190:193], v[8:11]
	v_mfma_f32_16x16x32_bf16 v[4:7], v[210:213], v[198:201], v[4:7]
	v_mfma_f32_16x16x32_bf16 v[0:3], v[218:221], v[198:201], v[0:3]
	v_mfma_f32_16x16x32_bf16 v[44:47], v[214:217], v[178:181], v[44:47]
	v_mfma_f32_16x16x32_bf16 v[40:43], v[222:225], v[178:181], v[40:43]
	v_mfma_f32_16x16x32_bf16 v[28:31], v[214:217], v[186:189], v[28:31]
	v_mfma_f32_16x16x32_bf16 v[24:27], v[222:225], v[186:189], v[24:27]
	v_mfma_f32_16x16x32_bf16 v[12:15], v[214:217], v[194:197], v[12:15]
	v_mfma_f32_16x16x32_bf16 v[8:11], v[222:225], v[194:197], v[8:11]
	v_mfma_f32_16x16x32_bf16 v[4:7], v[214:217], v[202:205], v[4:7]
	v_mfma_f32_16x16x32_bf16 v[0:3], v[222:225], v[202:205], v[0:3]
	s_setprio 0
	s_add_i32 s67, s67, 2
	s_cmp_gt_u32 s67, 13
	s_mov_b64 s[34:35], s[36:37]
	s_barrier
	s_cbranch_scc0 .LBB0_3168
	v_mov_b32_e32 v159, v140
	s_mov_b64 s[10:11], 0x80000
	v_ashrrev_i32_e32 v158, 2, v159
	v_and_b32_e32 v158, 0xffffffc0, v158
	v_lshl_add_u32 v158, s18, 8, v158
	v_and_or_b32 v158, v159, 15, v158
	v_lshrrev_b32_e32 v159, 1, v159
	v_and_b32_e32 v159, 0x78, v159
	v_lshl_or_b32 v160, s66, 8, v159
	v_ashrrev_i32_e32 v159, 31, v158
	v_ashrrev_i32_e32 v161, 31, v160
	v_lshlrev_b64 v[162:163], 12, v[158:159]
	v_lshl_add_u64 v[162:163], s[2:3], 0, v[162:163]
	v_lshlrev_b64 v[160:161], 1, v[160:161]
	v_lshl_add_u64 v[162:163], v[162:163], 0, v[160:161]
	v_cvt_pk_bf16_f32 v68, v68, v69
	v_cvt_pk_bf16_f32 v69, v70, v71
	v_cvt_pk_bf16_f32 v70, v64, v65
	v_lshl_add_u64 v[64:65], v[162:163], 0, s[10:11]
	s_mov_b32 s10, 0x80000
	v_cvt_pk_bf16_f32 v60, v60, v61
	v_cvt_pk_bf16_f32 v61, v62, v63
	v_cvt_pk_bf16_f32 v62, v56, v57
	v_add_co_u32_e32 v56, vcc, s10, v162
	v_cvt_pk_bf16_f32 v44, v44, v45
	s_nop 0
	v_addc_co_u32_e32 v57, vcc, 0, v163, vcc
	v_cvt_pk_bf16_f32 v45, v46, v47
	v_cvt_pk_bf16_f32 v46, v40, v41
	v_cvt_pk_bf16_f32 v47, v42, v43
	v_cvt_pk_bf16_f32 v112, v112, v113
	v_cvt_pk_bf16_f32 v113, v114, v115
	v_cvt_pk_bf16_f32 v114, v104, v105
	v_or_b32_e32 v104, 16, v158
	global_store_dwordx4 v[64:65], v[44:47], off offset:256
	s_mov_b64 s[10:11], 0x90000
	v_ashrrev_i32_e32 v105, 31, v104
	v_add_co_u32_e32 v46, vcc, s63, v162
	v_cvt_pk_bf16_f32 v96, v96, v97
	v_cvt_pk_bf16_f32 v97, v98, v99
	v_cvt_pk_bf16_f32 v98, v88, v89
	v_or_b32_e32 v88, 32, v158
	v_lshl_add_u64 v[44:45], v[162:163], 0, s[10:11]
	v_addc_co_u32_e32 v47, vcc, 0, v163, vcc
	v_cvt_pk_bf16_f32 v28, v28, v29
	v_cvt_pk_bf16_f32 v29, v30, v31
	v_cvt_pk_bf16_f32 v30, v24, v25
	v_cvt_pk_bf16_f32 v31, v26, v27
	v_lshlrev_b64 v[104:105], 12, v[104:105]
	v_ashrrev_i32_e32 v89, 31, v88
	v_cvt_pk_bf16_f32 v80, v80, v81
	v_cvt_pk_bf16_f32 v81, v82, v83
	v_cvt_pk_bf16_f32 v82, v72, v73
	v_or_b32_e32 v72, 48, v158
	global_store_dwordx4 v[44:45], v[28:31], off offset:256
	v_cvt_pk_bf16_f32 v115, v106, v107
	v_lshl_add_u64 v[104:105], s[2:3], 0, v[104:105]
	v_add_co_u32_e32 v30, vcc, s64, v162
	v_lshlrev_b64 v[88:89], 12, v[88:89]
	v_ashrrev_i32_e32 v73, 31, v72
	v_lshl_add_u64 v[28:29], v[162:163], 0, s[6:7]
	v_addc_co_u32_e32 v31, vcc, 0, v163, vcc
	v_cvt_pk_bf16_f32 v12, v12, v13
	v_cvt_pk_bf16_f32 v13, v14, v15
	v_cvt_pk_bf16_f32 v14, v8, v9
	v_cvt_pk_bf16_f32 v15, v10, v11
	global_store_dwordx4 v[162:163], v[112:115], off offset:256
	v_cvt_pk_bf16_f32 v99, v90, v91
	v_lshl_add_u64 v[88:89], s[2:3], 0, v[88:89]
	v_lshl_add_u64 v[112:113], v[104:105], 0, v[160:161]
	v_lshlrev_b64 v[72:73], 12, v[72:73]
	global_store_dwordx4 v[28:29], v[12:15], off offset:256
	global_store_dwordx4 v[112:113], v[96:99], off offset:256
	v_cvt_pk_bf16_f32 v83, v74, v75
	v_add_co_u32_e32 v14, vcc, s65, v162
	v_lshl_add_u64 v[96:97], v[88:89], 0, v[160:161]
	v_lshl_add_u64 v[72:73], s[2:3], 0, v[72:73]
	v_addc_co_u32_e32 v15, vcc, 0, v163, vcc
	v_cvt_pk_bf16_f32 v124, v124, v125
	v_cvt_pk_bf16_f32 v125, v126, v127
	v_cvt_pk_bf16_f32 v126, v120, v121
	v_cvt_pk_bf16_f32 v127, v122, v123
	v_cvt_pk_bf16_f32 v104, v116, v117
	v_cvt_pk_bf16_f32 v105, v118, v119
	v_cvt_pk_bf16_f32 v106, v108, v109
	v_cvt_pk_bf16_f32 v107, v110, v111
	v_cvt_pk_bf16_f32 v88, v100, v101
	v_cvt_pk_bf16_f32 v89, v102, v103
	v_cvt_pk_bf16_f32 v90, v92, v93
	v_cvt_pk_bf16_f32 v91, v94, v95
	global_store_dwordx4 v[96:97], v[80:83], off offset:256
	v_cvt_pk_bf16_f32 v74, v76, v77
	v_cvt_pk_bf16_f32 v75, v78, v79
	v_lshl_add_u64 v[80:81], v[72:73], 0, v[160:161]
	v_cvt_pk_bf16_f32 v72, v84, v85
	v_cvt_pk_bf16_f32 v73, v86, v87
	v_cvt_pk_bf16_f32 v71, v66, v67
	v_cvt_pk_bf16_f32 v63, v58, v59
	v_cvt_pk_bf16_f32 v40, v52, v53
	v_cvt_pk_bf16_f32 v41, v54, v55
	v_cvt_pk_bf16_f32 v42, v48, v49
	v_cvt_pk_bf16_f32 v43, v50, v51
	v_cvt_pk_bf16_f32 v24, v36, v37
	v_cvt_pk_bf16_f32 v25, v38, v39
	v_cvt_pk_bf16_f32 v26, v32, v33
	v_cvt_pk_bf16_f32 v27, v34, v35
	v_lshl_add_u64 v[12:13], v[162:163], 0, s[16:17]
	v_cvt_pk_bf16_f32 v8, v20, v21
	v_cvt_pk_bf16_f32 v9, v22, v23
	v_cvt_pk_bf16_f32 v10, v16, v17
	v_cvt_pk_bf16_f32 v11, v18, v19
	v_cvt_pk_bf16_f32 v4, v4, v5
	v_cvt_pk_bf16_f32 v5, v6, v7
	v_cvt_pk_bf16_f32 v6, v0, v1
	v_cvt_pk_bf16_f32 v7, v2, v3
	s_and_b64 vcc, exec, s[8:9]
	s_mov_b32 s66, s22
	s_mov_b32 s18, s26
	s_mov_b64 s[20:21], s[30:31]
	s_mov_b64 s[24:25], s[28:29]
	global_store_dwordx4 v[162:163], v[124:127], off
	global_store_dwordx4 v[112:113], v[104:107], off
	global_store_dwordx4 v[96:97], v[88:91], off
	global_store_dwordx4 v[80:81], v[72:75], off
	global_store_dwordx4 v[80:81], v[68:71], off offset:256
	global_store_dwordx4 v[56:57], v[60:63], off
	global_store_dwordx4 v[46:47], v[40:43], off
	global_store_dwordx4 v[30:31], v[24:27], off
	global_store_dwordx4 v[14:15], v[8:11], off
	global_store_dwordx4 v[12:13], v[4:7], off offset:256
	s_cbranch_vccz .LBB0_3165
	s_waitcnt vmcnt(0)
	s_cmpk_gt_u32 s33, 0xff
	v_readlane_b32 s58, v242, 45
	v_readlane_b32 s59, v242, 46
	s_cbranch_scc1 .LBB0_3172
	s_barrier

.LBB0_3428:
	s_or_b64 exec, exec, s[0:1]
	v_readlane_b32 s2, v242, 1
	v_readlane_b32 s3, v242, 2
	s_waitcnt lgkmcnt(0)
	s_barrier
	s_nop 0
	s_mov_b32 s8, 0
	s_load_dwordx2 s[20:21], s[2:3], s8 offset:0x108
	s_add_u32 s0, s2, s8
	s_addc_u32 s1, s3, 0
	s_load_dwordx4 s[4:7], s[2:3], s8 offset:0xb0
	s_load_dwordx2 s[22:23], s[2:3], s8 offset:0xc0
	v_readlane_b32 s2, v242, 57
	s_waitcnt lgkmcnt(0)
	s_add_u32 s18, s20, 0x11fff000
	s_addc_u32 s19, s21, 0
	s_add_u32 s16, s20, 0x1fcff000
	v_readlane_b32 s3, v242, 58
	s_addc_u32 s17, s21, 0
	v_mov_b32_e32 v180, v208
	s_and_b64 vcc, exec, s[2:3]
	s_cbranch_vccnz .LBB0_3430
	v_and_b32_e32 v110, 0x7f, v180
	v_mov_b32_e32 v111, 0
	s_mov_b64 s[2:3], 0
	s_branch .LBB0_3431

.LBB0_3521:
	s_add_u32 s46, s44, 0x100
	ds_read_b128 v[80:83], v163
	ds_read_b128 v[84:87], v164
	ds_read_b128 v[88:91], v171
	ds_read_b128 v[92:95], v172
	s_addc_u32 s47, s45, 0
	s_and_b32 s31, s46, 0x700
	s_add_u32 s33, s40, s31
	s_addc_u32 s35, s41, 0
	s_cmp_eq_u32 s16, 12
	s_cselect_b64 s[50:51], -1, 0
	s_and_b64 s[48:49], s[50:51], exec
	s_cselect_b32 s49, s1, s35
	s_cselect_b32 s48, s3, s33
	s_cselect_b32 s33, 0, 0
	s_cselect_b32 s31, 0, s31
	s_add_u32 s35, s42, s44
	s_addc_u32 s45, s43, s45
	s_add_u32 s44, s35, 0x40080
	s_addc_u32 s45, s45, 0
	ds_read_b128 v[158:161], v179
	ds_read_b128 v[180:183], v179 offset:1024
	ds_read_b128 v[184:187], v179 offset:2048
	ds_read_b128 v[188:191], v179 offset:3072
	ds_read_b128 v[192:195], v179 offset:4096
	ds_read_b128 v[196:199], v179 offset:5120
	ds_read_b128 v[200:203], v179 offset:6144
	ds_read_b128 v[204:207], v179 offset:7168
	s_add_i32 m0, s57, 0xc000
	s_nop 0
	global_load_lds_dwordx4 v144, s[44:45]
	s_add_i32 m0, s57, 0xe000
	s_nop 0
	global_load_lds_dwordx4 v148, s[44:45]
	s_waitcnt lgkmcnt(8)
	s_nop 0
	s_barrier
	s_waitcnt lgkmcnt(0)
	s_setprio 1
	s_waitcnt lgkmcnt(0)
	v_mfma_f32_16x16x32_bf16 v[140:143], v[80:83], v[158:161], v[140:143]
	v_mfma_f32_16x16x32_bf16 v[136:139], v[88:91], v[158:161], v[136:139]
	v_mfma_f32_16x16x32_bf16 v[124:127], v[80:83], v[184:187], v[124:127]
	v_mfma_f32_16x16x32_bf16 v[120:123], v[88:91], v[184:187], v[120:123]
	v_mfma_f32_16x16x32_bf16 v[108:111], v[80:83], v[192:195], v[108:111]
	v_mfma_f32_16x16x32_bf16 v[104:107], v[88:91], v[192:195], v[104:107]
	v_mfma_f32_16x16x32_bf16 v[76:79], v[80:83], v[200:203], v[76:79]
	v_mfma_f32_16x16x32_bf16 v[72:75], v[88:91], v[200:203], v[72:75]
	v_mfma_f32_16x16x32_bf16 v[140:143], v[84:87], v[180:183], v[140:143]
	v_mfma_f32_16x16x32_bf16 v[136:139], v[92:95], v[180:183], v[136:139]
	v_mfma_f32_16x16x32_bf16 v[124:127], v[84:87], v[188:191], v[124:127]
	v_mfma_f32_16x16x32_bf16 v[120:123], v[92:95], v[188:191], v[120:123]
	v_mfma_f32_16x16x32_bf16 v[108:111], v[84:87], v[196:199], v[108:111]
	v_mfma_f32_16x16x32_bf16 v[104:107], v[92:95], v[196:199], v[104:107]
	v_mfma_f32_16x16x32_bf16 v[76:79], v[84:87], v[204:207], v[76:79]
	v_mfma_f32_16x16x32_bf16 v[72:75], v[92:95], v[204:207], v[72:75]
	s_setprio 0
	s_barrier
	s_mov_b64 s[44:45], s[48:49]
	s_mov_b32 m0, s58
	ds_read_b128 v[210:213], v165
	ds_read_b128 v[214:217], v166
	ds_read_b128 v[218:221], v173
	ds_read_b128 v[222:225], v174
	s_nop 0
	global_load_lds_dwordx4 v146, s[44:45]
	s_mov_b32 m0, s59
	s_nop 0
	global_load_lds_dwordx4 v150, s[44:45]
	s_nop 0
	s_barrier
	s_waitcnt lgkmcnt(0)
	s_setprio 1
	s_waitcnt lgkmcnt(0)
	v_mfma_f32_16x16x32_bf16 v[132:135], v[210:213], v[158:161], v[132:135]
	v_mfma_f32_16x16x32_bf16 v[128:131], v[218:221], v[158:161], v[128:131]
	v_mfma_f32_16x16x32_bf16 v[116:119], v[210:213], v[184:187], v[116:119]
	v_mfma_f32_16x16x32_bf16 v[112:115], v[218:221], v[184:187], v[112:115]
	v_mfma_f32_16x16x32_bf16 v[100:103], v[210:213], v[192:195], v[100:103]
	v_mfma_f32_16x16x32_bf16 v[96:99], v[218:221], v[192:195], v[96:99]
	v_mfma_f32_16x16x32_bf16 v[68:71], v[210:213], v[200:203], v[68:71]
	v_mfma_f32_16x16x32_bf16 v[64:67], v[218:221], v[200:203], v[64:67]
	v_mfma_f32_16x16x32_bf16 v[132:135], v[214:217], v[180:183], v[132:135]
	v_mfma_f32_16x16x32_bf16 v[128:131], v[222:225], v[180:183], v[128:131]
	v_mfma_f32_16x16x32_bf16 v[116:119], v[214:217], v[188:191], v[116:119]
	v_mfma_f32_16x16x32_bf16 v[112:115], v[222:225], v[188:191], v[112:115]
	v_mfma_f32_16x16x32_bf16 v[100:103], v[214:217], v[196:199], v[100:103]
	v_mfma_f32_16x16x32_bf16 v[96:99], v[222:225], v[196:199], v[96:99]
	v_mfma_f32_16x16x32_bf16 v[68:71], v[214:217], v[204:207], v[68:71]
	v_mfma_f32_16x16x32_bf16 v[64:67], v[222:225], v[204:207], v[64:67]
	s_setprio 0
	s_and_b64 s[44:45], s[6:7], s[50:51]
	s_and_b64 s[44:45], s[44:45], exec
	s_cselect_b32 s44, s36, s42
	s_cselect_b32 s35, s37, s43
	s_add_u32 s44, s44, s31
	s_addc_u32 s45, s35, s33
	s_mov_b64 s[50:51], s[44:45]
	s_mov_b32 m0, s57
	s_barrier
	ds_read_b128 v[158:161], v179 offset:16384
	ds_read_b128 v[180:183], v179 offset:17408
	ds_read_b128 v[184:187], v179 offset:18432
	ds_read_b128 v[188:191], v179 offset:19456
	ds_read_b128 v[192:195], v179 offset:20480
	ds_read_b128 v[196:199], v179 offset:21504
	ds_read_b128 v[200:203], v179 offset:22528
	ds_read_b128 v[204:207], v179 offset:23552
	s_nop 0
	global_load_lds_dwordx4 v144, s[50:51]
	s_mov_b32 m0, s60
	s_nop 0
	global_load_lds_dwordx4 v148, s[50:51]
	s_nop 0
	s_barrier
	s_waitcnt lgkmcnt(0)
	s_setprio 1
	s_waitcnt lgkmcnt(0)
	v_mfma_f32_16x16x32_bf16 v[60:63], v[80:83], v[158:161], v[60:63]
	v_mfma_f32_16x16x32_bf16 v[56:59], v[88:91], v[158:161], v[56:59]
	v_mfma_f32_16x16x32_bf16 v[44:47], v[80:83], v[184:187], v[44:47]
	v_mfma_f32_16x16x32_bf16 v[40:43], v[88:91], v[184:187], v[40:43]
	v_mfma_f32_16x16x32_bf16 v[28:31], v[80:83], v[192:195], v[28:31]
	v_mfma_f32_16x16x32_bf16 v[24:27], v[88:91], v[192:195], v[24:27]
	v_mfma_f32_16x16x32_bf16 v[12:15], v[80:83], v[200:203], v[12:15]
	v_mfma_f32_16x16x32_bf16 v[8:11], v[88:91], v[200:203], v[8:11]
	v_mfma_f32_16x16x32_bf16 v[60:63], v[84:87], v[180:183], v[60:63]
	v_mfma_f32_16x16x32_bf16 v[56:59], v[92:95], v[180:183], v[56:59]
	v_mfma_f32_16x16x32_bf16 v[44:47], v[84:87], v[188:191], v[44:47]
	v_mfma_f32_16x16x32_bf16 v[40:43], v[92:95], v[188:191], v[40:43]
	v_mfma_f32_16x16x32_bf16 v[28:31], v[84:87], v[196:199], v[28:31]
	v_mfma_f32_16x16x32_bf16 v[24:27], v[92:95], v[196:199], v[24:27]
	v_mfma_f32_16x16x32_bf16 v[12:15], v[84:87], v[204:207], v[12:15]
	v_mfma_f32_16x16x32_bf16 v[8:11], v[92:95], v[204:207], v[8:11]
	s_setprio 0
	s_barrier
	s_add_u32 s50, s48, 0x40000
	s_addc_u32 s51, s49, 0
	s_mov_b32 m0, s61
	s_nop 0
	global_load_lds_dwordx4 v146, s[50:51]
	s_mov_b32 m0, s62
	s_nop 0
	global_load_lds_dwordx4 v150, s[50:51]
	s_waitcnt vmcnt(6)
	s_barrier
	s_setprio 1
	v_mfma_f32_16x16x32_bf16 v[52:55], v[210:213], v[158:161], v[52:55]
	v_mfma_f32_16x16x32_bf16 v[48:51], v[218:221], v[158:161], v[48:51]
	v_mfma_f32_16x16x32_bf16 v[36:39], v[210:213], v[184:187], v[36:39]
	v_mfma_f32_16x16x32_bf16 v[32:35], v[218:221], v[184:187], v[32:35]
	v_mfma_f32_16x16x32_bf16 v[20:23], v[210:213], v[192:195], v[20:23]
	v_mfma_f32_16x16x32_bf16 v[16:19], v[218:221], v[192:195], v[16:19]
	v_mfma_f32_16x16x32_bf16 v[4:7], v[210:213], v[200:203], v[4:7]
	v_mfma_f32_16x16x32_bf16 v[0:3], v[218:221], v[200:203], v[0:3]
	v_mfma_f32_16x16x32_bf16 v[52:55], v[214:217], v[180:183], v[52:55]
	v_mfma_f32_16x16x32_bf16 v[48:51], v[222:225], v[180:183], v[48:51]
	v_mfma_f32_16x16x32_bf16 v[36:39], v[214:217], v[188:191], v[36:39]
	v_mfma_f32_16x16x32_bf16 v[32:35], v[222:225], v[188:191], v[32:35]
	v_mfma_f32_16x16x32_bf16 v[20:23], v[214:217], v[196:199], v[20:23]
	v_mfma_f32_16x16x32_bf16 v[16:19], v[222:225], v[196:199], v[16:19]
	v_mfma_f32_16x16x32_bf16 v[4:7], v[214:217], v[204:207], v[4:7]
	v_mfma_f32_16x16x32_bf16 v[0:3], v[222:225], v[204:207], v[0:3]
	s_setprio 0
	s_barrier
	ds_read_b128 v[80:83], v167
	ds_read_b128 v[84:87], v168
	ds_read_b128 v[88:91], v175
	ds_read_b128 v[92:95], v176
	s_add_u32 s50, s44, 0x40000
	s_addc_u32 s51, s45, 0
	s_mov_b32 m0, s63
	ds_read_b128 v[158:161], v179 offset:32768
	ds_read_b128 v[180:183], v179 offset:33792
	ds_read_b128 v[184:187], v179 offset:34816
	ds_read_b128 v[188:191], v179 offset:35840
	ds_read_b128 v[192:195], v179 offset:36864
	ds_read_b128 v[196:199], v179 offset:37888
	ds_read_b128 v[200:203], v179 offset:38912
	ds_read_b128 v[204:207], v179 offset:39936
	s_nop 0
	global_load_lds_dwordx4 v144, s[50:51]
	s_mov_b32 m0, s64
	s_nop 0
	global_load_lds_dwordx4 v148, s[50:51]
	s_waitcnt lgkmcnt(8)
	s_barrier
	s_waitcnt lgkmcnt(0)
	s_setprio 1
	s_waitcnt lgkmcnt(0)
	v_mfma_f32_16x16x32_bf16 v[140:143], v[80:83], v[158:161], v[140:143]
	v_mfma_f32_16x16x32_bf16 v[136:139], v[88:91], v[158:161], v[136:139]
	v_mfma_f32_16x16x32_bf16 v[124:127], v[80:83], v[184:187], v[124:127]
	v_mfma_f32_16x16x32_bf16 v[120:123], v[88:91], v[184:187], v[120:123]
	v_mfma_f32_16x16x32_bf16 v[108:111], v[80:83], v[192:195], v[108:111]
	v_mfma_f32_16x16x32_bf16 v[104:107], v[88:91], v[192:195], v[104:107]
	v_mfma_f32_16x16x32_bf16 v[76:79], v[80:83], v[200:203], v[76:79]
	v_mfma_f32_16x16x32_bf16 v[72:75], v[88:91], v[200:203], v[72:75]
	v_mfma_f32_16x16x32_bf16 v[140:143], v[84:87], v[180:183], v[140:143]
	v_mfma_f32_16x16x32_bf16 v[136:139], v[92:95], v[180:183], v[136:139]
	v_mfma_f32_16x16x32_bf16 v[124:127], v[84:87], v[188:191], v[124:127]
	v_mfma_f32_16x16x32_bf16 v[120:123], v[92:95], v[188:191], v[120:123]
	v_mfma_f32_16x16x32_bf16 v[108:111], v[84:87], v[196:199], v[108:111]
	v_mfma_f32_16x16x32_bf16 v[104:107], v[92:95], v[196:199], v[104:107]
	v_mfma_f32_16x16x32_bf16 v[76:79], v[84:87], v[204:207], v[76:79]
	v_mfma_f32_16x16x32_bf16 v[72:75], v[92:95], v[204:207], v[72:75]
	s_setprio 0
	s_barrier
	s_add_u32 s50, s48, 0x80
	s_addc_u32 s51, s49, 0
	s_mov_b32 m0, s67
	ds_read_b128 v[210:213], v169
	ds_read_b128 v[214:217], v170
	ds_read_b128 v[218:221], v177
	ds_read_b128 v[222:225], v178
	s_nop 0
	global_load_lds_dwordx4 v146, s[50:51]
	s_mov_b32 m0, s68
	s_nop 0
	global_load_lds_dwordx4 v150, s[50:51]
	s_nop 0
	s_barrier
	s_waitcnt lgkmcnt(0)
	s_setprio 1
	s_waitcnt lgkmcnt(0)
	v_mfma_f32_16x16x32_bf16 v[132:135], v[210:213], v[158:161], v[132:135]
	v_mfma_f32_16x16x32_bf16 v[128:131], v[218:221], v[158:161], v[128:131]
	v_mfma_f32_16x16x32_bf16 v[116:119], v[210:213], v[184:187], v[116:119]
	v_mfma_f32_16x16x32_bf16 v[112:115], v[218:221], v[184:187], v[112:115]
	v_mfma_f32_16x16x32_bf16 v[100:103], v[210:213], v[192:195], v[100:103]
	v_mfma_f32_16x16x32_bf16 v[96:99], v[218:221], v[192:195], v[96:99]
	v_mfma_f32_16x16x32_bf16 v[68:71], v[210:213], v[200:203], v[68:71]
	v_mfma_f32_16x16x32_bf16 v[64:67], v[218:221], v[200:203], v[64:67]
	v_mfma_f32_16x16x32_bf16 v[132:135], v[214:217], v[180:183], v[132:135]
	v_mfma_f32_16x16x32_bf16 v[128:131], v[222:225], v[180:183], v[128:131]
	v_mfma_f32_16x16x32_bf16 v[116:119], v[214:217], v[188:191], v[116:119]
	v_mfma_f32_16x16x32_bf16 v[112:115], v[222:225], v[188:191], v[112:115]
	v_mfma_f32_16x16x32_bf16 v[100:103], v[214:217], v[196:199], v[100:103]
	v_mfma_f32_16x16x32_bf16 v[96:99], v[222:225], v[196:199], v[96:99]
	v_mfma_f32_16x16x32_bf16 v[68:71], v[214:217], v[204:207], v[68:71]
	v_mfma_f32_16x16x32_bf16 v[64:67], v[222:225], v[204:207], v[64:67]
	s_setprio 0
	s_add_u32 s44, s44, 0x80
	s_addc_u32 s45, s45, 0
	s_mov_b32 m0, s69
	s_barrier
	ds_read_b128 v[158:161], v179 offset:49152
	ds_read_b128 v[180:183], v179 offset:50176
	ds_read_b128 v[184:187], v179 offset:51200
	ds_read_b128 v[188:191], v179 offset:52224
	ds_read_b128 v[192:195], v179 offset:53248
	ds_read_b128 v[196:199], v179 offset:54272
	ds_read_b128 v[200:203], v179 offset:55296
	ds_read_b128 v[204:207], v179 offset:56320
	s_nop 0
	global_load_lds_dwordx4 v144, s[44:45]
	s_mov_b32 m0, s70
	s_nop 0
	global_load_lds_dwordx4 v148, s[44:45]
	s_nop 0
	s_barrier
	s_waitcnt lgkmcnt(0)
	s_setprio 1
	s_waitcnt lgkmcnt(0)
	v_mfma_f32_16x16x32_bf16 v[60:63], v[80:83], v[158:161], v[60:63]
	v_mfma_f32_16x16x32_bf16 v[56:59], v[88:91], v[158:161], v[56:59]
	v_mfma_f32_16x16x32_bf16 v[44:47], v[80:83], v[184:187], v[44:47]
	v_mfma_f32_16x16x32_bf16 v[40:43], v[88:91], v[184:187], v[40:43]
	v_mfma_f32_16x16x32_bf16 v[28:31], v[80:83], v[192:195], v[28:31]
	v_mfma_f32_16x16x32_bf16 v[24:27], v[88:91], v[192:195], v[24:27]
	v_mfma_f32_16x16x32_bf16 v[12:15], v[80:83], v[200:203], v[12:15]
	v_mfma_f32_16x16x32_bf16 v[8:11], v[88:91], v[200:203], v[8:11]
	v_mfma_f32_16x16x32_bf16 v[60:63], v[84:87], v[180:183], v[60:63]
	v_mfma_f32_16x16x32_bf16 v[56:59], v[92:95], v[180:183], v[56:59]
	v_mfma_f32_16x16x32_bf16 v[44:47], v[84:87], v[188:191], v[44:47]
	v_mfma_f32_16x16x32_bf16 v[40:43], v[92:95], v[188:191], v[40:43]
	v_mfma_f32_16x16x32_bf16 v[28:31], v[84:87], v[196:199], v[28:31]
	v_mfma_f32_16x16x32_bf16 v[24:27], v[92:95], v[196:199], v[24:27]
	v_mfma_f32_16x16x32_bf16 v[12:15], v[84:87], v[204:207], v[12:15]
	v_mfma_f32_16x16x32_bf16 v[8:11], v[92:95], v[204:207], v[8:11]
	s_setprio 0
	s_barrier
	s_add_u32 s44, s48, 0x40080
	s_addc_u32 s45, s49, 0
	s_mov_b32 m0, s71
	s_nop 0
	global_load_lds_dwordx4 v146, s[44:45]
	s_mov_b32 m0, s72
	s_nop 0
	global_load_lds_dwordx4 v150, s[44:45]
	s_waitcnt vmcnt(6)
	s_barrier
	s_setprio 1
	v_mfma_f32_16x16x32_bf16 v[52:55], v[210:213], v[158:161], v[52:55]
	v_mfma_f32_16x16x32_bf16 v[48:51], v[218:221], v[158:161], v[48:51]
	v_mfma_f32_16x16x32_bf16 v[36:39], v[210:213], v[184:187], v[36:39]
	v_mfma_f32_16x16x32_bf16 v[32:35], v[218:221], v[184:187], v[32:35]
	v_mfma_f32_16x16x32_bf16 v[20:23], v[210:213], v[192:195], v[20:23]
	v_mfma_f32_16x16x32_bf16 v[16:19], v[218:221], v[192:195], v[16:19]
	v_mfma_f32_16x16x32_bf16 v[4:7], v[210:213], v[200:203], v[4:7]
	v_mfma_f32_16x16x32_bf16 v[0:3], v[218:221], v[200:203], v[0:3]
	v_mfma_f32_16x16x32_bf16 v[52:55], v[214:217], v[180:183], v[52:55]
	v_mfma_f32_16x16x32_bf16 v[48:51], v[222:225], v[180:183], v[48:51]
	v_mfma_f32_16x16x32_bf16 v[36:39], v[214:217], v[188:191], v[36:39]
	v_mfma_f32_16x16x32_bf16 v[32:35], v[222:225], v[188:191], v[32:35]
	v_mfma_f32_16x16x32_bf16 v[20:23], v[214:217], v[196:199], v[20:23]
	v_mfma_f32_16x16x32_bf16 v[16:19], v[222:225], v[196:199], v[16:19]
	v_mfma_f32_16x16x32_bf16 v[4:7], v[214:217], v[204:207], v[4:7]
	v_mfma_f32_16x16x32_bf16 v[0:3], v[222:225], v[204:207], v[0:3]
	s_setprio 0
	s_add_i32 s16, s16, 2
	s_cmp_gt_u32 s16, 13
	s_mov_b64 s[44:45], s[46:47]
	s_barrier
	s_cbranch_scc0 .LBB0_3521
	v_mov_b32_e32 v80, v162
	s_cmpk_gt_i32 s2, 0x7f
	s_mov_b64 s[6:7], 0xc000
	s_cbranch_scc1 .LBB0_3524
	s_ashr_i32 s1, s2, 31
	s_lshr_b32 s1, s1, 28
	s_add_i32 s1, s2, s1
	s_ashr_i32 s1, s1, 4
	s_mul_hi_i32 s7, s1, 0x1800
	s_mul_i32 s6, s1, 0x1800

.LBB0_3715:
	s_or_b64 exec, exec, s[0:1]
	v_readlane_b32 s2, v242, 1
	s_waitcnt lgkmcnt(0)
	s_barrier
	s_nop 0
	s_mov_b32 s0, 0
	v_readlane_b32 s3, v242, 2
	s_load_dwordx4 s[88:91], s[2:3], s0 offset:0xe8
	s_load_dwordx2 s[92:93], s[2:3], s0 offset:0xf8
	s_load_dwordx2 s[12:13], s[2:3], s0 offset:0x108
	v_readlane_b32 s0, v242, 4
	s_waitcnt vmcnt(7)
	v_mov_b32_e32 v5, v208
	v_readlane_b32 s1, v242, 5
	s_andn2_b64 vcc, exec, s[0:1]
	s_waitcnt vmcnt(5)
	v_and_b32_e32 v12, 63, v5
	v_ashrrev_i32_e32 v4, 6, v5
	v_lshlrev_b32_e32 v6, 3, v5
	s_cbranch_vccnz .LBB0_3822
	s_waitcnt lgkmcnt(0)
	s_add_u32 s0, s12, 0x907000
	v_writelane_b32 v242, s0, 29
	s_addc_u32 s0, s13, 0
	s_add_u32 s2, s12, 0xd47000
	s_addc_u32 s3, s13, 0
	v_lshlrev_b32_e32 v13, 2, v5
	s_add_u32 s94, s12, 0xd8b000
	s_waitcnt vmcnt(2)
	v_or_b32_e32 v17, 3, v13
	s_addc_u32 s95, s13, 0
	v_lshlrev_b32_e32 v0, 2, v17
	v_writelane_b32 v242, s0, 31
	s_add_u32 s0, s12, 0xdcf000
	v_sub_u32_e32 v18, 0, v0
	v_add_u32_e32 v0, 0xfc, v13
	v_writelane_b32 v242, s0, 34
	v_and_b32_e32 v19, 0xfc, v0
	v_add_u32_e32 v0, 0xf8, v13
	v_writelane_b32 v242, s12, 49
	v_and_b32_e32 v20, 0xfc, v0
	v_add_u32_e32 v0, 0xf0, v13
	v_writelane_b32 v242, s13, 50
	s_addc_u32 s0, s13, 0
	v_and_b32_e32 v21, 0xfc, v0
	v_add_u32_e32 v0, 0xe0, v13
	v_writelane_b32 v242, s0, 21
	s_movk_i32 s0, 0x100
	v_and_b32_e32 v22, 0xfc, v0
	v_add_u32_e32 v0, 0xc0, v13
	v_cmp_gt_i32_e32 vcc, s0, v5
	v_and_b32_e32 v23, 0xfc, v0
	s_movk_i32 s0, 0x80
	v_bfrev_b32_e32 v0, 0.5
	s_waitcnt vmcnt(0)
	v_bitop3_b32 v25, v13, s0, v0 bitop3:0x6c
	v_cmp_eq_u32_e64 s[0:1], 63, v12
	v_or_b32_e32 v1, 1, v6
	v_lshl_add_u32 v0, v4, 2, 0
	v_writelane_b32 v242, s0, 41
	v_cmp_gt_u32_e64 s[4:5], 64, v5
	v_add_u32_e32 v14, 0, v13
	v_writelane_b32 v242, s1, 42
	v_cmp_lt_i32_e64 s[0:1], 0, v4
	v_not_b32_e32 v15, v13
	v_or_b32_e32 v16, 2, v13
	v_writelane_b32 v242, s0, 43
	v_cmp_eq_u32_e64 s[6:7], 0, v12
	v_cmp_gt_u32_e64 s[8:9], 2, v12
	v_writelane_b32 v242, s1, 44
	v_cmp_lt_i32_e64 s[0:1], 1, v4
	v_cmp_gt_u32_e64 s[10:11], 4, v12
	v_cmp_gt_u32_e64 s[12:13], 8, v12
	v_writelane_b32 v242, s0, 47
	v_cmp_gt_u32_e64 s[14:15], 16, v12
	v_xor_b32_e32 v24, 0x80, v13
	v_writelane_b32 v242, s1, 48
	s_movk_i32 s0, 0x200
	v_cmp_gt_i32_e64 s[38:39], s0, v5
	s_movk_i32 s0, 0x1000
	v_cmp_gt_i32_e64 s[40:41], s0, v1
	v_or_b32_e32 v1, 2, v6
	v_cmp_gt_i32_e64 s[42:43], s0, v1
	v_or_b32_e32 v1, 3, v6
	v_cmp_gt_i32_e64 s[44:45], s0, v1
	v_or_b32_e32 v1, 4, v6
	v_cmp_gt_i32_e64 s[46:47], s0, v1
	v_or_b32_e32 v1, 5, v6
	v_cmp_gt_i32_e64 s[48:49], s0, v1
	v_or_b32_e32 v1, 6, v6
	v_cmp_gt_i32_e64 s[50:51], s0, v1
	v_or_b32_e32 v1, 7, v6
	v_cmp_gt_u32_e64 s[16:17], 32, v12
	v_cmp_lt_i32_e64 s[24:25], 2, v4
	v_cmp_lt_i32_e64 s[26:27], 3, v4
	v_cmp_lt_i32_e64 s[28:29], 4, v4
	v_cmp_lt_i32_e64 s[30:31], 5, v4
	v_cmp_lt_i32_e64 s[34:35], 6, v4
	v_cmp_lt_i32_e64 s[36:37], 7, v4
	v_ashrrev_i32_e32 v7, 31, v6
	v_cmp_gt_i32_e64 s[52:53], s0, v1
	v_mov_b32_e32 v26, 0
	v_mov_b32_e32 v27, 1
	v_add_u32_e32 v28, 0x400, v0
	v_readlane_b32 s33, v242, 0
	s_branch .LBB0_3719

.LBB0_3899:
	s_or_b64 exec, exec, s[0:1]
	v_readlane_b32 s2, v242, 1
	v_readlane_b32 s3, v242, 2
	s_waitcnt lgkmcnt(0)
	s_barrier
	s_nop 0
	s_mov_b32 s0, 0
	s_load_dwordx2 s[8:9], s[2:3], s0 offset:0x108
	v_mov_b32_e32 v209, v208
	s_nop 0
	v_ashrrev_i32_e32 v0, 8, v209
	v_cmp_gt_i32_e32 vcc, 10, v0
	s_and_saveexec_b64 s[0:1], vcc
	s_cbranch_execz .LBB0_3906
	v_readlane_b32 s4, v242, 11
	v_readlane_b32 s5, v242, 12
	v_and_b32_e32 v2, 0xff, v209
	s_waitcnt lgkmcnt(0)
	s_add_u32 s2, s8, 0xd8b000
	v_readlane_b32 s5, v242, 0
	v_lshlrev_b32_e32 v1, 2, v2
	s_addc_u32 s3, s9, 0
	s_mov_b32 s6, s4
	s_ashr_i32 s7, s4, 31
	s_ashr_i32 s4, s5, 31
	v_lshl_or_b32 v1, v0, 10, v1
	v_mov_b32_e32 v6, s5
	v_mov_b32_e32 v7, s4
	v_add_u32_e32 v1, 0, v1
	v_add_u32_e32 v3, 0x20010, v1
	v_add_u32_e32 v4, -2, v0
	v_mad_i64_i32 v[0:1], s[4:5], s6, v0, v[6:7]
	s_mov_b32 s4, s6
	s_nop 0
	v_writelane_b32 v242, s4, 11
	s_mov_b64 s[10:11], 0x800
	v_mov_b32_e32 v5, 9
	v_writelane_b32 v242, s5, 12
	s_lshl_b64 s[4:5], s[6:7], 1
	s_mov_b64 s[6:7], 0
	v_mov_b32_e32 v6, 6
	v_mov_b32_e32 v7, 3
	s_waitcnt vmcnt(4)
	v_mov_b32_e32 v8, 12
	s_branch .LBB0_3902
